# baseline (speedup 1.0000x reference)
.LBB8_27:
	ds_read_b128 v[72:75], v231
	ds_read_b128 v[80:83], v231 offset:1024
	ds_read_b128 v[88:91], v231 offset:2048
	ds_read_b128 v[92:95], v231 offset:3072
	s_add_u32 s40, s38, 0xfffd0080
	s_addc_u32 s41, s39, -1
	s_cmp_eq_u32 s87, 8
	s_cselect_b32 s43, s9, s41
	s_cselect_b32 s42, s8, s40
	s_cselect_b32 s41, s1, s86
	s_cselect_b32 s40, s0, s85
	v_lshl_add_u64 v[190:191], s[38:39], 0, v[184:185]
	s_add_i32 m0, s51, 0xc000
	ds_read_b128 v[136:139], v232
	ds_read_b128 v[148:151], v232 offset:1024
	ds_read_b128 v[152:155], v232 offset:2048
	ds_read_b128 v[156:159], v232 offset:3072
	ds_read_b128 v[160:163], v232 offset:4096
	ds_read_b128 v[164:167], v232 offset:5120
	ds_read_b128 v[168:171], v232 offset:6144
	ds_read_b128 v[172:175], v232 offset:7168
	global_load_lds_dwordx4 v[190:191], off
	v_lshl_add_u64 v[190:191], s[38:39], 0, v[186:187]
	s_add_i32 m0, s51, 0xe000
	s_nop 0
	global_load_lds_dwordx4 v[190:191], off
	s_waitcnt lgkmcnt(8)
	s_barrier
	s_waitcnt lgkmcnt(0)
	s_setprio 1
	s_waitcnt lgkmcnt(0)
	v_mfma_f32_16x16x32_f16 v[144:147], v[72:75], v[136:139], v[144:147]
	v_mfma_f32_16x16x32_f16 v[140:143], v[88:91], v[136:139], v[140:143]
	v_mfma_f32_16x16x32_f16 v[124:127], v[72:75], v[152:155], v[124:127]
	v_mfma_f32_16x16x32_f16 v[120:123], v[88:91], v[152:155], v[120:123]
	v_mfma_f32_16x16x32_f16 v[108:111], v[72:75], v[160:163], v[108:111]
	v_mfma_f32_16x16x32_f16 v[104:107], v[88:91], v[160:163], v[104:107]
	v_mfma_f32_16x16x32_f16 v[84:87], v[72:75], v[168:171], v[84:87]
	v_mfma_f32_16x16x32_f16 v[76:79], v[88:91], v[168:171], v[76:79]
	v_mfma_f32_16x16x32_f16 v[144:147], v[80:83], v[148:151], v[144:147]
	v_mfma_f32_16x16x32_f16 v[140:143], v[92:95], v[148:151], v[140:143]
	v_mfma_f32_16x16x32_f16 v[124:127], v[80:83], v[156:159], v[124:127]
	v_mfma_f32_16x16x32_f16 v[120:123], v[92:95], v[156:159], v[120:123]
	v_mfma_f32_16x16x32_f16 v[108:111], v[80:83], v[164:167], v[108:111]
	v_mfma_f32_16x16x32_f16 v[104:107], v[92:95], v[164:167], v[104:107]
	v_mfma_f32_16x16x32_f16 v[84:87], v[80:83], v[172:175], v[84:87]
	v_mfma_f32_16x16x32_f16 v[76:79], v[92:95], v[172:175], v[76:79]
	s_setprio 0
	s_barrier
	s_add_i32 s88, s70, s50
	v_lshl_add_u64 v[206:207], s[40:41], 0, v[178:179]
	s_mov_b32 m0, s88
	ds_read_b128 v[190:193], v233
	ds_read_b128 v[194:197], v233 offset:1024
	ds_read_b128 v[198:201], v233 offset:2048
	ds_read_b128 v[202:205], v233 offset:3072
	global_load_lds_dwordx4 v[206:207], off
	v_lshl_add_u64 v[208:209], s[40:41], 0, v[182:183]
	s_add_i32 m0, s88, 0x2000
	s_nop 0
	global_load_lds_dwordx4 v[208:209], off
	s_barrier
	s_waitcnt lgkmcnt(0)
	s_setprio 1
	s_waitcnt lgkmcnt(0)
	v_mfma_f32_16x16x32_f16 v[132:135], v[190:193], v[136:139], v[132:135]
	v_mfma_f32_16x16x32_f16 v[128:131], v[198:201], v[136:139], v[128:131]
	v_mfma_f32_16x16x32_f16 v[116:119], v[190:193], v[152:155], v[116:119]
	v_mfma_f32_16x16x32_f16 v[112:115], v[198:201], v[152:155], v[112:115]
	v_mfma_f32_16x16x32_f16 v[100:103], v[190:193], v[160:163], v[100:103]
	v_mfma_f32_16x16x32_f16 v[96:99], v[198:201], v[160:163], v[96:99]
	v_mfma_f32_16x16x32_f16 v[68:71], v[190:193], v[168:171], v[68:71]
	v_mfma_f32_16x16x32_f16 v[64:67], v[198:201], v[168:171], v[64:67]
	v_mfma_f32_16x16x32_f16 v[132:135], v[194:197], v[148:151], v[132:135]
	v_mfma_f32_16x16x32_f16 v[128:131], v[202:205], v[148:151], v[128:131]
	v_mfma_f32_16x16x32_f16 v[116:119], v[194:197], v[156:159], v[116:119]
	v_mfma_f32_16x16x32_f16 v[112:115], v[202:205], v[156:159], v[112:115]
	v_mfma_f32_16x16x32_f16 v[100:103], v[194:197], v[164:167], v[100:103]
	v_mfma_f32_16x16x32_f16 v[96:99], v[202:205], v[164:167], v[96:99]
	v_mfma_f32_16x16x32_f16 v[68:71], v[194:197], v[172:175], v[68:71]
	v_mfma_f32_16x16x32_f16 v[64:67], v[202:205], v[172:175], v[64:67]
	s_setprio 0
	s_mov_b32 m0, s51
	v_lshl_add_u64 v[210:211], s[42:43], 0, v[176:177]
	s_barrier
	ds_read_b128 v[136:139], v232 offset:16384
	ds_read_b128 v[148:151], v232 offset:17408
	ds_read_b128 v[152:155], v232 offset:18432
	ds_read_b128 v[156:159], v232 offset:19456
	ds_read_b128 v[160:163], v232 offset:20480
	ds_read_b128 v[164:167], v232 offset:21504
	ds_read_b128 v[168:171], v232 offset:22528
	ds_read_b128 v[172:175], v232 offset:23552
	global_load_lds_dwordx4 v[210:211], off
	v_lshl_add_u64 v[212:213], s[42:43], 0, v[180:181]
	s_mov_b32 m0, s52
	s_nop 0
	global_load_lds_dwordx4 v[212:213], off
	s_barrier
	s_waitcnt lgkmcnt(0)
	s_setprio 1
	s_waitcnt lgkmcnt(0)
	v_mfma_f32_16x16x32_f16 v[60:63], v[72:75], v[136:139], v[60:63]
	v_mfma_f32_16x16x32_f16 v[56:59], v[88:91], v[136:139], v[56:59]
	v_mfma_f32_16x16x32_f16 v[44:47], v[72:75], v[152:155], v[44:47]
	v_mfma_f32_16x16x32_f16 v[40:43], v[88:91], v[152:155], v[40:43]
	v_mfma_f32_16x16x32_f16 v[28:31], v[72:75], v[160:163], v[28:31]
	v_mfma_f32_16x16x32_f16 v[24:27], v[88:91], v[160:163], v[24:27]
	v_mfma_f32_16x16x32_f16 v[12:15], v[72:75], v[168:171], v[12:15]
	v_mfma_f32_16x16x32_f16 v[8:11], v[88:91], v[168:171], v[8:11]
	v_mfma_f32_16x16x32_f16 v[60:63], v[80:83], v[148:151], v[60:63]
	v_mfma_f32_16x16x32_f16 v[56:59], v[92:95], v[148:151], v[56:59]
	v_mfma_f32_16x16x32_f16 v[44:47], v[80:83], v[156:159], v[44:47]
	v_mfma_f32_16x16x32_f16 v[40:43], v[92:95], v[156:159], v[40:43]
	v_mfma_f32_16x16x32_f16 v[28:31], v[80:83], v[164:167], v[28:31]
	v_mfma_f32_16x16x32_f16 v[24:27], v[92:95], v[164:167], v[24:27]
	v_mfma_f32_16x16x32_f16 v[12:15], v[80:83], v[172:175], v[12:15]
	v_mfma_f32_16x16x32_f16 v[8:11], v[92:95], v[172:175], v[8:11]
	s_setprio 0
	s_barrier
	s_add_u32 s88, s40, 0xc000
	s_addc_u32 s89, s41, 0
	s_add_i32 s90, s71, s50
	v_lshl_add_u64 v[72:73], s[88:89], 0, v[178:179]
	s_mov_b32 m0, s90
	s_nop 0
	global_load_lds_dwordx4 v[72:73], off
	v_lshl_add_u64 v[72:73], s[88:89], 0, v[182:183]
	s_add_i32 m0, s90, 0x2000
	s_nop 0
	global_load_lds_dwordx4 v[72:73], off
	s_waitcnt vmcnt(6)
	s_barrier
	s_setprio 1
	v_mfma_f32_16x16x32_f16 v[52:55], v[190:193], v[136:139], v[52:55]
	v_mfma_f32_16x16x32_f16 v[48:51], v[198:201], v[136:139], v[48:51]
	v_mfma_f32_16x16x32_f16 v[36:39], v[190:193], v[152:155], v[36:39]
	v_mfma_f32_16x16x32_f16 v[32:35], v[198:201], v[152:155], v[32:35]
	v_mfma_f32_16x16x32_f16 v[20:23], v[190:193], v[160:163], v[20:23]
	v_mfma_f32_16x16x32_f16 v[16:19], v[198:201], v[160:163], v[16:19]
	v_mfma_f32_16x16x32_f16 v[4:7], v[190:193], v[168:171], v[4:7]
	v_mfma_f32_16x16x32_f16 v[0:3], v[198:201], v[168:171], v[0:3]
	v_mfma_f32_16x16x32_f16 v[52:55], v[194:197], v[148:151], v[52:55]
	v_mfma_f32_16x16x32_f16 v[48:51], v[202:205], v[148:151], v[48:51]
	v_mfma_f32_16x16x32_f16 v[36:39], v[194:197], v[156:159], v[36:39]
	v_mfma_f32_16x16x32_f16 v[32:35], v[202:205], v[156:159], v[32:35]
	v_mfma_f32_16x16x32_f16 v[20:23], v[194:197], v[164:167], v[20:23]
	v_mfma_f32_16x16x32_f16 v[16:19], v[202:205], v[164:167], v[16:19]
	v_mfma_f32_16x16x32_f16 v[4:7], v[194:197], v[172:175], v[4:7]
	v_mfma_f32_16x16x32_f16 v[0:3], v[202:205], v[172:175], v[0:3]
	s_setprio 0
	s_add_i32 s88, 0, 0x18000
	v_add_u32_e32 v92, s88, v228
	s_barrier
	ds_read_b128 v[72:75], v92
	ds_read_b128 v[80:83], v92 offset:1024
	ds_read_b128 v[88:91], v92 offset:2048
	ds_read_b128 v[92:95], v92 offset:3072
	s_add_u32 s42, s42, 0x30000
	s_addc_u32 s43, s43, 0
	s_mov_b32 m0, s53
	v_lshl_add_u64 v[190:191], s[42:43], 0, v[176:177]
	ds_read_b128 v[136:139], v232 offset:32768
	ds_read_b128 v[148:151], v232 offset:33792
	ds_read_b128 v[152:155], v232 offset:34816
	ds_read_b128 v[156:159], v232 offset:35840
	ds_read_b128 v[160:163], v232 offset:36864
	ds_read_b128 v[164:167], v232 offset:37888
	ds_read_b128 v[168:171], v232 offset:38912
	ds_read_b128 v[172:175], v232 offset:39936
	global_load_lds_dwordx4 v[190:191], off
	v_lshl_add_u64 v[190:191], s[42:43], 0, v[180:181]
	s_mov_b32 m0, s54
	s_nop 0
	global_load_lds_dwordx4 v[190:191], off
	s_waitcnt lgkmcnt(8)
	s_barrier
	s_waitcnt lgkmcnt(0)
	s_setprio 1
	s_waitcnt lgkmcnt(0)
	v_mfma_f32_16x16x32_f16 v[144:147], v[72:75], v[136:139], v[144:147]
	v_mfma_f32_16x16x32_f16 v[140:143], v[88:91], v[136:139], v[140:143]
	v_mfma_f32_16x16x32_f16 v[124:127], v[72:75], v[152:155], v[124:127]
	v_mfma_f32_16x16x32_f16 v[120:123], v[88:91], v[152:155], v[120:123]
	v_mfma_f32_16x16x32_f16 v[108:111], v[72:75], v[160:163], v[108:111]
	v_mfma_f32_16x16x32_f16 v[104:107], v[88:91], v[160:163], v[104:107]
	v_mfma_f32_16x16x32_f16 v[84:87], v[72:75], v[168:171], v[84:87]
	v_mfma_f32_16x16x32_f16 v[76:79], v[88:91], v[168:171], v[76:79]
	v_mfma_f32_16x16x32_f16 v[144:147], v[80:83], v[148:151], v[144:147]
	v_mfma_f32_16x16x32_f16 v[140:143], v[92:95], v[148:151], v[140:143]
	v_mfma_f32_16x16x32_f16 v[124:127], v[80:83], v[156:159], v[124:127]
	v_mfma_f32_16x16x32_f16 v[120:123], v[92:95], v[156:159], v[120:123]
	v_mfma_f32_16x16x32_f16 v[108:111], v[80:83], v[164:167], v[108:111]
	v_mfma_f32_16x16x32_f16 v[104:107], v[92:95], v[164:167], v[104:107]
	v_mfma_f32_16x16x32_f16 v[84:87], v[80:83], v[172:175], v[84:87]
	v_mfma_f32_16x16x32_f16 v[76:79], v[92:95], v[172:175], v[76:79]
	s_setprio 0
	s_barrier
	s_add_i32 s42, 0, 0x1c000
	s_add_i32 s43, s88, s50
	v_add_u32_e32 v202, s42, v228
	v_lshl_add_u64 v[206:207], v[206:207], 0, s[36:37]
	s_mov_b32 m0, s43
	ds_read_b128 v[190:193], v202
	ds_read_b128 v[194:197], v202 offset:1024
	ds_read_b128 v[198:201], v202 offset:2048
	ds_read_b128 v[202:205], v202 offset:3072
	global_load_lds_dwordx4 v[206:207], off
	v_lshl_add_u64 v[206:207], v[208:209], 0, s[36:37]
	s_add_i32 m0, s43, 0x2000
	s_nop 0
	global_load_lds_dwordx4 v[206:207], off
	s_barrier
	s_waitcnt lgkmcnt(0)
	s_setprio 1
	s_waitcnt lgkmcnt(0)
	v_mfma_f32_16x16x32_f16 v[132:135], v[190:193], v[136:139], v[132:135]
	v_mfma_f32_16x16x32_f16 v[128:131], v[198:201], v[136:139], v[128:131]
	v_mfma_f32_16x16x32_f16 v[116:119], v[190:193], v[152:155], v[116:119]
	v_mfma_f32_16x16x32_f16 v[112:115], v[198:201], v[152:155], v[112:115]
	v_mfma_f32_16x16x32_f16 v[100:103], v[190:193], v[160:163], v[100:103]
	v_mfma_f32_16x16x32_f16 v[96:99], v[198:201], v[160:163], v[96:99]
	v_mfma_f32_16x16x32_f16 v[68:71], v[190:193], v[168:171], v[68:71]
	v_mfma_f32_16x16x32_f16 v[64:67], v[198:201], v[168:171], v[64:67]
	v_mfma_f32_16x16x32_f16 v[132:135], v[194:197], v[148:151], v[132:135]
	v_mfma_f32_16x16x32_f16 v[128:131], v[202:205], v[148:151], v[128:131]
	v_mfma_f32_16x16x32_f16 v[116:119], v[194:197], v[156:159], v[116:119]
	v_mfma_f32_16x16x32_f16 v[112:115], v[202:205], v[156:159], v[112:115]
	v_mfma_f32_16x16x32_f16 v[100:103], v[194:197], v[164:167], v[100:103]
	v_mfma_f32_16x16x32_f16 v[96:99], v[202:205], v[164:167], v[96:99]
	v_mfma_f32_16x16x32_f16 v[68:71], v[194:197], v[172:175], v[68:71]
	v_mfma_f32_16x16x32_f16 v[64:67], v[202:205], v[172:175], v[64:67]
	s_setprio 0
	s_mov_b32 m0, s59
	v_lshl_add_u64 v[206:207], v[210:211], 0, s[36:37]
	s_barrier
	ds_read_b128 v[136:139], v232 offset:49152
	ds_read_b128 v[148:151], v232 offset:50176
	ds_read_b128 v[152:155], v232 offset:51200
	ds_read_b128 v[156:159], v232 offset:52224
	ds_read_b128 v[160:163], v232 offset:53248
	ds_read_b128 v[164:167], v232 offset:54272
	ds_read_b128 v[168:171], v232 offset:55296
	ds_read_b128 v[172:175], v232 offset:56320
	global_load_lds_dwordx4 v[206:207], off
	v_lshl_add_u64 v[206:207], v[212:213], 0, s[36:37]
	s_mov_b32 m0, s60
	s_nop 0
	global_load_lds_dwordx4 v[206:207], off
	s_barrier
	s_waitcnt lgkmcnt(0)
	s_setprio 1
	s_waitcnt lgkmcnt(0)
	v_mfma_f32_16x16x32_f16 v[60:63], v[72:75], v[136:139], v[60:63]
	v_mfma_f32_16x16x32_f16 v[56:59], v[88:91], v[136:139], v[56:59]
	v_mfma_f32_16x16x32_f16 v[44:47], v[72:75], v[152:155], v[44:47]
	v_mfma_f32_16x16x32_f16 v[40:43], v[88:91], v[152:155], v[40:43]
	v_mfma_f32_16x16x32_f16 v[28:31], v[72:75], v[160:163], v[28:31]
	v_mfma_f32_16x16x32_f16 v[24:27], v[88:91], v[160:163], v[24:27]
	v_mfma_f32_16x16x32_f16 v[12:15], v[72:75], v[168:171], v[12:15]
	v_mfma_f32_16x16x32_f16 v[8:11], v[88:91], v[168:171], v[8:11]
	v_mfma_f32_16x16x32_f16 v[60:63], v[80:83], v[148:151], v[60:63]
	v_mfma_f32_16x16x32_f16 v[56:59], v[92:95], v[148:151], v[56:59]
	v_mfma_f32_16x16x32_f16 v[44:47], v[80:83], v[156:159], v[44:47]
	v_mfma_f32_16x16x32_f16 v[40:43], v[92:95], v[156:159], v[40:43]
	v_mfma_f32_16x16x32_f16 v[28:31], v[80:83], v[164:167], v[28:31]
	v_mfma_f32_16x16x32_f16 v[24:27], v[92:95], v[164:167], v[24:27]
	v_mfma_f32_16x16x32_f16 v[12:15], v[80:83], v[172:175], v[12:15]
	v_mfma_f32_16x16x32_f16 v[8:11], v[92:95], v[172:175], v[8:11]
	s_setprio 0
	s_barrier
	s_add_u32 s40, s40, 0xc080
	s_addc_u32 s41, s41, 0
	s_add_i32 s42, s42, s50
	v_lshl_add_u64 v[72:73], s[40:41], 0, v[178:179]
	s_mov_b32 m0, s42
	s_nop 0
	global_load_lds_dwordx4 v[72:73], off
	v_lshl_add_u64 v[72:73], s[40:41], 0, v[182:183]
	s_add_i32 m0, s42, 0x2000
	s_nop 0
	global_load_lds_dwordx4 v[72:73], off
	s_waitcnt vmcnt(6)
	s_barrier
	s_setprio 1
	v_mfma_f32_16x16x32_f16 v[52:55], v[190:193], v[136:139], v[52:55]
	v_mfma_f32_16x16x32_f16 v[48:51], v[198:201], v[136:139], v[48:51]
	v_mfma_f32_16x16x32_f16 v[36:39], v[190:193], v[152:155], v[36:39]
	v_mfma_f32_16x16x32_f16 v[32:35], v[198:201], v[152:155], v[32:35]
	v_mfma_f32_16x16x32_f16 v[20:23], v[190:193], v[160:163], v[20:23]
	v_mfma_f32_16x16x32_f16 v[16:19], v[198:201], v[160:163], v[16:19]
	v_mfma_f32_16x16x32_f16 v[4:7], v[190:193], v[168:171], v[4:7]
	v_mfma_f32_16x16x32_f16 v[0:3], v[198:201], v[168:171], v[0:3]
	v_mfma_f32_16x16x32_f16 v[52:55], v[194:197], v[148:151], v[52:55]
	v_mfma_f32_16x16x32_f16 v[48:51], v[202:205], v[148:151], v[48:51]
	v_mfma_f32_16x16x32_f16 v[36:39], v[194:197], v[156:159], v[36:39]
	v_mfma_f32_16x16x32_f16 v[32:35], v[202:205], v[156:159], v[32:35]
	v_mfma_f32_16x16x32_f16 v[20:23], v[194:197], v[164:167], v[20:23]
	v_mfma_f32_16x16x32_f16 v[16:19], v[202:205], v[164:167], v[16:19]
	v_mfma_f32_16x16x32_f16 v[4:7], v[194:197], v[172:175], v[4:7]
	v_mfma_f32_16x16x32_f16 v[0:3], v[202:205], v[172:175], v[0:3]
	s_setprio 0
	s_add_i32 s87, s87, 2
	s_add_u32 s38, s38, 0x100
	s_addc_u32 s39, s39, 0
	s_add_u32 s85, s85, 0x100
	s_addc_u32 s86, s86, 0
	s_cmp_gt_u32 s87, 9
	s_barrier
	s_cbranch_scc0 .LBB8_27
	s_lshl_b32 s92, s84, 8
	s_add_i32 s92, s92, s58
	s_lshl_b32 s93, s83, 8
	s_or_b32 s93, s93, s61
	v_lshlrev_b32_e32 v237, 2, v226
	s_lshl_b32 s96, s93, 2
	s_add_u32 s94, s16, s96
	s_addc_u32 s95, s17, 0
	global_load_dwordx4 v[72:75], v237, s[94:95] offset:0
	global_load_dwordx4 v[80:83], v237, s[94:95] offset:16
	global_load_dwordx4 v[88:91], v237, s[94:95] offset:128
	global_load_dwordx4 v[92:95], v237, s[94:95] offset:144
	s_add_u32 s94, s18, s96
	s_addc_u32 s95, s19, 0
	global_load_dwordx4 v[136:139], v237, s[94:95] offset:0
	global_load_dwordx4 v[148:151], v237, s[94:95] offset:16
	global_load_dwordx4 v[152:155], v237, s[94:95] offset:128
	global_load_dwordx4 v[156:159], v237, s[94:95] offset:144
	s_add_u32 s94, s14, s96
	s_addc_u32 s95, s15, 0
	global_load_dwordx4 v[160:163], v237, s[94:95] offset:0
	global_load_dwordx4 v[164:167], v237, s[94:95] offset:16
	global_load_dwordx4 v[168:171], v237, s[94:95] offset:128
	global_load_dwordx4 v[172:175], v237, s[94:95] offset:144
	v_lshlrev_b32_e32 v190, 3, v227
	s_lshl_b32 s96, s92, 3
	s_add_u32 s94, s12, s96
	s_addc_u32 s95, s13, 0
	global_load_dwordx2 v[238:239], v190, s[94:95] offset:0
	global_load_dwordx2 v[192:193], v190, s[94:95] offset:128
	global_load_dwordx2 v[194:195], v190, s[94:95] offset:256
	global_load_dwordx2 v[196:197], v190, s[94:95] offset:384
	global_load_dwordx2 v[198:199], v190, s[94:95] offset:1024
	global_load_dwordx2 v[200:201], v190, s[94:95] offset:1152
	global_load_dwordx2 v[202:203], v190, s[94:95] offset:1280
	global_load_dwordx2 v[204:205], v190, s[94:95] offset:1408
	v_mul_u32_u24_e32 v191, 0x600, v227
	v_lshl_add_u32 v191, v226, 1, v191
	s_mul_i32 s96, s92, 0x600
	s_lshl_b32 s97, s93, 1
	s_add_u32 s96, s96, s97
	s_add_u32 s98, s10, s96
	s_addc_u32 s99, s11, 0
	s_add_u32 s94, s98, 0x0
	s_addc_u32 s95, s99, 0
	global_load_dwordx4 v[208:211], v191, s[94:95] offset:0 nt
	global_load_dwordx4 v[212:215], v191, s[94:95] offset:64 nt
	s_add_u32 s94, s98, 0x6000
	s_addc_u32 s95, s99, 0
	global_load_dwordx4 v[216:219], v191, s[94:95] offset:0 nt
	global_load_dwordx4 v[220:223], v191, s[94:95] offset:64 nt
	v_add_u32_e32 v225, s92, v229
	v_mul_u32_u24_e32 v225, 0x600, v225
	s_lshl_b32 s97, s93, 1
	v_add3_u32 v225, v225, v230, s97
	v_mul_u32_u24_e32 v224, 0x60, v227
	s_mul_i32 s96, s92, 0x60
	s_lshl_b32 s97, s83, 5
	s_add_u32 s96, s96, s97
	s_lshr_b32 s97, s61, 3
	s_add_u32 s96, s96, s97
	s_add_u32 s96, s96, 0x800
	s_add_u32 s100, s28, s96
	s_addc_u32 s101, s29, 0
	s_waitcnt vmcnt(19)
	v_pk_add_f32 v[72:73], v[72:73], v[136:137]
	v_pk_add_f32 v[74:75], v[74:75], v[138:139]
	s_waitcnt vmcnt(18)
	v_pk_add_f32 v[80:81], v[80:81], v[148:149]
	v_pk_add_f32 v[82:83], v[82:83], v[150:151]
	s_waitcnt vmcnt(17)
	v_pk_add_f32 v[88:89], v[88:89], v[152:153]
	v_pk_add_f32 v[90:91], v[90:91], v[154:155]
	s_waitcnt vmcnt(16)
	v_pk_add_f32 v[92:93], v[92:93], v[156:157]
	v_pk_add_f32 v[94:95], v[94:95], v[158:159]
	v_pk_add_f32 v[144:145], v[144:145], v[72:73]
	v_pk_add_f32 v[146:147], v[146:147], v[74:75]
	v_pk_add_f32 v[124:125], v[124:125], v[72:73]
	v_pk_add_f32 v[126:127], v[126:127], v[74:75]
	v_pk_add_f32 v[108:109], v[108:109], v[72:73]
	v_pk_add_f32 v[110:111], v[110:111], v[74:75]
	v_pk_add_f32 v[84:85], v[84:85], v[72:73]
	v_pk_add_f32 v[86:87], v[86:87], v[74:75]
	v_pk_add_f32 v[60:61], v[60:61], v[72:73]
	v_pk_add_f32 v[62:63], v[62:63], v[74:75]
	v_pk_add_f32 v[44:45], v[44:45], v[72:73]
	v_pk_add_f32 v[46:47], v[46:47], v[74:75]
	v_pk_add_f32 v[28:29], v[28:29], v[72:73]
	v_pk_add_f32 v[30:31], v[30:31], v[74:75]
	v_pk_add_f32 v[12:13], v[12:13], v[72:73]
	v_pk_add_f32 v[14:15], v[14:15], v[74:75]
	v_pk_add_f32 v[140:141], v[140:141], v[80:81]
	v_pk_add_f32 v[142:143], v[142:143], v[82:83]
	v_pk_add_f32 v[120:121], v[120:121], v[80:81]
	v_pk_add_f32 v[122:123], v[122:123], v[82:83]
	v_pk_add_f32 v[104:105], v[104:105], v[80:81]
	v_pk_add_f32 v[106:107], v[106:107], v[82:83]
	v_pk_add_f32 v[76:77], v[76:77], v[80:81]
	v_pk_add_f32 v[78:79], v[78:79], v[82:83]
	v_pk_add_f32 v[56:57], v[56:57], v[80:81]
	v_pk_add_f32 v[58:59], v[58:59], v[82:83]
	v_pk_add_f32 v[40:41], v[40:41], v[80:81]
	v_pk_add_f32 v[42:43], v[42:43], v[82:83]
	v_pk_add_f32 v[24:25], v[24:25], v[80:81]
	v_pk_add_f32 v[26:27], v[26:27], v[82:83]
	v_pk_add_f32 v[8:9], v[8:9], v[80:81]
	v_pk_add_f32 v[10:11], v[10:11], v[82:83]
	v_pk_add_f32 v[132:133], v[132:133], v[88:89]
	v_pk_add_f32 v[134:135], v[134:135], v[90:91]
	v_pk_add_f32 v[116:117], v[116:117], v[88:89]
	v_pk_add_f32 v[118:119], v[118:119], v[90:91]
	v_pk_add_f32 v[100:101], v[100:101], v[88:89]
	v_pk_add_f32 v[102:103], v[102:103], v[90:91]
	v_pk_add_f32 v[68:69], v[68:69], v[88:89]
	v_pk_add_f32 v[70:71], v[70:71], v[90:91]
	v_pk_add_f32 v[52:53], v[52:53], v[88:89]
	v_pk_add_f32 v[54:55], v[54:55], v[90:91]
	v_pk_add_f32 v[36:37], v[36:37], v[88:89]
	v_pk_add_f32 v[38:39], v[38:39], v[90:91]
	v_pk_add_f32 v[20:21], v[20:21], v[88:89]
	v_pk_add_f32 v[22:23], v[22:23], v[90:91]
	v_pk_add_f32 v[4:5], v[4:5], v[88:89]
	v_pk_add_f32 v[6:7], v[6:7], v[90:91]
	v_pk_add_f32 v[128:129], v[128:129], v[92:93]
	v_pk_add_f32 v[130:131], v[130:131], v[94:95]
	v_pk_add_f32 v[112:113], v[112:113], v[92:93]
	v_pk_add_f32 v[114:115], v[114:115], v[94:95]
	v_pk_add_f32 v[96:97], v[96:97], v[92:93]
	v_pk_add_f32 v[98:99], v[98:99], v[94:95]
	v_pk_add_f32 v[64:65], v[64:65], v[92:93]
	v_pk_add_f32 v[66:67], v[66:67], v[94:95]
	v_pk_add_f32 v[48:49], v[48:49], v[92:93]
	v_pk_add_f32 v[50:51], v[50:51], v[94:95]
	v_pk_add_f32 v[32:33], v[32:33], v[92:93]
	v_pk_add_f32 v[34:35], v[34:35], v[94:95]
	v_pk_add_f32 v[16:17], v[16:17], v[92:93]
	v_pk_add_f32 v[18:19], v[18:19], v[94:95]
	v_pk_add_f32 v[0:1], v[0:1], v[92:93]
	v_pk_add_f32 v[2:3], v[2:3], v[94:95]
	s_add_u32 s94, s98, 0xc000
	s_addc_u32 s95, s99, 0
	global_load_dwordx4 v[240:243], v191, s[94:95] offset:0 nt
	global_load_dwordx4 v[244:247], v191, s[94:95] offset:64 nt
	s_add_u32 s94, s98, 0x12000
	s_addc_u32 s95, s99, 0
	global_load_dwordx4 v[248:251], v191, s[94:95] offset:0 nt
	global_load_dwordx4 v[252:255], v191, s[94:95] offset:64 nt
	s_add_u32 s94, s98, 0x30000
	s_addc_u32 s95, s99, 0
	global_load_dwordx4 v[136:139], v191, s[94:95] offset:0 nt
	global_load_dwordx4 v[148:151], v191, s[94:95] offset:64 nt
	s_add_u32 s94, s98, 0x36000
	s_addc_u32 s95, s99, 0
	global_load_dwordx4 v[152:155], v191, s[94:95] offset:0 nt
	global_load_dwordx4 v[156:159], v191, s[94:95] offset:64 nt
	s_waitcnt vmcnt(19)
	s_waitcnt vmcnt(11)
	v_cvt_f32_f16_e32 v72, v208
	v_cvt_f32_f16_sdwa v73, v208 dst_sel:DWORD dst_unused:UNUSED_PAD src0_sel:WORD_1
	v_cvt_f32_f16_e32 v74, v209
	v_cvt_f32_f16_sdwa v75, v209 dst_sel:DWORD dst_unused:UNUSED_PAD src0_sel:WORD_1
	v_cvt_f32_f16_e32 v80, v210
	v_cvt_f32_f16_sdwa v81, v210 dst_sel:DWORD dst_unused:UNUSED_PAD src0_sel:WORD_1
	v_cvt_f32_f16_e32 v82, v211
	v_cvt_f32_f16_sdwa v83, v211 dst_sel:DWORD dst_unused:UNUSED_PAD src0_sel:WORD_1
	v_sub_f32_e32 v72, v72, v238
	v_sub_f32_e32 v73, v73, v238
	v_sub_f32_e32 v74, v74, v238
	v_sub_f32_e32 v75, v75, v238
	v_sub_f32_e32 v80, v80, v238
	v_sub_f32_e32 v81, v81, v238
	v_sub_f32_e32 v82, v82, v238
	v_sub_f32_e32 v83, v83, v238
	v_pk_mul_f32 v[72:73], v[238:239], v[72:73] op_sel:[1,0]
	v_pk_mul_f32 v[74:75], v[238:239], v[74:75] op_sel:[1,0]
	v_pk_mul_f32 v[80:81], v[238:239], v[80:81] op_sel:[1,0]
	v_pk_mul_f32 v[82:83], v[238:239], v[82:83] op_sel:[1,0]
	v_pk_fma_f32 v[144:145], v[72:73], v[160:161], v[144:145]
	v_pk_fma_f32 v[146:147], v[74:75], v[162:163], v[146:147]
	v_pk_fma_f32 v[140:141], v[80:81], v[164:165], v[140:141]
	v_pk_fma_f32 v[142:143], v[82:83], v[166:167], v[142:143]
	v_cvt_pk_f16_f32 v144, v144, v145
	v_cvt_pk_f16_f32 v145, v146, v147
	v_cvt_pk_f16_f32 v146, v140, v141
	v_cvt_pk_f16_f32 v147, v142, v143
	ds_write_b128 v235, v[144:147]
	v_fma_mix_f32 v206, v144, 1.0, 0 op_sel_hi:[1,0,0]
	v_fma_mix_f32 v207, v144, v144, 0 op_sel_hi:[1,1,0]
	v_fma_mix_f32 v206, v144, 1.0, v206 op_sel:[1,0,0] op_sel_hi:[1,0,0]
	v_fma_mix_f32 v207, v144, v144, v207 op_sel:[1,1,0] op_sel_hi:[1,1,0]
	v_fma_mix_f32 v206, v145, 1.0, v206 op_sel_hi:[1,0,0]
	v_fma_mix_f32 v207, v145, v145, v207 op_sel_hi:[1,1,0]
	v_fma_mix_f32 v206, v145, 1.0, v206 op_sel:[1,0,0] op_sel_hi:[1,0,0]
	v_fma_mix_f32 v207, v145, v145, v207 op_sel:[1,1,0] op_sel_hi:[1,1,0]
	v_fma_mix_f32 v206, v146, 1.0, v206 op_sel_hi:[1,0,0]
	v_fma_mix_f32 v207, v146, v146, v207 op_sel_hi:[1,1,0]
	v_fma_mix_f32 v206, v146, 1.0, v206 op_sel:[1,0,0] op_sel_hi:[1,0,0]
	v_fma_mix_f32 v207, v146, v146, v207 op_sel:[1,1,0] op_sel_hi:[1,1,0]
	v_fma_mix_f32 v206, v147, 1.0, v206 op_sel_hi:[1,0,0]
	v_fma_mix_f32 v207, v147, v147, v207 op_sel_hi:[1,1,0]
	v_fma_mix_f32 v206, v147, 1.0, v206 op_sel:[1,0,0] op_sel_hi:[1,0,0]
	v_fma_mix_f32 v207, v147, v147, v207 op_sel:[1,1,0] op_sel_hi:[1,1,0]
	s_waitcnt vmcnt(10)
	v_cvt_f32_f16_e32 v72, v212
	v_cvt_f32_f16_sdwa v73, v212 dst_sel:DWORD dst_unused:UNUSED_PAD src0_sel:WORD_1
	v_cvt_f32_f16_e32 v74, v213
	v_cvt_f32_f16_sdwa v75, v213 dst_sel:DWORD dst_unused:UNUSED_PAD src0_sel:WORD_1
	v_cvt_f32_f16_e32 v80, v214
	v_cvt_f32_f16_sdwa v81, v214 dst_sel:DWORD dst_unused:UNUSED_PAD src0_sel:WORD_1
	v_cvt_f32_f16_e32 v82, v215
	v_cvt_f32_f16_sdwa v83, v215 dst_sel:DWORD dst_unused:UNUSED_PAD src0_sel:WORD_1
	v_sub_f32_e32 v72, v72, v238
	v_sub_f32_e32 v73, v73, v238
	v_sub_f32_e32 v74, v74, v238
	v_sub_f32_e32 v75, v75, v238
	v_sub_f32_e32 v80, v80, v238
	v_sub_f32_e32 v81, v81, v238
	v_sub_f32_e32 v82, v82, v238
	v_sub_f32_e32 v83, v83, v238
	v_pk_mul_f32 v[72:73], v[238:239], v[72:73] op_sel:[1,0]
	v_pk_mul_f32 v[74:75], v[238:239], v[74:75] op_sel:[1,0]
	v_pk_mul_f32 v[80:81], v[238:239], v[80:81] op_sel:[1,0]
	v_pk_mul_f32 v[82:83], v[238:239], v[82:83] op_sel:[1,0]
	v_pk_fma_f32 v[132:133], v[72:73], v[168:169], v[132:133]
	v_pk_fma_f32 v[134:135], v[74:75], v[170:171], v[134:135]
	v_pk_fma_f32 v[128:129], v[80:81], v[172:173], v[128:129]
	v_pk_fma_f32 v[130:131], v[82:83], v[174:175], v[130:131]
	v_cvt_pk_f16_f32 v132, v132, v133
	v_cvt_pk_f16_f32 v133, v134, v135
	v_cvt_pk_f16_f32 v134, v128, v129
	v_cvt_pk_f16_f32 v135, v130, v131
	ds_write_b128 v235, v[132:135] offset:64
	v_fma_mix_f32 v206, v132, 1.0, v206 op_sel_hi:[1,0,0]
	v_fma_mix_f32 v207, v132, v132, v207 op_sel_hi:[1,1,0]
	v_fma_mix_f32 v206, v132, 1.0, v206 op_sel:[1,0,0] op_sel_hi:[1,0,0]
	v_fma_mix_f32 v207, v132, v132, v207 op_sel:[1,1,0] op_sel_hi:[1,1,0]
	v_fma_mix_f32 v206, v133, 1.0, v206 op_sel_hi:[1,0,0]
	v_fma_mix_f32 v207, v133, v133, v207 op_sel_hi:[1,1,0]
	v_fma_mix_f32 v206, v133, 1.0, v206 op_sel:[1,0,0] op_sel_hi:[1,0,0]
	v_fma_mix_f32 v207, v133, v133, v207 op_sel:[1,1,0] op_sel_hi:[1,1,0]
	v_fma_mix_f32 v206, v134, 1.0, v206 op_sel_hi:[1,0,0]
	v_fma_mix_f32 v207, v134, v134, v207 op_sel_hi:[1,1,0]
	v_fma_mix_f32 v206, v134, 1.0, v206 op_sel:[1,0,0] op_sel_hi:[1,0,0]
	v_fma_mix_f32 v207, v134, v134, v207 op_sel:[1,1,0] op_sel_hi:[1,1,0]
	v_fma_mix_f32 v206, v135, 1.0, v206 op_sel_hi:[1,0,0]
	v_fma_mix_f32 v207, v135, v135, v207 op_sel_hi:[1,1,0]
	v_fma_mix_f32 v206, v135, 1.0, v206 op_sel:[1,0,0] op_sel_hi:[1,0,0]
	v_fma_mix_f32 v207, v135, v135, v207 op_sel:[1,1,0] op_sel_hi:[1,1,0]
	ds_read_b128 v[88:91], v236
	ds_read_b128 v[92:95], v236 offset:1152
	s_waitcnt vmcnt(9)
	v_cvt_f32_f16_e32 v72, v216
	v_cvt_f32_f16_sdwa v73, v216 dst_sel:DWORD dst_unused:UNUSED_PAD src0_sel:WORD_1
	v_cvt_f32_f16_e32 v74, v217
	v_cvt_f32_f16_sdwa v75, v217 dst_sel:DWORD dst_unused:UNUSED_PAD src0_sel:WORD_1
	v_cvt_f32_f16_e32 v80, v218
	v_cvt_f32_f16_sdwa v81, v218 dst_sel:DWORD dst_unused:UNUSED_PAD src0_sel:WORD_1
	v_cvt_f32_f16_e32 v82, v219
	v_cvt_f32_f16_sdwa v83, v219 dst_sel:DWORD dst_unused:UNUSED_PAD src0_sel:WORD_1
	v_sub_f32_e32 v72, v72, v192
	v_sub_f32_e32 v73, v73, v192
	v_sub_f32_e32 v74, v74, v192
	v_sub_f32_e32 v75, v75, v192
	v_sub_f32_e32 v80, v80, v192
	v_sub_f32_e32 v81, v81, v192
	v_sub_f32_e32 v82, v82, v192
	v_sub_f32_e32 v83, v83, v192
	v_pk_mul_f32 v[72:73], v[192:193], v[72:73] op_sel:[1,0]
	v_pk_mul_f32 v[74:75], v[192:193], v[74:75] op_sel:[1,0]
	v_pk_mul_f32 v[80:81], v[192:193], v[80:81] op_sel:[1,0]
	v_pk_mul_f32 v[82:83], v[192:193], v[82:83] op_sel:[1,0]
	v_pk_fma_f32 v[124:125], v[72:73], v[160:161], v[124:125]
	v_pk_fma_f32 v[126:127], v[74:75], v[162:163], v[126:127]
	v_pk_fma_f32 v[120:121], v[80:81], v[164:165], v[120:121]
	v_pk_fma_f32 v[122:123], v[82:83], v[166:167], v[122:123]
	v_cvt_pk_f16_f32 v124, v124, v125
	v_cvt_pk_f16_f32 v125, v126, v127
	v_cvt_pk_f16_f32 v126, v120, v121
	v_cvt_pk_f16_f32 v127, v122, v123
	s_waitcnt lgkmcnt(0)
	buffer_store_dwordx4 v[88:91], v225, s[24:27], 0 offen nt
	v_add_u32_e32 v82, 0x3000, v225
	buffer_store_dwordx4 v[92:95], v82, s[24:27], 0 offen nt
	ds_write_b128 v235, v[124:127]
	v_fma_mix_f32 v140, v124, 1.0, 0 op_sel_hi:[1,0,0]
	v_fma_mix_f32 v141, v124, v124, 0 op_sel_hi:[1,1,0]
	v_fma_mix_f32 v140, v124, 1.0, v140 op_sel:[1,0,0] op_sel_hi:[1,0,0]
	v_fma_mix_f32 v141, v124, v124, v141 op_sel:[1,1,0] op_sel_hi:[1,1,0]
	v_fma_mix_f32 v140, v125, 1.0, v140 op_sel_hi:[1,0,0]
	v_fma_mix_f32 v141, v125, v125, v141 op_sel_hi:[1,1,0]
	v_fma_mix_f32 v140, v125, 1.0, v140 op_sel:[1,0,0] op_sel_hi:[1,0,0]
	v_fma_mix_f32 v141, v125, v125, v141 op_sel:[1,1,0] op_sel_hi:[1,1,0]
	v_fma_mix_f32 v140, v126, 1.0, v140 op_sel_hi:[1,0,0]
	v_fma_mix_f32 v141, v126, v126, v141 op_sel_hi:[1,1,0]
	v_fma_mix_f32 v140, v126, 1.0, v140 op_sel:[1,0,0] op_sel_hi:[1,0,0]
	v_fma_mix_f32 v141, v126, v126, v141 op_sel:[1,1,0] op_sel_hi:[1,1,0]
	v_fma_mix_f32 v140, v127, 1.0, v140 op_sel_hi:[1,0,0]
	v_fma_mix_f32 v141, v127, v127, v141 op_sel_hi:[1,1,0]
	v_fma_mix_f32 v140, v127, 1.0, v140 op_sel:[1,0,0] op_sel_hi:[1,0,0]
	v_fma_mix_f32 v141, v127, v127, v141 op_sel:[1,1,0] op_sel_hi:[1,1,0]
	s_waitcnt vmcnt(10)
	v_cvt_f32_f16_e32 v72, v220
	v_cvt_f32_f16_sdwa v73, v220 dst_sel:DWORD dst_unused:UNUSED_PAD src0_sel:WORD_1
	v_cvt_f32_f16_e32 v74, v221
	v_cvt_f32_f16_sdwa v75, v221 dst_sel:DWORD dst_unused:UNUSED_PAD src0_sel:WORD_1
	v_cvt_f32_f16_e32 v80, v222
	v_cvt_f32_f16_sdwa v81, v222 dst_sel:DWORD dst_unused:UNUSED_PAD src0_sel:WORD_1
	v_cvt_f32_f16_e32 v82, v223
	v_cvt_f32_f16_sdwa v83, v223 dst_sel:DWORD dst_unused:UNUSED_PAD src0_sel:WORD_1
	v_sub_f32_e32 v72, v72, v192
	v_sub_f32_e32 v73, v73, v192
	v_sub_f32_e32 v74, v74, v192
	v_sub_f32_e32 v75, v75, v192
	v_sub_f32_e32 v80, v80, v192
	v_sub_f32_e32 v81, v81, v192
	v_sub_f32_e32 v82, v82, v192
	v_sub_f32_e32 v83, v83, v192
	v_pk_mul_f32 v[72:73], v[192:193], v[72:73] op_sel:[1,0]
	v_pk_mul_f32 v[74:75], v[192:193], v[74:75] op_sel:[1,0]
	v_pk_mul_f32 v[80:81], v[192:193], v[80:81] op_sel:[1,0]
	v_pk_mul_f32 v[82:83], v[192:193], v[82:83] op_sel:[1,0]
	v_pk_fma_f32 v[116:117], v[72:73], v[168:169], v[116:117]
	v_pk_fma_f32 v[118:119], v[74:75], v[170:171], v[118:119]
	v_pk_fma_f32 v[112:113], v[80:81], v[172:173], v[112:113]
	v_pk_fma_f32 v[114:115], v[82:83], v[174:175], v[114:115]
	v_cvt_pk_f16_f32 v116, v116, v117
	v_cvt_pk_f16_f32 v117, v118, v119
	v_cvt_pk_f16_f32 v118, v112, v113
	v_cvt_pk_f16_f32 v119, v114, v115
	ds_write_b128 v235, v[116:119] offset:64
	v_fma_mix_f32 v140, v116, 1.0, v140 op_sel_hi:[1,0,0]
	v_fma_mix_f32 v141, v116, v116, v141 op_sel_hi:[1,1,0]
	v_fma_mix_f32 v140, v116, 1.0, v140 op_sel:[1,0,0] op_sel_hi:[1,0,0]
	v_fma_mix_f32 v141, v116, v116, v141 op_sel:[1,1,0] op_sel_hi:[1,1,0]
	v_fma_mix_f32 v140, v117, 1.0, v140 op_sel_hi:[1,0,0]
	v_fma_mix_f32 v141, v117, v117, v141 op_sel_hi:[1,1,0]
	v_fma_mix_f32 v140, v117, 1.0, v140 op_sel:[1,0,0] op_sel_hi:[1,0,0]
	v_fma_mix_f32 v141, v117, v117, v141 op_sel:[1,1,0] op_sel_hi:[1,1,0]
	v_fma_mix_f32 v140, v118, 1.0, v140 op_sel_hi:[1,0,0]
	v_fma_mix_f32 v141, v118, v118, v141 op_sel_hi:[1,1,0]
	v_fma_mix_f32 v140, v118, 1.0, v140 op_sel:[1,0,0] op_sel_hi:[1,0,0]
	v_fma_mix_f32 v141, v118, v118, v141 op_sel:[1,1,0] op_sel_hi:[1,1,0]
	v_fma_mix_f32 v140, v119, 1.0, v140 op_sel_hi:[1,0,0]
	v_fma_mix_f32 v141, v119, v119, v141 op_sel_hi:[1,1,0]
	v_fma_mix_f32 v140, v119, 1.0, v140 op_sel:[1,0,0] op_sel_hi:[1,0,0]
	v_fma_mix_f32 v141, v119, v119, v141 op_sel:[1,1,0] op_sel_hi:[1,1,0]
	ds_read_b128 v[208:211], v236
	ds_read_b128 v[128:131], v236 offset:1152
	s_add_u32 s94, s98, 0x3c000
	s_addc_u32 s95, s99, 0
	global_load_dwordx4 v[212:215], v191, s[94:95] offset:0 nt
	global_load_dwordx4 v[144:147], v191, s[94:95] offset:64 nt
	s_add_u32 s94, s98, 0x42000
	s_addc_u32 s95, s99, 0
	global_load_dwordx4 v[132:135], v191, s[94:95] offset:0 nt
	global_load_dwordx4 v[88:91], v191, s[94:95] offset:64 nt
	s_waitcnt vmcnt(13)
	v_cvt_f32_f16_e32 v72, v240
	v_cvt_f32_f16_sdwa v73, v240 dst_sel:DWORD dst_unused:UNUSED_PAD src0_sel:WORD_1
	v_cvt_f32_f16_e32 v74, v241
	v_cvt_f32_f16_sdwa v75, v241 dst_sel:DWORD dst_unused:UNUSED_PAD src0_sel:WORD_1
	v_cvt_f32_f16_e32 v80, v242
	v_cvt_f32_f16_sdwa v81, v242 dst_sel:DWORD dst_unused:UNUSED_PAD src0_sel:WORD_1
	v_cvt_f32_f16_e32 v82, v243
	v_cvt_f32_f16_sdwa v83, v243 dst_sel:DWORD dst_unused:UNUSED_PAD src0_sel:WORD_1
	v_sub_f32_e32 v72, v72, v194
	v_sub_f32_e32 v73, v73, v194
	v_sub_f32_e32 v74, v74, v194
	v_sub_f32_e32 v75, v75, v194
	v_sub_f32_e32 v80, v80, v194
	v_sub_f32_e32 v81, v81, v194
	v_sub_f32_e32 v82, v82, v194
	v_sub_f32_e32 v83, v83, v194
	v_pk_mul_f32 v[72:73], v[194:195], v[72:73] op_sel:[1,0]
	v_pk_mul_f32 v[74:75], v[194:195], v[74:75] op_sel:[1,0]
	v_pk_mul_f32 v[80:81], v[194:195], v[80:81] op_sel:[1,0]
	v_pk_mul_f32 v[82:83], v[194:195], v[82:83] op_sel:[1,0]
	v_pk_fma_f32 v[108:109], v[72:73], v[160:161], v[108:109]
	v_pk_fma_f32 v[110:111], v[74:75], v[162:163], v[110:111]
	v_pk_fma_f32 v[104:105], v[80:81], v[164:165], v[104:105]
	v_pk_fma_f32 v[106:107], v[82:83], v[166:167], v[106:107]
	v_cvt_pk_f16_f32 v108, v108, v109
	v_cvt_pk_f16_f32 v109, v110, v111
	v_cvt_pk_f16_f32 v110, v104, v105
	v_cvt_pk_f16_f32 v111, v106, v107
	s_waitcnt lgkmcnt(0)
	v_add_u32_e32 v83, 0x6000, v225
	buffer_store_dwordx4 v[208:211], v83, s[24:27], 0 offen nt
	v_add_u32_e32 v82, 0x9000, v225
	buffer_store_dwordx4 v[128:131], v82, s[24:27], 0 offen nt
	ds_write_b128 v235, v[108:111]
	v_fma_mix_f32 v142, v108, 1.0, 0 op_sel_hi:[1,0,0]
	v_fma_mix_f32 v143, v108, v108, 0 op_sel_hi:[1,1,0]
	v_fma_mix_f32 v142, v108, 1.0, v142 op_sel:[1,0,0] op_sel_hi:[1,0,0]
	v_fma_mix_f32 v143, v108, v108, v143 op_sel:[1,1,0] op_sel_hi:[1,1,0]
	v_fma_mix_f32 v142, v109, 1.0, v142 op_sel_hi:[1,0,0]
	v_fma_mix_f32 v143, v109, v109, v143 op_sel_hi:[1,1,0]
	v_fma_mix_f32 v142, v109, 1.0, v142 op_sel:[1,0,0] op_sel_hi:[1,0,0]
	v_fma_mix_f32 v143, v109, v109, v143 op_sel:[1,1,0] op_sel_hi:[1,1,0]
	v_fma_mix_f32 v142, v110, 1.0, v142 op_sel_hi:[1,0,0]
	v_fma_mix_f32 v143, v110, v110, v143 op_sel_hi:[1,1,0]
	v_fma_mix_f32 v142, v110, 1.0, v142 op_sel:[1,0,0] op_sel_hi:[1,0,0]
	v_fma_mix_f32 v143, v110, v110, v143 op_sel:[1,1,0] op_sel_hi:[1,1,0]
	v_fma_mix_f32 v142, v111, 1.0, v142 op_sel_hi:[1,0,0]
	v_fma_mix_f32 v143, v111, v111, v143 op_sel_hi:[1,1,0]
	v_fma_mix_f32 v142, v111, 1.0, v142 op_sel:[1,0,0] op_sel_hi:[1,0,0]
	v_fma_mix_f32 v143, v111, v111, v143 op_sel:[1,1,0] op_sel_hi:[1,1,0]
	s_waitcnt vmcnt(14)
	v_cvt_f32_f16_e32 v72, v244
	v_cvt_f32_f16_sdwa v73, v244 dst_sel:DWORD dst_unused:UNUSED_PAD src0_sel:WORD_1
	v_cvt_f32_f16_e32 v74, v245
	v_cvt_f32_f16_sdwa v75, v245 dst_sel:DWORD dst_unused:UNUSED_PAD src0_sel:WORD_1
	v_cvt_f32_f16_e32 v80, v246
	v_cvt_f32_f16_sdwa v81, v246 dst_sel:DWORD dst_unused:UNUSED_PAD src0_sel:WORD_1
	v_cvt_f32_f16_e32 v82, v247
	v_cvt_f32_f16_sdwa v83, v247 dst_sel:DWORD dst_unused:UNUSED_PAD src0_sel:WORD_1
	v_sub_f32_e32 v72, v72, v194
	v_sub_f32_e32 v73, v73, v194
	v_sub_f32_e32 v74, v74, v194
	v_sub_f32_e32 v75, v75, v194
	v_sub_f32_e32 v80, v80, v194
	v_sub_f32_e32 v81, v81, v194
	v_sub_f32_e32 v82, v82, v194
	v_sub_f32_e32 v83, v83, v194
	v_pk_mul_f32 v[72:73], v[194:195], v[72:73] op_sel:[1,0]
	v_pk_mul_f32 v[74:75], v[194:195], v[74:75] op_sel:[1,0]
	v_pk_mul_f32 v[80:81], v[194:195], v[80:81] op_sel:[1,0]
	v_pk_mul_f32 v[82:83], v[194:195], v[82:83] op_sel:[1,0]
	v_pk_fma_f32 v[100:101], v[72:73], v[168:169], v[100:101]
	v_pk_fma_f32 v[102:103], v[74:75], v[170:171], v[102:103]
	v_pk_fma_f32 v[96:97], v[80:81], v[172:173], v[96:97]
	v_pk_fma_f32 v[98:99], v[82:83], v[174:175], v[98:99]
	v_cvt_pk_f16_f32 v100, v100, v101
	v_cvt_pk_f16_f32 v101, v102, v103
	v_cvt_pk_f16_f32 v102, v96, v97
	v_cvt_pk_f16_f32 v103, v98, v99
	ds_write_b128 v235, v[100:103] offset:64
	v_fma_mix_f32 v142, v100, 1.0, v142 op_sel_hi:[1,0,0]
	v_fma_mix_f32 v143, v100, v100, v143 op_sel_hi:[1,1,0]
	v_fma_mix_f32 v142, v100, 1.0, v142 op_sel:[1,0,0] op_sel_hi:[1,0,0]
	v_fma_mix_f32 v143, v100, v100, v143 op_sel:[1,1,0] op_sel_hi:[1,1,0]
	v_fma_mix_f32 v142, v101, 1.0, v142 op_sel_hi:[1,0,0]
	v_fma_mix_f32 v143, v101, v101, v143 op_sel_hi:[1,1,0]
	v_fma_mix_f32 v142, v101, 1.0, v142 op_sel:[1,0,0] op_sel_hi:[1,0,0]
	v_fma_mix_f32 v143, v101, v101, v143 op_sel:[1,1,0] op_sel_hi:[1,1,0]
	v_fma_mix_f32 v142, v102, 1.0, v142 op_sel_hi:[1,0,0]
	v_fma_mix_f32 v143, v102, v102, v143 op_sel_hi:[1,1,0]
	v_fma_mix_f32 v142, v102, 1.0, v142 op_sel:[1,0,0] op_sel_hi:[1,0,0]
	v_fma_mix_f32 v143, v102, v102, v143 op_sel:[1,1,0] op_sel_hi:[1,1,0]
	v_fma_mix_f32 v142, v103, 1.0, v142 op_sel_hi:[1,0,0]
	v_fma_mix_f32 v143, v103, v103, v143 op_sel_hi:[1,1,0]
	v_fma_mix_f32 v142, v103, 1.0, v142 op_sel:[1,0,0] op_sel_hi:[1,0,0]
	v_fma_mix_f32 v143, v103, v103, v143 op_sel:[1,1,0] op_sel_hi:[1,1,0]
	ds_read_b128 v[92:95], v236
	ds_read_b128 v[120:123], v236 offset:1152
	s_waitcnt vmcnt(13)
	v_cvt_f32_f16_e32 v72, v248
	v_cvt_f32_f16_sdwa v73, v248 dst_sel:DWORD dst_unused:UNUSED_PAD src0_sel:WORD_1
	v_cvt_f32_f16_e32 v74, v249
	v_cvt_f32_f16_sdwa v75, v249 dst_sel:DWORD dst_unused:UNUSED_PAD src0_sel:WORD_1
	v_cvt_f32_f16_e32 v80, v250
	v_cvt_f32_f16_sdwa v81, v250 dst_sel:DWORD dst_unused:UNUSED_PAD src0_sel:WORD_1
	v_cvt_f32_f16_e32 v82, v251
	v_cvt_f32_f16_sdwa v83, v251 dst_sel:DWORD dst_unused:UNUSED_PAD src0_sel:WORD_1
	v_sub_f32_e32 v72, v72, v196
	v_sub_f32_e32 v73, v73, v196
	v_sub_f32_e32 v74, v74, v196
	v_sub_f32_e32 v75, v75, v196
	v_sub_f32_e32 v80, v80, v196
	v_sub_f32_e32 v81, v81, v196
	v_sub_f32_e32 v82, v82, v196
	v_sub_f32_e32 v83, v83, v196
	v_pk_mul_f32 v[72:73], v[196:197], v[72:73] op_sel:[1,0]
	v_pk_mul_f32 v[74:75], v[196:197], v[74:75] op_sel:[1,0]
	v_pk_mul_f32 v[80:81], v[196:197], v[80:81] op_sel:[1,0]
	v_pk_mul_f32 v[82:83], v[196:197], v[82:83] op_sel:[1,0]
	v_pk_fma_f32 v[84:85], v[72:73], v[160:161], v[84:85]
	v_pk_fma_f32 v[86:87], v[74:75], v[162:163], v[86:87]
	v_pk_fma_f32 v[76:77], v[80:81], v[164:165], v[76:77]
	v_pk_fma_f32 v[78:79], v[82:83], v[166:167], v[78:79]
	v_cvt_pk_f16_f32 v84, v84, v85
	v_cvt_pk_f16_f32 v85, v86, v87
	v_cvt_pk_f16_f32 v86, v76, v77
	v_cvt_pk_f16_f32 v87, v78, v79
	s_waitcnt lgkmcnt(0)
	v_add_u32_e32 v83, 0xc000, v225
	buffer_store_dwordx4 v[92:95], v83, s[24:27], 0 offen nt
	v_add_u32_e32 v82, 0xf000, v225
	buffer_store_dwordx4 v[120:123], v82, s[24:27], 0 offen nt
	ds_write_b128 v235, v[84:87]
	v_fma_mix_f32 v216, v84, 1.0, 0 op_sel_hi:[1,0,0]
	v_fma_mix_f32 v217, v84, v84, 0 op_sel_hi:[1,1,0]
	v_fma_mix_f32 v216, v84, 1.0, v216 op_sel:[1,0,0] op_sel_hi:[1,0,0]
	v_fma_mix_f32 v217, v84, v84, v217 op_sel:[1,1,0] op_sel_hi:[1,1,0]
	v_fma_mix_f32 v216, v85, 1.0, v216 op_sel_hi:[1,0,0]
	v_fma_mix_f32 v217, v85, v85, v217 op_sel_hi:[1,1,0]
	v_fma_mix_f32 v216, v85, 1.0, v216 op_sel:[1,0,0] op_sel_hi:[1,0,0]
	v_fma_mix_f32 v217, v85, v85, v217 op_sel:[1,1,0] op_sel_hi:[1,1,0]
	v_fma_mix_f32 v216, v86, 1.0, v216 op_sel_hi:[1,0,0]
	v_fma_mix_f32 v217, v86, v86, v217 op_sel_hi:[1,1,0]
	v_fma_mix_f32 v216, v86, 1.0, v216 op_sel:[1,0,0] op_sel_hi:[1,0,0]
	v_fma_mix_f32 v217, v86, v86, v217 op_sel:[1,1,0] op_sel_hi:[1,1,0]
	v_fma_mix_f32 v216, v87, 1.0, v216 op_sel_hi:[1,0,0]
	v_fma_mix_f32 v217, v87, v87, v217 op_sel_hi:[1,1,0]
	v_fma_mix_f32 v216, v87, 1.0, v216 op_sel:[1,0,0] op_sel_hi:[1,0,0]
	v_fma_mix_f32 v217, v87, v87, v217 op_sel:[1,1,0] op_sel_hi:[1,1,0]
	s_waitcnt vmcnt(14)
	v_cvt_f32_f16_e32 v72, v252
	v_cvt_f32_f16_sdwa v73, v252 dst_sel:DWORD dst_unused:UNUSED_PAD src0_sel:WORD_1
	v_cvt_f32_f16_e32 v74, v253
	v_cvt_f32_f16_sdwa v75, v253 dst_sel:DWORD dst_unused:UNUSED_PAD src0_sel:WORD_1
	v_cvt_f32_f16_e32 v80, v254
	v_cvt_f32_f16_sdwa v81, v254 dst_sel:DWORD dst_unused:UNUSED_PAD src0_sel:WORD_1
	v_cvt_f32_f16_e32 v82, v255
	v_cvt_f32_f16_sdwa v83, v255 dst_sel:DWORD dst_unused:UNUSED_PAD src0_sel:WORD_1
	v_sub_f32_e32 v72, v72, v196
	v_sub_f32_e32 v73, v73, v196
	v_sub_f32_e32 v74, v74, v196
	v_sub_f32_e32 v75, v75, v196
	v_sub_f32_e32 v80, v80, v196
	v_sub_f32_e32 v81, v81, v196
	v_sub_f32_e32 v82, v82, v196
	v_sub_f32_e32 v83, v83, v196
	v_pk_mul_f32 v[72:73], v[196:197], v[72:73] op_sel:[1,0]
	v_pk_mul_f32 v[74:75], v[196:197], v[74:75] op_sel:[1,0]
	v_pk_mul_f32 v[80:81], v[196:197], v[80:81] op_sel:[1,0]
	v_pk_mul_f32 v[82:83], v[196:197], v[82:83] op_sel:[1,0]
	v_pk_fma_f32 v[68:69], v[72:73], v[168:169], v[68:69]
	v_pk_fma_f32 v[70:71], v[74:75], v[170:171], v[70:71]
	v_pk_fma_f32 v[64:65], v[80:81], v[172:173], v[64:65]
	v_pk_fma_f32 v[66:67], v[82:83], v[174:175], v[66:67]
	v_cvt_pk_f16_f32 v68, v68, v69
	v_cvt_pk_f16_f32 v69, v70, v71
	v_cvt_pk_f16_f32 v70, v64, v65
	v_cvt_pk_f16_f32 v71, v66, v67
	ds_write_b128 v235, v[68:71] offset:64
	v_fma_mix_f32 v216, v68, 1.0, v216 op_sel_hi:[1,0,0]
	v_fma_mix_f32 v217, v68, v68, v217 op_sel_hi:[1,1,0]
	v_fma_mix_f32 v216, v68, 1.0, v216 op_sel:[1,0,0] op_sel_hi:[1,0,0]
	v_fma_mix_f32 v217, v68, v68, v217 op_sel:[1,1,0] op_sel_hi:[1,1,0]
	v_fma_mix_f32 v216, v69, 1.0, v216 op_sel_hi:[1,0,0]
	v_fma_mix_f32 v217, v69, v69, v217 op_sel_hi:[1,1,0]
	v_fma_mix_f32 v216, v69, 1.0, v216 op_sel:[1,0,0] op_sel_hi:[1,0,0]
	v_fma_mix_f32 v217, v69, v69, v217 op_sel:[1,1,0] op_sel_hi:[1,1,0]
	v_fma_mix_f32 v216, v70, 1.0, v216 op_sel_hi:[1,0,0]
	v_fma_mix_f32 v217, v70, v70, v217 op_sel_hi:[1,1,0]
	v_fma_mix_f32 v216, v70, 1.0, v216 op_sel:[1,0,0] op_sel_hi:[1,0,0]
	v_fma_mix_f32 v217, v70, v70, v217 op_sel:[1,1,0] op_sel_hi:[1,1,0]
	v_fma_mix_f32 v216, v71, 1.0, v216 op_sel_hi:[1,0,0]
	v_fma_mix_f32 v217, v71, v71, v217 op_sel_hi:[1,1,0]
	v_fma_mix_f32 v216, v71, 1.0, v216 op_sel:[1,0,0] op_sel_hi:[1,0,0]
	v_fma_mix_f32 v217, v71, v71, v217 op_sel:[1,1,0] op_sel_hi:[1,1,0]
	ds_read_b128 v[112:115], v236
	ds_read_b128 v[220:223], v236 offset:1152
	s_waitcnt vmcnt(13)
	v_cvt_f32_f16_e32 v72, v136
	v_cvt_f32_f16_sdwa v73, v136 dst_sel:DWORD dst_unused:UNUSED_PAD src0_sel:WORD_1
	v_cvt_f32_f16_e32 v74, v137
	v_cvt_f32_f16_sdwa v75, v137 dst_sel:DWORD dst_unused:UNUSED_PAD src0_sel:WORD_1
	v_cvt_f32_f16_e32 v80, v138
	v_cvt_f32_f16_sdwa v81, v138 dst_sel:DWORD dst_unused:UNUSED_PAD src0_sel:WORD_1
	v_cvt_f32_f16_e32 v82, v139
	v_cvt_f32_f16_sdwa v83, v139 dst_sel:DWORD dst_unused:UNUSED_PAD src0_sel:WORD_1
	v_sub_f32_e32 v72, v72, v198
	v_sub_f32_e32 v73, v73, v198
	v_sub_f32_e32 v74, v74, v198
	v_sub_f32_e32 v75, v75, v198
	v_sub_f32_e32 v80, v80, v198
	v_sub_f32_e32 v81, v81, v198
	v_sub_f32_e32 v82, v82, v198
	v_sub_f32_e32 v83, v83, v198
	v_pk_mul_f32 v[72:73], v[198:199], v[72:73] op_sel:[1,0]
	v_pk_mul_f32 v[74:75], v[198:199], v[74:75] op_sel:[1,0]
	v_pk_mul_f32 v[80:81], v[198:199], v[80:81] op_sel:[1,0]
	v_pk_mul_f32 v[82:83], v[198:199], v[82:83] op_sel:[1,0]
	v_pk_fma_f32 v[60:61], v[72:73], v[160:161], v[60:61]
	v_pk_fma_f32 v[62:63], v[74:75], v[162:163], v[62:63]
	v_pk_fma_f32 v[56:57], v[80:81], v[164:165], v[56:57]
	v_pk_fma_f32 v[58:59], v[82:83], v[166:167], v[58:59]
	v_cvt_pk_f16_f32 v60, v60, v61
	v_cvt_pk_f16_f32 v61, v62, v63
	v_cvt_pk_f16_f32 v62, v56, v57
	v_cvt_pk_f16_f32 v63, v58, v59
	s_waitcnt lgkmcnt(0)
	v_add_u32_e32 v83, 0x12000, v225
	buffer_store_dwordx4 v[112:115], v83, s[24:27], 0 offen nt
	v_add_u32_e32 v82, 0x15000, v225
	buffer_store_dwordx4 v[220:223], v82, s[24:27], 0 offen nt
	ds_write_b128 v235, v[60:63]
	v_fma_mix_f32 v218, v60, 1.0, 0 op_sel_hi:[1,0,0]
	v_fma_mix_f32 v219, v60, v60, 0 op_sel_hi:[1,1,0]
	v_fma_mix_f32 v218, v60, 1.0, v218 op_sel:[1,0,0] op_sel_hi:[1,0,0]
	v_fma_mix_f32 v219, v60, v60, v219 op_sel:[1,1,0] op_sel_hi:[1,1,0]
	v_fma_mix_f32 v218, v61, 1.0, v218 op_sel_hi:[1,0,0]
	v_fma_mix_f32 v219, v61, v61, v219 op_sel_hi:[1,1,0]
	v_fma_mix_f32 v218, v61, 1.0, v218 op_sel:[1,0,0] op_sel_hi:[1,0,0]
	v_fma_mix_f32 v219, v61, v61, v219 op_sel:[1,1,0] op_sel_hi:[1,1,0]
	v_fma_mix_f32 v218, v62, 1.0, v218 op_sel_hi:[1,0,0]
	v_fma_mix_f32 v219, v62, v62, v219 op_sel_hi:[1,1,0]
	v_fma_mix_f32 v218, v62, 1.0, v218 op_sel:[1,0,0] op_sel_hi:[1,0,0]
	v_fma_mix_f32 v219, v62, v62, v219 op_sel:[1,1,0] op_sel_hi:[1,1,0]
	v_fma_mix_f32 v218, v63, 1.0, v218 op_sel_hi:[1,0,0]
	v_fma_mix_f32 v219, v63, v63, v219 op_sel_hi:[1,1,0]
	v_fma_mix_f32 v218, v63, 1.0, v218 op_sel:[1,0,0] op_sel_hi:[1,0,0]
	v_fma_mix_f32 v219, v63, v63, v219 op_sel:[1,1,0] op_sel_hi:[1,1,0]
	s_waitcnt vmcnt(14)
	v_cvt_f32_f16_e32 v72, v148
	v_cvt_f32_f16_sdwa v73, v148 dst_sel:DWORD dst_unused:UNUSED_PAD src0_sel:WORD_1
	v_cvt_f32_f16_e32 v74, v149
	v_cvt_f32_f16_sdwa v75, v149 dst_sel:DWORD dst_unused:UNUSED_PAD src0_sel:WORD_1
	v_cvt_f32_f16_e32 v80, v150
	v_cvt_f32_f16_sdwa v81, v150 dst_sel:DWORD dst_unused:UNUSED_PAD src0_sel:WORD_1
	v_cvt_f32_f16_e32 v82, v151
	v_cvt_f32_f16_sdwa v83, v151 dst_sel:DWORD dst_unused:UNUSED_PAD src0_sel:WORD_1
	v_sub_f32_e32 v72, v72, v198
	v_sub_f32_e32 v73, v73, v198
	v_sub_f32_e32 v74, v74, v198
	v_sub_f32_e32 v75, v75, v198
	v_sub_f32_e32 v80, v80, v198
	v_sub_f32_e32 v81, v81, v198
	v_sub_f32_e32 v82, v82, v198
	v_sub_f32_e32 v83, v83, v198
	v_pk_mul_f32 v[72:73], v[198:199], v[72:73] op_sel:[1,0]
	v_pk_mul_f32 v[74:75], v[198:199], v[74:75] op_sel:[1,0]
	v_pk_mul_f32 v[80:81], v[198:199], v[80:81] op_sel:[1,0]
	v_pk_mul_f32 v[82:83], v[198:199], v[82:83] op_sel:[1,0]
	v_pk_fma_f32 v[52:53], v[72:73], v[168:169], v[52:53]
	v_pk_fma_f32 v[54:55], v[74:75], v[170:171], v[54:55]
	v_pk_fma_f32 v[48:49], v[80:81], v[172:173], v[48:49]
	v_pk_fma_f32 v[50:51], v[82:83], v[174:175], v[50:51]
	v_cvt_pk_f16_f32 v52, v52, v53
	v_cvt_pk_f16_f32 v53, v54, v55
	v_cvt_pk_f16_f32 v54, v48, v49
	v_cvt_pk_f16_f32 v55, v50, v51
	ds_write_b128 v235, v[52:55] offset:64
	v_fma_mix_f32 v218, v52, 1.0, v218 op_sel_hi:[1,0,0]
	v_fma_mix_f32 v219, v52, v52, v219 op_sel_hi:[1,1,0]
	v_fma_mix_f32 v218, v52, 1.0, v218 op_sel:[1,0,0] op_sel_hi:[1,0,0]
	v_fma_mix_f32 v219, v52, v52, v219 op_sel:[1,1,0] op_sel_hi:[1,1,0]
	v_fma_mix_f32 v218, v53, 1.0, v218 op_sel_hi:[1,0,0]
	v_fma_mix_f32 v219, v53, v53, v219 op_sel_hi:[1,1,0]
	v_fma_mix_f32 v218, v53, 1.0, v218 op_sel:[1,0,0] op_sel_hi:[1,0,0]
	v_fma_mix_f32 v219, v53, v53, v219 op_sel:[1,1,0] op_sel_hi:[1,1,0]
	v_fma_mix_f32 v218, v54, 1.0, v218 op_sel_hi:[1,0,0]
	v_fma_mix_f32 v219, v54, v54, v219 op_sel_hi:[1,1,0]
	v_fma_mix_f32 v218, v54, 1.0, v218 op_sel:[1,0,0] op_sel_hi:[1,0,0]
	v_fma_mix_f32 v219, v54, v54, v219 op_sel:[1,1,0] op_sel_hi:[1,1,0]
	v_fma_mix_f32 v218, v55, 1.0, v218 op_sel_hi:[1,0,0]
	v_fma_mix_f32 v219, v55, v55, v219 op_sel_hi:[1,1,0]
	v_fma_mix_f32 v218, v55, 1.0, v218 op_sel:[1,0,0] op_sel_hi:[1,0,0]
	v_fma_mix_f32 v219, v55, v55, v219 op_sel:[1,1,0] op_sel_hi:[1,1,0]
	ds_read_b128 v[124:127], v236
	ds_read_b128 v[116:119], v236 offset:1152
	s_waitcnt vmcnt(13)
	v_cvt_f32_f16_e32 v72, v152
	v_cvt_f32_f16_sdwa v73, v152 dst_sel:DWORD dst_unused:UNUSED_PAD src0_sel:WORD_1
	v_cvt_f32_f16_e32 v74, v153
	v_cvt_f32_f16_sdwa v75, v153 dst_sel:DWORD dst_unused:UNUSED_PAD src0_sel:WORD_1
	v_cvt_f32_f16_e32 v80, v154
	v_cvt_f32_f16_sdwa v81, v154 dst_sel:DWORD dst_unused:UNUSED_PAD src0_sel:WORD_1
	v_cvt_f32_f16_e32 v82, v155
	v_cvt_f32_f16_sdwa v83, v155 dst_sel:DWORD dst_unused:UNUSED_PAD src0_sel:WORD_1
	v_sub_f32_e32 v72, v72, v200
	v_sub_f32_e32 v73, v73, v200
	v_sub_f32_e32 v74, v74, v200
	v_sub_f32_e32 v75, v75, v200
	v_sub_f32_e32 v80, v80, v200
	v_sub_f32_e32 v81, v81, v200
	v_sub_f32_e32 v82, v82, v200
	v_sub_f32_e32 v83, v83, v200
	v_pk_mul_f32 v[72:73], v[200:201], v[72:73] op_sel:[1,0]
	v_pk_mul_f32 v[74:75], v[200:201], v[74:75] op_sel:[1,0]
	v_pk_mul_f32 v[80:81], v[200:201], v[80:81] op_sel:[1,0]
	v_pk_mul_f32 v[82:83], v[200:201], v[82:83] op_sel:[1,0]
	v_pk_fma_f32 v[44:45], v[72:73], v[160:161], v[44:45]
	v_pk_fma_f32 v[46:47], v[74:75], v[162:163], v[46:47]
	v_pk_fma_f32 v[40:41], v[80:81], v[164:165], v[40:41]
	v_pk_fma_f32 v[42:43], v[82:83], v[166:167], v[42:43]
	v_cvt_pk_f16_f32 v44, v44, v45
	v_cvt_pk_f16_f32 v45, v46, v47
	v_cvt_pk_f16_f32 v46, v40, v41
	v_cvt_pk_f16_f32 v47, v42, v43
	s_waitcnt lgkmcnt(0)
	v_add_u32_e32 v83, 0x30000, v225
	buffer_store_dwordx4 v[124:127], v83, s[24:27], 0 offen nt
	v_add_u32_e32 v82, 0x33000, v225
	buffer_store_dwordx4 v[116:119], v82, s[24:27], 0 offen nt
	ds_write_b128 v235, v[44:47]
	v_fma_mix_f32 v208, v44, 1.0, 0 op_sel_hi:[1,0,0]
	v_fma_mix_f32 v209, v44, v44, 0 op_sel_hi:[1,1,0]
	v_fma_mix_f32 v208, v44, 1.0, v208 op_sel:[1,0,0] op_sel_hi:[1,0,0]
	v_fma_mix_f32 v209, v44, v44, v209 op_sel:[1,1,0] op_sel_hi:[1,1,0]
	v_fma_mix_f32 v208, v45, 1.0, v208 op_sel_hi:[1,0,0]
	v_fma_mix_f32 v209, v45, v45, v209 op_sel_hi:[1,1,0]
	v_fma_mix_f32 v208, v45, 1.0, v208 op_sel:[1,0,0] op_sel_hi:[1,0,0]
	v_fma_mix_f32 v209, v45, v45, v209 op_sel:[1,1,0] op_sel_hi:[1,1,0]
	v_fma_mix_f32 v208, v46, 1.0, v208 op_sel_hi:[1,0,0]
	v_fma_mix_f32 v209, v46, v46, v209 op_sel_hi:[1,1,0]
	v_fma_mix_f32 v208, v46, 1.0, v208 op_sel:[1,0,0] op_sel_hi:[1,0,0]
	v_fma_mix_f32 v209, v46, v46, v209 op_sel:[1,1,0] op_sel_hi:[1,1,0]
	v_fma_mix_f32 v208, v47, 1.0, v208 op_sel_hi:[1,0,0]
	v_fma_mix_f32 v209, v47, v47, v209 op_sel_hi:[1,1,0]
	v_fma_mix_f32 v208, v47, 1.0, v208 op_sel:[1,0,0] op_sel_hi:[1,0,0]
	v_fma_mix_f32 v209, v47, v47, v209 op_sel:[1,1,0] op_sel_hi:[1,1,0]
	s_waitcnt vmcnt(14)
	v_cvt_f32_f16_e32 v72, v156
	v_cvt_f32_f16_sdwa v73, v156 dst_sel:DWORD dst_unused:UNUSED_PAD src0_sel:WORD_1
	v_cvt_f32_f16_e32 v74, v157
	v_cvt_f32_f16_sdwa v75, v157 dst_sel:DWORD dst_unused:UNUSED_PAD src0_sel:WORD_1
	v_cvt_f32_f16_e32 v80, v158
	v_cvt_f32_f16_sdwa v81, v158 dst_sel:DWORD dst_unused:UNUSED_PAD src0_sel:WORD_1
	v_cvt_f32_f16_e32 v82, v159
	v_cvt_f32_f16_sdwa v83, v159 dst_sel:DWORD dst_unused:UNUSED_PAD src0_sel:WORD_1
	v_sub_f32_e32 v72, v72, v200
	v_sub_f32_e32 v73, v73, v200
	v_sub_f32_e32 v74, v74, v200
	v_sub_f32_e32 v75, v75, v200
	v_sub_f32_e32 v80, v80, v200
	v_sub_f32_e32 v81, v81, v200
	v_sub_f32_e32 v82, v82, v200
	v_sub_f32_e32 v83, v83, v200
	v_pk_mul_f32 v[72:73], v[200:201], v[72:73] op_sel:[1,0]
	v_pk_mul_f32 v[74:75], v[200:201], v[74:75] op_sel:[1,0]
	v_pk_mul_f32 v[80:81], v[200:201], v[80:81] op_sel:[1,0]
	v_pk_mul_f32 v[82:83], v[200:201], v[82:83] op_sel:[1,0]
	v_pk_fma_f32 v[36:37], v[72:73], v[168:169], v[36:37]
	v_pk_fma_f32 v[38:39], v[74:75], v[170:171], v[38:39]
	v_pk_fma_f32 v[32:33], v[80:81], v[172:173], v[32:33]
	v_pk_fma_f32 v[34:35], v[82:83], v[174:175], v[34:35]
	v_cvt_pk_f16_f32 v36, v36, v37
	v_cvt_pk_f16_f32 v37, v38, v39
	v_cvt_pk_f16_f32 v38, v32, v33
	v_cvt_pk_f16_f32 v39, v34, v35
	ds_write_b128 v235, v[36:39] offset:64
	v_fma_mix_f32 v208, v36, 1.0, v208 op_sel_hi:[1,0,0]
	v_fma_mix_f32 v209, v36, v36, v209 op_sel_hi:[1,1,0]
	v_fma_mix_f32 v208, v36, 1.0, v208 op_sel:[1,0,0] op_sel_hi:[1,0,0]
	v_fma_mix_f32 v209, v36, v36, v209 op_sel:[1,1,0] op_sel_hi:[1,1,0]
	v_fma_mix_f32 v208, v37, 1.0, v208 op_sel_hi:[1,0,0]
	v_fma_mix_f32 v209, v37, v37, v209 op_sel_hi:[1,1,0]
	v_fma_mix_f32 v208, v37, 1.0, v208 op_sel:[1,0,0] op_sel_hi:[1,0,0]
	v_fma_mix_f32 v209, v37, v37, v209 op_sel:[1,1,0] op_sel_hi:[1,1,0]
	v_fma_mix_f32 v208, v38, 1.0, v208 op_sel_hi:[1,0,0]
	v_fma_mix_f32 v209, v38, v38, v209 op_sel_hi:[1,1,0]
	v_fma_mix_f32 v208, v38, 1.0, v208 op_sel:[1,0,0] op_sel_hi:[1,0,0]
	v_fma_mix_f32 v209, v38, v38, v209 op_sel:[1,1,0] op_sel_hi:[1,1,0]
	v_fma_mix_f32 v208, v39, 1.0, v208 op_sel_hi:[1,0,0]
	v_fma_mix_f32 v209, v39, v39, v209 op_sel_hi:[1,1,0]
	v_fma_mix_f32 v208, v39, 1.0, v208 op_sel:[1,0,0] op_sel_hi:[1,0,0]
	v_fma_mix_f32 v209, v39, v39, v209 op_sel:[1,1,0] op_sel_hi:[1,1,0]
	ds_read_b128 v[128:131], v236
	ds_read_b128 v[104:107], v236 offset:1152
	s_waitcnt vmcnt(11)
	v_cvt_f32_f16_e32 v72, v212
	v_cvt_f32_f16_sdwa v73, v212 dst_sel:DWORD dst_unused:UNUSED_PAD src0_sel:WORD_1
	v_cvt_f32_f16_e32 v74, v213
	v_cvt_f32_f16_sdwa v75, v213 dst_sel:DWORD dst_unused:UNUSED_PAD src0_sel:WORD_1
	v_cvt_f32_f16_e32 v80, v214
	v_cvt_f32_f16_sdwa v81, v214 dst_sel:DWORD dst_unused:UNUSED_PAD src0_sel:WORD_1
	v_cvt_f32_f16_e32 v82, v215
	v_cvt_f32_f16_sdwa v83, v215 dst_sel:DWORD dst_unused:UNUSED_PAD src0_sel:WORD_1
	v_sub_f32_e32 v72, v72, v202
	v_sub_f32_e32 v73, v73, v202
	v_sub_f32_e32 v74, v74, v202
	v_sub_f32_e32 v75, v75, v202
	v_sub_f32_e32 v80, v80, v202
	v_sub_f32_e32 v81, v81, v202
	v_sub_f32_e32 v82, v82, v202
	v_sub_f32_e32 v83, v83, v202
	v_pk_mul_f32 v[72:73], v[202:203], v[72:73] op_sel:[1,0]
	v_pk_mul_f32 v[74:75], v[202:203], v[74:75] op_sel:[1,0]
	v_pk_mul_f32 v[80:81], v[202:203], v[80:81] op_sel:[1,0]
	v_pk_mul_f32 v[82:83], v[202:203], v[82:83] op_sel:[1,0]
	v_pk_fma_f32 v[28:29], v[72:73], v[160:161], v[28:29]
	v_pk_fma_f32 v[30:31], v[74:75], v[162:163], v[30:31]
	v_pk_fma_f32 v[24:25], v[80:81], v[164:165], v[24:25]
	v_pk_fma_f32 v[26:27], v[82:83], v[166:167], v[26:27]
	v_cvt_pk_f16_f32 v28, v28, v29
	v_cvt_pk_f16_f32 v29, v30, v31
	v_cvt_pk_f16_f32 v30, v24, v25
	v_cvt_pk_f16_f32 v31, v26, v27
	s_waitcnt lgkmcnt(0)
	v_add_u32_e32 v83, 0x36000, v225
	buffer_store_dwordx4 v[128:131], v83, s[24:27], 0 offen nt
	v_add_u32_e32 v82, 0x39000, v225
	buffer_store_dwordx4 v[104:107], v82, s[24:27], 0 offen nt
	ds_write_b128 v235, v[28:31]
	v_fma_mix_f32 v210, v28, 1.0, 0 op_sel_hi:[1,0,0]
	v_fma_mix_f32 v211, v28, v28, 0 op_sel_hi:[1,1,0]
	v_fma_mix_f32 v210, v28, 1.0, v210 op_sel:[1,0,0] op_sel_hi:[1,0,0]
	v_fma_mix_f32 v211, v28, v28, v211 op_sel:[1,1,0] op_sel_hi:[1,1,0]
	v_fma_mix_f32 v210, v29, 1.0, v210 op_sel_hi:[1,0,0]
	v_fma_mix_f32 v211, v29, v29, v211 op_sel_hi:[1,1,0]
	v_fma_mix_f32 v210, v29, 1.0, v210 op_sel:[1,0,0] op_sel_hi:[1,0,0]
	v_fma_mix_f32 v211, v29, v29, v211 op_sel:[1,1,0] op_sel_hi:[1,1,0]
	v_fma_mix_f32 v210, v30, 1.0, v210 op_sel_hi:[1,0,0]
	v_fma_mix_f32 v211, v30, v30, v211 op_sel_hi:[1,1,0]
	v_fma_mix_f32 v210, v30, 1.0, v210 op_sel:[1,0,0] op_sel_hi:[1,0,0]
	v_fma_mix_f32 v211, v30, v30, v211 op_sel:[1,1,0] op_sel_hi:[1,1,0]
	v_fma_mix_f32 v210, v31, 1.0, v210 op_sel_hi:[1,0,0]
	v_fma_mix_f32 v211, v31, v31, v211 op_sel_hi:[1,1,0]
	v_fma_mix_f32 v210, v31, 1.0, v210 op_sel:[1,0,0] op_sel_hi:[1,0,0]
	v_fma_mix_f32 v211, v31, v31, v211 op_sel:[1,1,0] op_sel_hi:[1,1,0]
	s_waitcnt vmcnt(12)
	v_cvt_f32_f16_e32 v72, v144
	v_cvt_f32_f16_sdwa v73, v144 dst_sel:DWORD dst_unused:UNUSED_PAD src0_sel:WORD_1
	v_cvt_f32_f16_e32 v74, v145
	v_cvt_f32_f16_sdwa v75, v145 dst_sel:DWORD dst_unused:UNUSED_PAD src0_sel:WORD_1
	v_cvt_f32_f16_e32 v80, v146
	v_cvt_f32_f16_sdwa v81, v146 dst_sel:DWORD dst_unused:UNUSED_PAD src0_sel:WORD_1
	v_cvt_f32_f16_e32 v82, v147
	v_cvt_f32_f16_sdwa v83, v147 dst_sel:DWORD dst_unused:UNUSED_PAD src0_sel:WORD_1
	v_sub_f32_e32 v72, v72, v202
	v_sub_f32_e32 v73, v73, v202
	v_sub_f32_e32 v74, v74, v202
	v_sub_f32_e32 v75, v75, v202
	v_sub_f32_e32 v80, v80, v202
	v_sub_f32_e32 v81, v81, v202
	v_sub_f32_e32 v82, v82, v202
	v_sub_f32_e32 v83, v83, v202
	v_pk_mul_f32 v[72:73], v[202:203], v[72:73] op_sel:[1,0]
	v_pk_mul_f32 v[74:75], v[202:203], v[74:75] op_sel:[1,0]
	v_pk_mul_f32 v[80:81], v[202:203], v[80:81] op_sel:[1,0]
	v_pk_mul_f32 v[82:83], v[202:203], v[82:83] op_sel:[1,0]
	v_pk_fma_f32 v[20:21], v[72:73], v[168:169], v[20:21]
	v_pk_fma_f32 v[22:23], v[74:75], v[170:171], v[22:23]
	v_pk_fma_f32 v[16:17], v[80:81], v[172:173], v[16:17]
	v_pk_fma_f32 v[18:19], v[82:83], v[174:175], v[18:19]
	v_cvt_pk_f16_f32 v20, v20, v21
	v_cvt_pk_f16_f32 v21, v22, v23
	v_cvt_pk_f16_f32 v22, v16, v17
	v_cvt_pk_f16_f32 v23, v18, v19
	ds_write_b128 v235, v[20:23] offset:64
	v_fma_mix_f32 v210, v20, 1.0, v210 op_sel_hi:[1,0,0]
	v_fma_mix_f32 v211, v20, v20, v211 op_sel_hi:[1,1,0]
	v_fma_mix_f32 v210, v20, 1.0, v210 op_sel:[1,0,0] op_sel_hi:[1,0,0]
	v_fma_mix_f32 v211, v20, v20, v211 op_sel:[1,1,0] op_sel_hi:[1,1,0]
	v_fma_mix_f32 v210, v21, 1.0, v210 op_sel_hi:[1,0,0]
	v_fma_mix_f32 v211, v21, v21, v211 op_sel_hi:[1,1,0]
	v_fma_mix_f32 v210, v21, 1.0, v210 op_sel:[1,0,0] op_sel_hi:[1,0,0]
	v_fma_mix_f32 v211, v21, v21, v211 op_sel:[1,1,0] op_sel_hi:[1,1,0]
	v_fma_mix_f32 v210, v22, 1.0, v210 op_sel_hi:[1,0,0]
	v_fma_mix_f32 v211, v22, v22, v211 op_sel_hi:[1,1,0]
	v_fma_mix_f32 v210, v22, 1.0, v210 op_sel:[1,0,0] op_sel_hi:[1,0,0]
	v_fma_mix_f32 v211, v22, v22, v211 op_sel:[1,1,0] op_sel_hi:[1,1,0]
	v_fma_mix_f32 v210, v23, 1.0, v210 op_sel_hi:[1,0,0]
	v_fma_mix_f32 v211, v23, v23, v211 op_sel_hi:[1,1,0]
	v_fma_mix_f32 v210, v23, 1.0, v210 op_sel:[1,0,0] op_sel_hi:[1,0,0]
	v_fma_mix_f32 v211, v23, v23, v211 op_sel:[1,1,0] op_sel_hi:[1,1,0]
	ds_read_b128 v[240:243], v236
	ds_read_b128 v[96:99], v236 offset:1152
	s_waitcnt vmcnt(11)
	v_cvt_f32_f16_e32 v72, v132
	v_cvt_f32_f16_sdwa v73, v132 dst_sel:DWORD dst_unused:UNUSED_PAD src0_sel:WORD_1
	v_cvt_f32_f16_e32 v74, v133
	v_cvt_f32_f16_sdwa v75, v133 dst_sel:DWORD dst_unused:UNUSED_PAD src0_sel:WORD_1
	v_cvt_f32_f16_e32 v80, v134
	v_cvt_f32_f16_sdwa v81, v134 dst_sel:DWORD dst_unused:UNUSED_PAD src0_sel:WORD_1
	v_cvt_f32_f16_e32 v82, v135
	v_cvt_f32_f16_sdwa v83, v135 dst_sel:DWORD dst_unused:UNUSED_PAD src0_sel:WORD_1
	v_sub_f32_e32 v72, v72, v204
	v_sub_f32_e32 v73, v73, v204
	v_sub_f32_e32 v74, v74, v204
	v_sub_f32_e32 v75, v75, v204
	v_sub_f32_e32 v80, v80, v204
	v_sub_f32_e32 v81, v81, v204
	v_sub_f32_e32 v82, v82, v204
	v_sub_f32_e32 v83, v83, v204
	v_pk_mul_f32 v[72:73], v[204:205], v[72:73] op_sel:[1,0]
	v_pk_mul_f32 v[74:75], v[204:205], v[74:75] op_sel:[1,0]
	v_pk_mul_f32 v[80:81], v[204:205], v[80:81] op_sel:[1,0]
	v_pk_mul_f32 v[82:83], v[204:205], v[82:83] op_sel:[1,0]
	v_pk_fma_f32 v[12:13], v[72:73], v[160:161], v[12:13]
	v_pk_fma_f32 v[14:15], v[74:75], v[162:163], v[14:15]
	v_pk_fma_f32 v[8:9], v[80:81], v[164:165], v[8:9]
	v_pk_fma_f32 v[10:11], v[82:83], v[166:167], v[10:11]
	v_cvt_pk_f16_f32 v12, v12, v13
	v_cvt_pk_f16_f32 v13, v14, v15
	v_cvt_pk_f16_f32 v14, v8, v9
	v_cvt_pk_f16_f32 v15, v10, v11
	s_waitcnt lgkmcnt(0)
	v_add_u32_e32 v83, 0x3c000, v225
	buffer_store_dwordx4 v[240:243], v83, s[24:27], 0 offen nt
	v_add_u32_e32 v82, 0x3f000, v225
	buffer_store_dwordx4 v[96:99], v82, s[24:27], 0 offen nt
	ds_write_b128 v235, v[12:15]
	v_fma_mix_f32 v244, v12, 1.0, 0 op_sel_hi:[1,0,0]
	v_fma_mix_f32 v245, v12, v12, 0 op_sel_hi:[1,1,0]
	v_fma_mix_f32 v244, v12, 1.0, v244 op_sel:[1,0,0] op_sel_hi:[1,0,0]
	v_fma_mix_f32 v245, v12, v12, v245 op_sel:[1,1,0] op_sel_hi:[1,1,0]
	v_fma_mix_f32 v244, v13, 1.0, v244 op_sel_hi:[1,0,0]
	v_fma_mix_f32 v245, v13, v13, v245 op_sel_hi:[1,1,0]
	v_fma_mix_f32 v244, v13, 1.0, v244 op_sel:[1,0,0] op_sel_hi:[1,0,0]
	v_fma_mix_f32 v245, v13, v13, v245 op_sel:[1,1,0] op_sel_hi:[1,1,0]
	v_fma_mix_f32 v244, v14, 1.0, v244 op_sel_hi:[1,0,0]
	v_fma_mix_f32 v245, v14, v14, v245 op_sel_hi:[1,1,0]
	v_fma_mix_f32 v244, v14, 1.0, v244 op_sel:[1,0,0] op_sel_hi:[1,0,0]
	v_fma_mix_f32 v245, v14, v14, v245 op_sel:[1,1,0] op_sel_hi:[1,1,0]
	v_fma_mix_f32 v244, v15, 1.0, v244 op_sel_hi:[1,0,0]
	v_fma_mix_f32 v245, v15, v15, v245 op_sel_hi:[1,1,0]
	v_fma_mix_f32 v244, v15, 1.0, v244 op_sel:[1,0,0] op_sel_hi:[1,0,0]
	v_fma_mix_f32 v245, v15, v15, v245 op_sel:[1,1,0] op_sel_hi:[1,1,0]
	s_waitcnt vmcnt(12)
	v_cvt_f32_f16_e32 v72, v88
	v_cvt_f32_f16_sdwa v73, v88 dst_sel:DWORD dst_unused:UNUSED_PAD src0_sel:WORD_1
	v_cvt_f32_f16_e32 v74, v89
	v_cvt_f32_f16_sdwa v75, v89 dst_sel:DWORD dst_unused:UNUSED_PAD src0_sel:WORD_1
	v_cvt_f32_f16_e32 v80, v90
	v_cvt_f32_f16_sdwa v81, v90 dst_sel:DWORD dst_unused:UNUSED_PAD src0_sel:WORD_1
	v_cvt_f32_f16_e32 v82, v91
	v_cvt_f32_f16_sdwa v83, v91 dst_sel:DWORD dst_unused:UNUSED_PAD src0_sel:WORD_1
	v_sub_f32_e32 v72, v72, v204
	v_sub_f32_e32 v73, v73, v204
	v_sub_f32_e32 v74, v74, v204
	v_sub_f32_e32 v75, v75, v204
	v_sub_f32_e32 v80, v80, v204
	v_sub_f32_e32 v81, v81, v204
	v_sub_f32_e32 v82, v82, v204
	v_sub_f32_e32 v83, v83, v204
	v_pk_mul_f32 v[72:73], v[204:205], v[72:73] op_sel:[1,0]
	v_pk_mul_f32 v[74:75], v[204:205], v[74:75] op_sel:[1,0]
	v_pk_mul_f32 v[80:81], v[204:205], v[80:81] op_sel:[1,0]
	v_pk_mul_f32 v[82:83], v[204:205], v[82:83] op_sel:[1,0]
	v_pk_fma_f32 v[4:5], v[72:73], v[168:169], v[4:5]
	v_pk_fma_f32 v[6:7], v[74:75], v[170:171], v[6:7]
	v_pk_fma_f32 v[0:1], v[80:81], v[172:173], v[0:1]
	v_pk_fma_f32 v[2:3], v[82:83], v[174:175], v[2:3]
	v_cvt_pk_f16_f32 v4, v4, v5
	v_cvt_pk_f16_f32 v5, v6, v7
	v_cvt_pk_f16_f32 v6, v0, v1
	v_cvt_pk_f16_f32 v7, v2, v3
	ds_write_b128 v235, v[4:7] offset:64
	v_fma_mix_f32 v244, v4, 1.0, v244 op_sel_hi:[1,0,0]
	v_fma_mix_f32 v245, v4, v4, v245 op_sel_hi:[1,1,0]
	v_fma_mix_f32 v244, v4, 1.0, v244 op_sel:[1,0,0] op_sel_hi:[1,0,0]
	v_fma_mix_f32 v245, v4, v4, v245 op_sel:[1,1,0] op_sel_hi:[1,1,0]
	v_fma_mix_f32 v244, v5, 1.0, v244 op_sel_hi:[1,0,0]
	v_fma_mix_f32 v245, v5, v5, v245 op_sel_hi:[1,1,0]
	v_fma_mix_f32 v244, v5, 1.0, v244 op_sel:[1,0,0] op_sel_hi:[1,0,0]
	v_fma_mix_f32 v245, v5, v5, v245 op_sel:[1,1,0] op_sel_hi:[1,1,0]
	v_fma_mix_f32 v244, v6, 1.0, v244 op_sel_hi:[1,0,0]
	v_fma_mix_f32 v245, v6, v6, v245 op_sel_hi:[1,1,0]
	v_fma_mix_f32 v244, v6, 1.0, v244 op_sel:[1,0,0] op_sel_hi:[1,0,0]
	v_fma_mix_f32 v245, v6, v6, v245 op_sel:[1,1,0] op_sel_hi:[1,1,0]
	v_fma_mix_f32 v244, v7, 1.0, v244 op_sel_hi:[1,0,0]
	v_fma_mix_f32 v245, v7, v7, v245 op_sel_hi:[1,1,0]
	v_fma_mix_f32 v244, v7, 1.0, v244 op_sel:[1,0,0] op_sel_hi:[1,0,0]
	v_fma_mix_f32 v245, v7, v7, v245 op_sel:[1,1,0] op_sel_hi:[1,1,0]
	ds_read_b128 v[108:111], v236
	ds_read_b128 v[100:103], v236 offset:1152
	s_waitcnt lgkmcnt(0)
	v_add_u32_e32 v83, 0x42000, v225
	buffer_store_dwordx4 v[108:111], v83, s[24:27], 0 offen nt
	v_add_u32_e32 v82, 0x45000, v225
	buffer_store_dwordx4 v[100:103], v82, s[24:27], 0 offen nt
	v_xor_b32_e32 v246, 16, v234
	v_lshlrev_b32_e32 v246, 2, v246
	v_xor_b32_e32 v247, 32, v234
	v_lshlrev_b32_e32 v247, 2, v247
	ds_bpermute_b32 v92, v246, v206
	ds_bpermute_b32 v93, v246, v207
	ds_bpermute_b32 v94, v246, v140
	ds_bpermute_b32 v95, v246, v141
	ds_bpermute_b32 v120, v246, v142
	ds_bpermute_b32 v121, v246, v143
	ds_bpermute_b32 v122, v246, v216
	ds_bpermute_b32 v123, v246, v217
	s_waitcnt lgkmcnt(0)
	v_pk_add_f32 v[206:207], v[206:207], v[92:93]
	v_pk_add_f32 v[140:141], v[140:141], v[94:95]
	v_pk_add_f32 v[142:143], v[142:143], v[120:121]
	v_pk_add_f32 v[216:217], v[216:217], v[122:123]
	ds_bpermute_b32 v92, v246, v218
	ds_bpermute_b32 v93, v246, v219
	ds_bpermute_b32 v94, v246, v208
	ds_bpermute_b32 v95, v246, v209
	ds_bpermute_b32 v120, v246, v210
	ds_bpermute_b32 v121, v246, v211
	ds_bpermute_b32 v122, v246, v244
	ds_bpermute_b32 v123, v246, v245
	s_waitcnt lgkmcnt(0)
	v_pk_add_f32 v[218:219], v[218:219], v[92:93]
	v_pk_add_f32 v[208:209], v[208:209], v[94:95]
	v_pk_add_f32 v[210:211], v[210:211], v[120:121]
	v_pk_add_f32 v[244:245], v[244:245], v[122:123]
	ds_bpermute_b32 v92, v247, v206
	ds_bpermute_b32 v93, v247, v207
	ds_bpermute_b32 v94, v247, v140
	ds_bpermute_b32 v95, v247, v141
	ds_bpermute_b32 v120, v247, v142
	ds_bpermute_b32 v121, v247, v143
	ds_bpermute_b32 v122, v247, v216
	ds_bpermute_b32 v123, v247, v217
	s_waitcnt lgkmcnt(0)
	v_pk_add_f32 v[206:207], v[206:207], v[92:93]
	v_pk_add_f32 v[140:141], v[140:141], v[94:95]
	v_pk_add_f32 v[142:143], v[142:143], v[120:121]
	v_pk_add_f32 v[216:217], v[216:217], v[122:123]
	ds_bpermute_b32 v92, v247, v218
	ds_bpermute_b32 v93, v247, v219
	ds_bpermute_b32 v94, v247, v208
	ds_bpermute_b32 v95, v247, v209
	ds_bpermute_b32 v120, v247, v210
	ds_bpermute_b32 v121, v247, v211
	ds_bpermute_b32 v122, v247, v244
	ds_bpermute_b32 v123, v247, v245
	s_waitcnt lgkmcnt(0)
	v_pk_add_f32 v[218:219], v[218:219], v[92:93]
	v_pk_add_f32 v[208:209], v[208:209], v[94:95]
	v_pk_add_f32 v[210:211], v[210:211], v[120:121]
	v_pk_add_f32 v[244:245], v[244:245], v[122:123]
	s_mov_b64 exec, 0xffff
	global_store_dwordx2 v224, v[206:207], s[100:101] offset:-2048
	global_store_dwordx2 v224, v[140:141], s[100:101] offset:-512
	global_store_dwordx2 v224, v[142:143], s[100:101] offset:1024
	global_store_dwordx2 v224, v[216:217], s[100:101] offset:2560
	s_add_u32 s100, s100, 0x3000
	s_addc_u32 s101, s101, 0
	global_store_dwordx2 v224, v[218:219], s[100:101] offset:-2048
	global_store_dwordx2 v224, v[208:209], s[100:101] offset:-512
	global_store_dwordx2 v224, v[210:211], s[100:101] offset:1024
	global_store_dwordx2 v224, v[244:245], s[100:101] offset:2560
	s_mov_b64 exec, -1
	s_mov_b32 s83, s81
	s_mov_b32 s84, s82
	s_mov_b64 s[40:41], s[0:1]
	s_mov_b64 s[38:39], s[8:9]
	s_mov_b64 vcc, s[6:7]
	s_cbranch_vccz .LBB8_12
	s_waitcnt vmcnt(0)
	s_cmpk_gt_u32 s44, 0xff
	s_cbranch_scc1 .LBB8_31
	s_barrier

.LBB8_32:
	s_endpgm
	s_endpgm
	s_endpgm
	s_endpgm
	s_endpgm
	s_endpgm
	s_endpgm
	s_endpgm
	s_endpgm
	s_endpgm
	s_endpgm
	s_endpgm
	s_endpgm
	s_endpgm
	s_endpgm
	s_endpgm
	s_endpgm
	s_endpgm
	s_endpgm
	s_endpgm
	s_endpgm
	s_endpgm
	s_endpgm
	s_endpgm
	s_endpgm
	s_endpgm
	s_endpgm
	s_endpgm
	s_endpgm
	s_endpgm
	s_endpgm
	s_endpgm
	s_endpgm
	s_endpgm
	s_endpgm
	s_endpgm
	s_endpgm
	s_endpgm
	s_endpgm
	s_endpgm
	s_endpgm
	s_endpgm
	s_endpgm
	.section	.rodata,"a",@progbits
	.p2align	6, 0x0

.LBB10_27:
	ds_read_b128 v[72:75], v231
	ds_read_b128 v[80:83], v231 offset:1024
	ds_read_b128 v[88:91], v231 offset:2048
	ds_read_b128 v[92:95], v231 offset:3072
	s_add_u32 s40, s38, 0xfff40080
	s_addc_u32 s41, s39, -1
	s_cmp_eq_u32 s87, 44
	s_cselect_b32 s43, s9, s41
	s_cselect_b32 s42, s8, s40
	s_cselect_b32 s41, s1, s86
	s_cselect_b32 s40, s0, s85
	v_lshl_add_u64 v[190:191], s[38:39], 0, v[184:185]
	s_add_i32 m0, s51, 0xc000
	ds_read_b128 v[136:139], v232
	ds_read_b128 v[148:151], v232 offset:1024
	ds_read_b128 v[152:155], v232 offset:2048
	ds_read_b128 v[156:159], v232 offset:3072
	ds_read_b128 v[160:163], v232 offset:4096
	ds_read_b128 v[164:167], v232 offset:5120
	ds_read_b128 v[168:171], v232 offset:6144
	ds_read_b128 v[172:175], v232 offset:7168
	global_load_lds_dwordx4 v[190:191], off
	v_lshl_add_u64 v[190:191], s[38:39], 0, v[186:187]
	s_add_i32 m0, s51, 0xe000
	s_nop 0
	global_load_lds_dwordx4 v[190:191], off
	s_waitcnt lgkmcnt(8)
	s_barrier
	s_waitcnt lgkmcnt(0)
	s_setprio 1
	s_waitcnt lgkmcnt(0)
	v_mfma_f32_16x16x32_f16 v[144:147], v[72:75], v[136:139], v[144:147]
	v_mfma_f32_16x16x32_f16 v[140:143], v[88:91], v[136:139], v[140:143]
	v_mfma_f32_16x16x32_f16 v[124:127], v[72:75], v[152:155], v[124:127]
	v_mfma_f32_16x16x32_f16 v[120:123], v[88:91], v[152:155], v[120:123]
	v_mfma_f32_16x16x32_f16 v[108:111], v[72:75], v[160:163], v[108:111]
	v_mfma_f32_16x16x32_f16 v[104:107], v[88:91], v[160:163], v[104:107]
	v_mfma_f32_16x16x32_f16 v[84:87], v[72:75], v[168:171], v[84:87]
	v_mfma_f32_16x16x32_f16 v[76:79], v[88:91], v[168:171], v[76:79]
	v_mfma_f32_16x16x32_f16 v[144:147], v[80:83], v[148:151], v[144:147]
	v_mfma_f32_16x16x32_f16 v[140:143], v[92:95], v[148:151], v[140:143]
	v_mfma_f32_16x16x32_f16 v[124:127], v[80:83], v[156:159], v[124:127]
	v_mfma_f32_16x16x32_f16 v[120:123], v[92:95], v[156:159], v[120:123]
	v_mfma_f32_16x16x32_f16 v[108:111], v[80:83], v[164:167], v[108:111]
	v_mfma_f32_16x16x32_f16 v[104:107], v[92:95], v[164:167], v[104:107]
	v_mfma_f32_16x16x32_f16 v[84:87], v[80:83], v[172:175], v[84:87]
	v_mfma_f32_16x16x32_f16 v[76:79], v[92:95], v[172:175], v[76:79]
	s_setprio 0
	s_barrier
	s_add_i32 s88, s69, s50
	v_lshl_add_u64 v[206:207], s[40:41], 0, v[178:179]
	s_mov_b32 m0, s88
	ds_read_b128 v[190:193], v233
	ds_read_b128 v[194:197], v233 offset:1024
	ds_read_b128 v[198:201], v233 offset:2048
	ds_read_b128 v[202:205], v233 offset:3072
	global_load_lds_dwordx4 v[206:207], off
	v_lshl_add_u64 v[208:209], s[40:41], 0, v[182:183]
	s_add_i32 m0, s88, 0x2000
	s_nop 0
	global_load_lds_dwordx4 v[208:209], off
	s_barrier
	s_waitcnt lgkmcnt(0)
	s_setprio 1
	s_waitcnt lgkmcnt(0)
	v_mfma_f32_16x16x32_f16 v[132:135], v[190:193], v[136:139], v[132:135]
	v_mfma_f32_16x16x32_f16 v[128:131], v[198:201], v[136:139], v[128:131]
	v_mfma_f32_16x16x32_f16 v[116:119], v[190:193], v[152:155], v[116:119]
	v_mfma_f32_16x16x32_f16 v[112:115], v[198:201], v[152:155], v[112:115]
	v_mfma_f32_16x16x32_f16 v[100:103], v[190:193], v[160:163], v[100:103]
	v_mfma_f32_16x16x32_f16 v[96:99], v[198:201], v[160:163], v[96:99]
	v_mfma_f32_16x16x32_f16 v[68:71], v[190:193], v[168:171], v[68:71]
	v_mfma_f32_16x16x32_f16 v[64:67], v[198:201], v[168:171], v[64:67]
	v_mfma_f32_16x16x32_f16 v[132:135], v[194:197], v[148:151], v[132:135]
	v_mfma_f32_16x16x32_f16 v[128:131], v[202:205], v[148:151], v[128:131]
	v_mfma_f32_16x16x32_f16 v[116:119], v[194:197], v[156:159], v[116:119]
	v_mfma_f32_16x16x32_f16 v[112:115], v[202:205], v[156:159], v[112:115]
	v_mfma_f32_16x16x32_f16 v[100:103], v[194:197], v[164:167], v[100:103]
	v_mfma_f32_16x16x32_f16 v[96:99], v[202:205], v[164:167], v[96:99]
	v_mfma_f32_16x16x32_f16 v[68:71], v[194:197], v[172:175], v[68:71]
	v_mfma_f32_16x16x32_f16 v[64:67], v[202:205], v[172:175], v[64:67]
	s_setprio 0
	s_mov_b32 m0, s51
	v_lshl_add_u64 v[210:211], s[42:43], 0, v[176:177]
	s_barrier
	ds_read_b128 v[136:139], v232 offset:16384
	ds_read_b128 v[148:151], v232 offset:17408
	ds_read_b128 v[152:155], v232 offset:18432
	ds_read_b128 v[156:159], v232 offset:19456
	ds_read_b128 v[160:163], v232 offset:20480
	ds_read_b128 v[164:167], v232 offset:21504
	ds_read_b128 v[168:171], v232 offset:22528
	ds_read_b128 v[172:175], v232 offset:23552
	global_load_lds_dwordx4 v[210:211], off
	v_lshl_add_u64 v[212:213], s[42:43], 0, v[180:181]
	s_mov_b32 m0, s52
	s_nop 0
	global_load_lds_dwordx4 v[212:213], off
	s_barrier
	s_waitcnt lgkmcnt(0)
	s_setprio 1
	s_waitcnt lgkmcnt(0)
	v_mfma_f32_16x16x32_f16 v[60:63], v[72:75], v[136:139], v[60:63]
	v_mfma_f32_16x16x32_f16 v[56:59], v[88:91], v[136:139], v[56:59]
	v_mfma_f32_16x16x32_f16 v[44:47], v[72:75], v[152:155], v[44:47]
	v_mfma_f32_16x16x32_f16 v[40:43], v[88:91], v[152:155], v[40:43]
	v_mfma_f32_16x16x32_f16 v[28:31], v[72:75], v[160:163], v[28:31]
	v_mfma_f32_16x16x32_f16 v[24:27], v[88:91], v[160:163], v[24:27]
	v_mfma_f32_16x16x32_f16 v[12:15], v[72:75], v[168:171], v[12:15]
	v_mfma_f32_16x16x32_f16 v[8:11], v[88:91], v[168:171], v[8:11]
	v_mfma_f32_16x16x32_f16 v[60:63], v[80:83], v[148:151], v[60:63]
	v_mfma_f32_16x16x32_f16 v[56:59], v[92:95], v[148:151], v[56:59]
	v_mfma_f32_16x16x32_f16 v[44:47], v[80:83], v[156:159], v[44:47]
	v_mfma_f32_16x16x32_f16 v[40:43], v[92:95], v[156:159], v[40:43]
	v_mfma_f32_16x16x32_f16 v[28:31], v[80:83], v[164:167], v[28:31]
	v_mfma_f32_16x16x32_f16 v[24:27], v[92:95], v[164:167], v[24:27]
	v_mfma_f32_16x16x32_f16 v[12:15], v[80:83], v[172:175], v[12:15]
	v_mfma_f32_16x16x32_f16 v[8:11], v[92:95], v[172:175], v[8:11]
	s_setprio 0
	s_barrier
	s_add_u32 s88, s40, 0x30000
	s_addc_u32 s89, s41, 0
	s_add_i32 s90, s70, s50
	v_lshl_add_u64 v[72:73], s[88:89], 0, v[178:179]
	s_mov_b32 m0, s90
	s_nop 0
	global_load_lds_dwordx4 v[72:73], off
	v_lshl_add_u64 v[72:73], s[88:89], 0, v[182:183]
	s_add_i32 m0, s90, 0x2000
	s_nop 0
	global_load_lds_dwordx4 v[72:73], off
	s_waitcnt vmcnt(6)
	s_barrier
	s_setprio 1
	v_mfma_f32_16x16x32_f16 v[52:55], v[190:193], v[136:139], v[52:55]
	v_mfma_f32_16x16x32_f16 v[48:51], v[198:201], v[136:139], v[48:51]
	v_mfma_f32_16x16x32_f16 v[36:39], v[190:193], v[152:155], v[36:39]
	v_mfma_f32_16x16x32_f16 v[32:35], v[198:201], v[152:155], v[32:35]
	v_mfma_f32_16x16x32_f16 v[20:23], v[190:193], v[160:163], v[20:23]
	v_mfma_f32_16x16x32_f16 v[16:19], v[198:201], v[160:163], v[16:19]
	v_mfma_f32_16x16x32_f16 v[4:7], v[190:193], v[168:171], v[4:7]
	v_mfma_f32_16x16x32_f16 v[0:3], v[198:201], v[168:171], v[0:3]
	v_mfma_f32_16x16x32_f16 v[52:55], v[194:197], v[148:151], v[52:55]
	v_mfma_f32_16x16x32_f16 v[48:51], v[202:205], v[148:151], v[48:51]
	v_mfma_f32_16x16x32_f16 v[36:39], v[194:197], v[156:159], v[36:39]
	v_mfma_f32_16x16x32_f16 v[32:35], v[202:205], v[156:159], v[32:35]
	v_mfma_f32_16x16x32_f16 v[20:23], v[194:197], v[164:167], v[20:23]
	v_mfma_f32_16x16x32_f16 v[16:19], v[202:205], v[164:167], v[16:19]
	v_mfma_f32_16x16x32_f16 v[4:7], v[194:197], v[172:175], v[4:7]
	v_mfma_f32_16x16x32_f16 v[0:3], v[202:205], v[172:175], v[0:3]
	s_setprio 0
	s_add_i32 s88, 0, 0x18000
	v_add_u32_e32 v92, s88, v228
	s_barrier
	ds_read_b128 v[72:75], v92
	ds_read_b128 v[80:83], v92 offset:1024
	ds_read_b128 v[88:91], v92 offset:2048
	ds_read_b128 v[92:95], v92 offset:3072
	s_add_u32 s42, s42, 0xc0000
	s_addc_u32 s43, s43, 0
	s_mov_b32 m0, s53
	v_lshl_add_u64 v[190:191], s[42:43], 0, v[176:177]
	ds_read_b128 v[136:139], v232 offset:32768
	ds_read_b128 v[148:151], v232 offset:33792
	ds_read_b128 v[152:155], v232 offset:34816
	ds_read_b128 v[156:159], v232 offset:35840
	ds_read_b128 v[160:163], v232 offset:36864
	ds_read_b128 v[164:167], v232 offset:37888
	ds_read_b128 v[168:171], v232 offset:38912
	ds_read_b128 v[172:175], v232 offset:39936
	global_load_lds_dwordx4 v[190:191], off
	v_lshl_add_u64 v[190:191], s[42:43], 0, v[180:181]
	s_mov_b32 m0, s54
	s_nop 0
	global_load_lds_dwordx4 v[190:191], off
	s_waitcnt lgkmcnt(8)
	s_barrier
	s_waitcnt lgkmcnt(0)
	s_setprio 1
	s_waitcnt lgkmcnt(0)
	v_mfma_f32_16x16x32_f16 v[144:147], v[72:75], v[136:139], v[144:147]
	v_mfma_f32_16x16x32_f16 v[140:143], v[88:91], v[136:139], v[140:143]
	v_mfma_f32_16x16x32_f16 v[124:127], v[72:75], v[152:155], v[124:127]
	v_mfma_f32_16x16x32_f16 v[120:123], v[88:91], v[152:155], v[120:123]
	v_mfma_f32_16x16x32_f16 v[108:111], v[72:75], v[160:163], v[108:111]
	v_mfma_f32_16x16x32_f16 v[104:107], v[88:91], v[160:163], v[104:107]
	v_mfma_f32_16x16x32_f16 v[84:87], v[72:75], v[168:171], v[84:87]
	v_mfma_f32_16x16x32_f16 v[76:79], v[88:91], v[168:171], v[76:79]
	v_mfma_f32_16x16x32_f16 v[144:147], v[80:83], v[148:151], v[144:147]
	v_mfma_f32_16x16x32_f16 v[140:143], v[92:95], v[148:151], v[140:143]
	v_mfma_f32_16x16x32_f16 v[124:127], v[80:83], v[156:159], v[124:127]
	v_mfma_f32_16x16x32_f16 v[120:123], v[92:95], v[156:159], v[120:123]
	v_mfma_f32_16x16x32_f16 v[108:111], v[80:83], v[164:167], v[108:111]
	v_mfma_f32_16x16x32_f16 v[104:107], v[92:95], v[164:167], v[104:107]
	v_mfma_f32_16x16x32_f16 v[84:87], v[80:83], v[172:175], v[84:87]
	v_mfma_f32_16x16x32_f16 v[76:79], v[92:95], v[172:175], v[76:79]
	s_setprio 0
	s_barrier
	s_add_i32 s42, 0, 0x1c000
	s_add_i32 s43, s88, s50
	v_add_u32_e32 v202, s42, v228
	v_lshl_add_u64 v[206:207], v[206:207], 0, s[36:37]
	s_mov_b32 m0, s43
	ds_read_b128 v[190:193], v202
	ds_read_b128 v[194:197], v202 offset:1024
	ds_read_b128 v[198:201], v202 offset:2048
	ds_read_b128 v[202:205], v202 offset:3072
	global_load_lds_dwordx4 v[206:207], off
	v_lshl_add_u64 v[206:207], v[208:209], 0, s[36:37]
	s_add_i32 m0, s43, 0x2000
	s_nop 0
	global_load_lds_dwordx4 v[206:207], off
	s_barrier
	s_waitcnt lgkmcnt(0)
	s_setprio 1
	s_waitcnt lgkmcnt(0)
	v_mfma_f32_16x16x32_f16 v[132:135], v[190:193], v[136:139], v[132:135]
	v_mfma_f32_16x16x32_f16 v[128:131], v[198:201], v[136:139], v[128:131]
	v_mfma_f32_16x16x32_f16 v[116:119], v[190:193], v[152:155], v[116:119]
	v_mfma_f32_16x16x32_f16 v[112:115], v[198:201], v[152:155], v[112:115]
	v_mfma_f32_16x16x32_f16 v[100:103], v[190:193], v[160:163], v[100:103]
	v_mfma_f32_16x16x32_f16 v[96:99], v[198:201], v[160:163], v[96:99]
	v_mfma_f32_16x16x32_f16 v[68:71], v[190:193], v[168:171], v[68:71]
	v_mfma_f32_16x16x32_f16 v[64:67], v[198:201], v[168:171], v[64:67]
	v_mfma_f32_16x16x32_f16 v[132:135], v[194:197], v[148:151], v[132:135]
	v_mfma_f32_16x16x32_f16 v[128:131], v[202:205], v[148:151], v[128:131]
	v_mfma_f32_16x16x32_f16 v[116:119], v[194:197], v[156:159], v[116:119]
	v_mfma_f32_16x16x32_f16 v[112:115], v[202:205], v[156:159], v[112:115]
	v_mfma_f32_16x16x32_f16 v[100:103], v[194:197], v[164:167], v[100:103]
	v_mfma_f32_16x16x32_f16 v[96:99], v[202:205], v[164:167], v[96:99]
	v_mfma_f32_16x16x32_f16 v[68:71], v[194:197], v[172:175], v[68:71]
	v_mfma_f32_16x16x32_f16 v[64:67], v[202:205], v[172:175], v[64:67]
	s_setprio 0
	s_mov_b32 m0, s58
	v_lshl_add_u64 v[206:207], v[210:211], 0, s[36:37]
	s_barrier
	ds_read_b128 v[136:139], v232 offset:49152
	ds_read_b128 v[148:151], v232 offset:50176
	ds_read_b128 v[152:155], v232 offset:51200
	ds_read_b128 v[156:159], v232 offset:52224
	ds_read_b128 v[160:163], v232 offset:53248
	ds_read_b128 v[164:167], v232 offset:54272
	ds_read_b128 v[168:171], v232 offset:55296
	ds_read_b128 v[172:175], v232 offset:56320
	global_load_lds_dwordx4 v[206:207], off
	v_lshl_add_u64 v[206:207], v[212:213], 0, s[36:37]
	s_mov_b32 m0, s59
	s_nop 0
	global_load_lds_dwordx4 v[206:207], off
	s_barrier
	s_waitcnt lgkmcnt(0)
	s_setprio 1
	s_waitcnt lgkmcnt(0)
	v_mfma_f32_16x16x32_f16 v[60:63], v[72:75], v[136:139], v[60:63]
	v_mfma_f32_16x16x32_f16 v[56:59], v[88:91], v[136:139], v[56:59]
	v_mfma_f32_16x16x32_f16 v[44:47], v[72:75], v[152:155], v[44:47]
	v_mfma_f32_16x16x32_f16 v[40:43], v[88:91], v[152:155], v[40:43]
	v_mfma_f32_16x16x32_f16 v[28:31], v[72:75], v[160:163], v[28:31]
	v_mfma_f32_16x16x32_f16 v[24:27], v[88:91], v[160:163], v[24:27]
	v_mfma_f32_16x16x32_f16 v[12:15], v[72:75], v[168:171], v[12:15]
	v_mfma_f32_16x16x32_f16 v[8:11], v[88:91], v[168:171], v[8:11]
	v_mfma_f32_16x16x32_f16 v[60:63], v[80:83], v[148:151], v[60:63]
	v_mfma_f32_16x16x32_f16 v[56:59], v[92:95], v[148:151], v[56:59]
	v_mfma_f32_16x16x32_f16 v[44:47], v[80:83], v[156:159], v[44:47]
	v_mfma_f32_16x16x32_f16 v[40:43], v[92:95], v[156:159], v[40:43]
	v_mfma_f32_16x16x32_f16 v[28:31], v[80:83], v[164:167], v[28:31]
	v_mfma_f32_16x16x32_f16 v[24:27], v[92:95], v[164:167], v[24:27]
	v_mfma_f32_16x16x32_f16 v[12:15], v[80:83], v[172:175], v[12:15]
	v_mfma_f32_16x16x32_f16 v[8:11], v[92:95], v[172:175], v[8:11]
	s_setprio 0
	s_barrier
	s_add_u32 s40, s40, 0x30080
	s_addc_u32 s41, s41, 0
	s_add_i32 s42, s42, s50
	v_lshl_add_u64 v[72:73], s[40:41], 0, v[178:179]
	s_mov_b32 m0, s42
	s_nop 0
	global_load_lds_dwordx4 v[72:73], off
	v_lshl_add_u64 v[72:73], s[40:41], 0, v[182:183]
	s_add_i32 m0, s42, 0x2000
	s_nop 0
	global_load_lds_dwordx4 v[72:73], off
	s_waitcnt vmcnt(6)
	s_barrier
	s_setprio 1
	v_mfma_f32_16x16x32_f16 v[52:55], v[190:193], v[136:139], v[52:55]
	v_mfma_f32_16x16x32_f16 v[48:51], v[198:201], v[136:139], v[48:51]
	v_mfma_f32_16x16x32_f16 v[36:39], v[190:193], v[152:155], v[36:39]
	v_mfma_f32_16x16x32_f16 v[32:35], v[198:201], v[152:155], v[32:35]
	v_mfma_f32_16x16x32_f16 v[20:23], v[190:193], v[160:163], v[20:23]
	v_mfma_f32_16x16x32_f16 v[16:19], v[198:201], v[160:163], v[16:19]
	v_mfma_f32_16x16x32_f16 v[4:7], v[190:193], v[168:171], v[4:7]
	v_mfma_f32_16x16x32_f16 v[0:3], v[198:201], v[168:171], v[0:3]
	v_mfma_f32_16x16x32_f16 v[52:55], v[194:197], v[148:151], v[52:55]
	v_mfma_f32_16x16x32_f16 v[48:51], v[202:205], v[148:151], v[48:51]
	v_mfma_f32_16x16x32_f16 v[36:39], v[194:197], v[156:159], v[36:39]
	v_mfma_f32_16x16x32_f16 v[32:35], v[202:205], v[156:159], v[32:35]
	v_mfma_f32_16x16x32_f16 v[20:23], v[194:197], v[164:167], v[20:23]
	v_mfma_f32_16x16x32_f16 v[16:19], v[202:205], v[164:167], v[16:19]
	v_mfma_f32_16x16x32_f16 v[4:7], v[194:197], v[172:175], v[4:7]
	v_mfma_f32_16x16x32_f16 v[0:3], v[202:205], v[172:175], v[0:3]
	s_setprio 0
	s_add_i32 s87, s87, 2
	s_add_u32 s38, s38, 0x100
	s_addc_u32 s39, s39, 0
	s_add_u32 s85, s85, 0x100
	s_addc_u32 s86, s86, 0
	s_cmp_gt_u32 s87, 45
	s_barrier
	s_cbranch_scc0 .LBB10_27
	s_lshl_b32 s92, s84, 8
	s_add_i32 s92, s92, s57
	s_lshl_b32 s93, s83, 8
	s_or_b32 s93, s93, s60
	v_lshlrev_b32_e32 v237, 2, v226
	s_lshl_b32 s96, s93, 2
	s_add_u32 s94, s16, s96
	s_addc_u32 s95, s17, 0
	global_load_dwordx4 v[72:75], v237, s[94:95] offset:0
	global_load_dwordx4 v[80:83], v237, s[94:95] offset:16
	global_load_dwordx4 v[88:91], v237, s[94:95] offset:128
	global_load_dwordx4 v[92:95], v237, s[94:95] offset:144
	s_add_u32 s94, s18, s96
	s_addc_u32 s95, s19, 0
	global_load_dwordx4 v[136:139], v237, s[94:95] offset:0
	global_load_dwordx4 v[148:151], v237, s[94:95] offset:16
	global_load_dwordx4 v[152:155], v237, s[94:95] offset:128
	global_load_dwordx4 v[156:159], v237, s[94:95] offset:144
	s_add_u32 s94, s14, s96
	s_addc_u32 s95, s15, 0
	global_load_dwordx4 v[160:163], v237, s[94:95] offset:0
	global_load_dwordx4 v[164:167], v237, s[94:95] offset:16
	global_load_dwordx4 v[168:171], v237, s[94:95] offset:128
	global_load_dwordx4 v[172:175], v237, s[94:95] offset:144
	v_lshlrev_b32_e32 v190, 3, v227
	s_lshl_b32 s96, s92, 3
	s_add_u32 s94, s12, s96
	s_addc_u32 s95, s13, 0
	global_load_dwordx2 v[238:239], v190, s[94:95] offset:0
	global_load_dwordx2 v[192:193], v190, s[94:95] offset:128
	global_load_dwordx2 v[194:195], v190, s[94:95] offset:256
	global_load_dwordx2 v[196:197], v190, s[94:95] offset:384
	global_load_dwordx2 v[198:199], v190, s[94:95] offset:1024
	global_load_dwordx2 v[200:201], v190, s[94:95] offset:1152
	global_load_dwordx2 v[202:203], v190, s[94:95] offset:1280
	global_load_dwordx2 v[204:205], v190, s[94:95] offset:1408
	v_mul_u32_u24_e32 v191, 0x600, v227
	v_lshl_add_u32 v191, v226, 1, v191
	s_mul_i32 s96, s92, 0x600
	s_lshl_b32 s97, s93, 1
	s_add_u32 s96, s96, s97
	s_add_u32 s98, s10, s96
	s_addc_u32 s99, s11, 0
	s_add_u32 s94, s98, 0x0
	s_addc_u32 s95, s99, 0
	global_load_dwordx4 v[208:211], v191, s[94:95] offset:0 nt
	global_load_dwordx4 v[212:215], v191, s[94:95] offset:64 nt
	s_add_u32 s94, s98, 0x6000
	s_addc_u32 s95, s99, 0
	global_load_dwordx4 v[216:219], v191, s[94:95] offset:0 nt
	global_load_dwordx4 v[220:223], v191, s[94:95] offset:64 nt
	v_add_u32_e32 v225, s92, v229
	v_mul_u32_u24_e32 v225, 0x600, v225
	s_lshl_b32 s97, s93, 1
	v_add3_u32 v225, v225, v230, s97
	v_mul_u32_u24_e32 v224, 0x60, v227
	s_mul_i32 s96, s92, 0x60
	s_lshl_b32 s97, s83, 5
	s_add_u32 s96, s96, s97
	s_lshr_b32 s97, s60, 3
	s_add_u32 s96, s96, s97
	s_add_u32 s96, s96, 0x800
	s_add_u32 s100, s28, s96
	s_addc_u32 s101, s29, 0
	s_waitcnt vmcnt(19)
	v_pk_add_f32 v[72:73], v[72:73], v[136:137]
	v_pk_add_f32 v[74:75], v[74:75], v[138:139]
	s_waitcnt vmcnt(18)
	v_pk_add_f32 v[80:81], v[80:81], v[148:149]
	v_pk_add_f32 v[82:83], v[82:83], v[150:151]
	s_waitcnt vmcnt(17)
	v_pk_add_f32 v[88:89], v[88:89], v[152:153]
	v_pk_add_f32 v[90:91], v[90:91], v[154:155]
	s_waitcnt vmcnt(16)
	v_pk_add_f32 v[92:93], v[92:93], v[156:157]
	v_pk_add_f32 v[94:95], v[94:95], v[158:159]
	v_pk_add_f32 v[144:145], v[144:145], v[72:73]
	v_pk_add_f32 v[146:147], v[146:147], v[74:75]
	v_pk_add_f32 v[124:125], v[124:125], v[72:73]
	v_pk_add_f32 v[126:127], v[126:127], v[74:75]
	v_pk_add_f32 v[108:109], v[108:109], v[72:73]
	v_pk_add_f32 v[110:111], v[110:111], v[74:75]
	v_pk_add_f32 v[84:85], v[84:85], v[72:73]
	v_pk_add_f32 v[86:87], v[86:87], v[74:75]
	v_pk_add_f32 v[60:61], v[60:61], v[72:73]
	v_pk_add_f32 v[62:63], v[62:63], v[74:75]
	v_pk_add_f32 v[44:45], v[44:45], v[72:73]
	v_pk_add_f32 v[46:47], v[46:47], v[74:75]
	v_pk_add_f32 v[28:29], v[28:29], v[72:73]
	v_pk_add_f32 v[30:31], v[30:31], v[74:75]
	v_pk_add_f32 v[12:13], v[12:13], v[72:73]
	v_pk_add_f32 v[14:15], v[14:15], v[74:75]
	v_pk_add_f32 v[140:141], v[140:141], v[80:81]
	v_pk_add_f32 v[142:143], v[142:143], v[82:83]
	v_pk_add_f32 v[120:121], v[120:121], v[80:81]
	v_pk_add_f32 v[122:123], v[122:123], v[82:83]
	v_pk_add_f32 v[104:105], v[104:105], v[80:81]
	v_pk_add_f32 v[106:107], v[106:107], v[82:83]
	v_pk_add_f32 v[76:77], v[76:77], v[80:81]
	v_pk_add_f32 v[78:79], v[78:79], v[82:83]
	v_pk_add_f32 v[56:57], v[56:57], v[80:81]
	v_pk_add_f32 v[58:59], v[58:59], v[82:83]
	v_pk_add_f32 v[40:41], v[40:41], v[80:81]
	v_pk_add_f32 v[42:43], v[42:43], v[82:83]
	v_pk_add_f32 v[24:25], v[24:25], v[80:81]
	v_pk_add_f32 v[26:27], v[26:27], v[82:83]
	v_pk_add_f32 v[8:9], v[8:9], v[80:81]
	v_pk_add_f32 v[10:11], v[10:11], v[82:83]
	v_pk_add_f32 v[132:133], v[132:133], v[88:89]
	v_pk_add_f32 v[134:135], v[134:135], v[90:91]
	v_pk_add_f32 v[116:117], v[116:117], v[88:89]
	v_pk_add_f32 v[118:119], v[118:119], v[90:91]
	v_pk_add_f32 v[100:101], v[100:101], v[88:89]
	v_pk_add_f32 v[102:103], v[102:103], v[90:91]
	v_pk_add_f32 v[68:69], v[68:69], v[88:89]
	v_pk_add_f32 v[70:71], v[70:71], v[90:91]
	v_pk_add_f32 v[52:53], v[52:53], v[88:89]
	v_pk_add_f32 v[54:55], v[54:55], v[90:91]
	v_pk_add_f32 v[36:37], v[36:37], v[88:89]
	v_pk_add_f32 v[38:39], v[38:39], v[90:91]
	v_pk_add_f32 v[20:21], v[20:21], v[88:89]
	v_pk_add_f32 v[22:23], v[22:23], v[90:91]
	v_pk_add_f32 v[4:5], v[4:5], v[88:89]
	v_pk_add_f32 v[6:7], v[6:7], v[90:91]
	v_pk_add_f32 v[128:129], v[128:129], v[92:93]
	v_pk_add_f32 v[130:131], v[130:131], v[94:95]
	v_pk_add_f32 v[112:113], v[112:113], v[92:93]
	v_pk_add_f32 v[114:115], v[114:115], v[94:95]
	v_pk_add_f32 v[96:97], v[96:97], v[92:93]
	v_pk_add_f32 v[98:99], v[98:99], v[94:95]
	v_pk_add_f32 v[64:65], v[64:65], v[92:93]
	v_pk_add_f32 v[66:67], v[66:67], v[94:95]
	v_pk_add_f32 v[48:49], v[48:49], v[92:93]
	v_pk_add_f32 v[50:51], v[50:51], v[94:95]
	v_pk_add_f32 v[32:33], v[32:33], v[92:93]
	v_pk_add_f32 v[34:35], v[34:35], v[94:95]
	v_pk_add_f32 v[16:17], v[16:17], v[92:93]
	v_pk_add_f32 v[18:19], v[18:19], v[94:95]
	v_pk_add_f32 v[0:1], v[0:1], v[92:93]
	v_pk_add_f32 v[2:3], v[2:3], v[94:95]
	s_add_u32 s94, s98, 0xc000
	s_addc_u32 s95, s99, 0
	global_load_dwordx4 v[240:243], v191, s[94:95] offset:0 nt
	global_load_dwordx4 v[244:247], v191, s[94:95] offset:64 nt
	s_add_u32 s94, s98, 0x12000
	s_addc_u32 s95, s99, 0
	global_load_dwordx4 v[248:251], v191, s[94:95] offset:0 nt
	global_load_dwordx4 v[252:255], v191, s[94:95] offset:64 nt
	s_add_u32 s94, s98, 0x30000
	s_addc_u32 s95, s99, 0
	global_load_dwordx4 v[136:139], v191, s[94:95] offset:0 nt
	global_load_dwordx4 v[148:151], v191, s[94:95] offset:64 nt
	s_add_u32 s94, s98, 0x36000
	s_addc_u32 s95, s99, 0
	global_load_dwordx4 v[152:155], v191, s[94:95] offset:0 nt
	global_load_dwordx4 v[156:159], v191, s[94:95] offset:64 nt
	s_waitcnt vmcnt(19)
	s_waitcnt vmcnt(11)
	v_cvt_f32_f16_e32 v72, v208
	v_cvt_f32_f16_sdwa v73, v208 dst_sel:DWORD dst_unused:UNUSED_PAD src0_sel:WORD_1
	v_cvt_f32_f16_e32 v74, v209
	v_cvt_f32_f16_sdwa v75, v209 dst_sel:DWORD dst_unused:UNUSED_PAD src0_sel:WORD_1
	v_cvt_f32_f16_e32 v80, v210
	v_cvt_f32_f16_sdwa v81, v210 dst_sel:DWORD dst_unused:UNUSED_PAD src0_sel:WORD_1
	v_cvt_f32_f16_e32 v82, v211
	v_cvt_f32_f16_sdwa v83, v211 dst_sel:DWORD dst_unused:UNUSED_PAD src0_sel:WORD_1
	v_sub_f32_e32 v72, v72, v238
	v_sub_f32_e32 v73, v73, v238
	v_sub_f32_e32 v74, v74, v238
	v_sub_f32_e32 v75, v75, v238
	v_sub_f32_e32 v80, v80, v238
	v_sub_f32_e32 v81, v81, v238
	v_sub_f32_e32 v82, v82, v238
	v_sub_f32_e32 v83, v83, v238
	v_pk_mul_f32 v[72:73], v[238:239], v[72:73] op_sel:[1,0]
	v_pk_mul_f32 v[74:75], v[238:239], v[74:75] op_sel:[1,0]
	v_pk_mul_f32 v[80:81], v[238:239], v[80:81] op_sel:[1,0]
	v_pk_mul_f32 v[82:83], v[238:239], v[82:83] op_sel:[1,0]
	v_pk_fma_f32 v[144:145], v[72:73], v[160:161], v[144:145]
	v_pk_fma_f32 v[146:147], v[74:75], v[162:163], v[146:147]
	v_pk_fma_f32 v[140:141], v[80:81], v[164:165], v[140:141]
	v_pk_fma_f32 v[142:143], v[82:83], v[166:167], v[142:143]
	v_cvt_pk_f16_f32 v144, v144, v145
	v_cvt_pk_f16_f32 v145, v146, v147
	v_cvt_pk_f16_f32 v146, v140, v141
	v_cvt_pk_f16_f32 v147, v142, v143
	ds_write_b128 v235, v[144:147]
	v_fma_mix_f32 v206, v144, 1.0, 0 op_sel_hi:[1,0,0]
	v_fma_mix_f32 v207, v144, v144, 0 op_sel_hi:[1,1,0]
	v_fma_mix_f32 v206, v144, 1.0, v206 op_sel:[1,0,0] op_sel_hi:[1,0,0]
	v_fma_mix_f32 v207, v144, v144, v207 op_sel:[1,1,0] op_sel_hi:[1,1,0]
	v_fma_mix_f32 v206, v145, 1.0, v206 op_sel_hi:[1,0,0]
	v_fma_mix_f32 v207, v145, v145, v207 op_sel_hi:[1,1,0]
	v_fma_mix_f32 v206, v145, 1.0, v206 op_sel:[1,0,0] op_sel_hi:[1,0,0]
	v_fma_mix_f32 v207, v145, v145, v207 op_sel:[1,1,0] op_sel_hi:[1,1,0]
	v_fma_mix_f32 v206, v146, 1.0, v206 op_sel_hi:[1,0,0]
	v_fma_mix_f32 v207, v146, v146, v207 op_sel_hi:[1,1,0]
	v_fma_mix_f32 v206, v146, 1.0, v206 op_sel:[1,0,0] op_sel_hi:[1,0,0]
	v_fma_mix_f32 v207, v146, v146, v207 op_sel:[1,1,0] op_sel_hi:[1,1,0]
	v_fma_mix_f32 v206, v147, 1.0, v206 op_sel_hi:[1,0,0]
	v_fma_mix_f32 v207, v147, v147, v207 op_sel_hi:[1,1,0]
	v_fma_mix_f32 v206, v147, 1.0, v206 op_sel:[1,0,0] op_sel_hi:[1,0,0]
	v_fma_mix_f32 v207, v147, v147, v207 op_sel:[1,1,0] op_sel_hi:[1,1,0]
	s_waitcnt vmcnt(10)
	v_cvt_f32_f16_e32 v72, v212
	v_cvt_f32_f16_sdwa v73, v212 dst_sel:DWORD dst_unused:UNUSED_PAD src0_sel:WORD_1
	v_cvt_f32_f16_e32 v74, v213
	v_cvt_f32_f16_sdwa v75, v213 dst_sel:DWORD dst_unused:UNUSED_PAD src0_sel:WORD_1
	v_cvt_f32_f16_e32 v80, v214
	v_cvt_f32_f16_sdwa v81, v214 dst_sel:DWORD dst_unused:UNUSED_PAD src0_sel:WORD_1
	v_cvt_f32_f16_e32 v82, v215
	v_cvt_f32_f16_sdwa v83, v215 dst_sel:DWORD dst_unused:UNUSED_PAD src0_sel:WORD_1
	v_sub_f32_e32 v72, v72, v238
	v_sub_f32_e32 v73, v73, v238
	v_sub_f32_e32 v74, v74, v238
	v_sub_f32_e32 v75, v75, v238
	v_sub_f32_e32 v80, v80, v238
	v_sub_f32_e32 v81, v81, v238
	v_sub_f32_e32 v82, v82, v238
	v_sub_f32_e32 v83, v83, v238
	v_pk_mul_f32 v[72:73], v[238:239], v[72:73] op_sel:[1,0]
	v_pk_mul_f32 v[74:75], v[238:239], v[74:75] op_sel:[1,0]
	v_pk_mul_f32 v[80:81], v[238:239], v[80:81] op_sel:[1,0]
	v_pk_mul_f32 v[82:83], v[238:239], v[82:83] op_sel:[1,0]
	v_pk_fma_f32 v[132:133], v[72:73], v[168:169], v[132:133]
	v_pk_fma_f32 v[134:135], v[74:75], v[170:171], v[134:135]
	v_pk_fma_f32 v[128:129], v[80:81], v[172:173], v[128:129]
	v_pk_fma_f32 v[130:131], v[82:83], v[174:175], v[130:131]
	v_cvt_pk_f16_f32 v132, v132, v133
	v_cvt_pk_f16_f32 v133, v134, v135
	v_cvt_pk_f16_f32 v134, v128, v129
	v_cvt_pk_f16_f32 v135, v130, v131
	ds_write_b128 v235, v[132:135] offset:64
	v_fma_mix_f32 v206, v132, 1.0, v206 op_sel_hi:[1,0,0]
	v_fma_mix_f32 v207, v132, v132, v207 op_sel_hi:[1,1,0]
	v_fma_mix_f32 v206, v132, 1.0, v206 op_sel:[1,0,0] op_sel_hi:[1,0,0]
	v_fma_mix_f32 v207, v132, v132, v207 op_sel:[1,1,0] op_sel_hi:[1,1,0]
	v_fma_mix_f32 v206, v133, 1.0, v206 op_sel_hi:[1,0,0]
	v_fma_mix_f32 v207, v133, v133, v207 op_sel_hi:[1,1,0]
	v_fma_mix_f32 v206, v133, 1.0, v206 op_sel:[1,0,0] op_sel_hi:[1,0,0]
	v_fma_mix_f32 v207, v133, v133, v207 op_sel:[1,1,0] op_sel_hi:[1,1,0]
	v_fma_mix_f32 v206, v134, 1.0, v206 op_sel_hi:[1,0,0]
	v_fma_mix_f32 v207, v134, v134, v207 op_sel_hi:[1,1,0]
	v_fma_mix_f32 v206, v134, 1.0, v206 op_sel:[1,0,0] op_sel_hi:[1,0,0]
	v_fma_mix_f32 v207, v134, v134, v207 op_sel:[1,1,0] op_sel_hi:[1,1,0]
	v_fma_mix_f32 v206, v135, 1.0, v206 op_sel_hi:[1,0,0]
	v_fma_mix_f32 v207, v135, v135, v207 op_sel_hi:[1,1,0]
	v_fma_mix_f32 v206, v135, 1.0, v206 op_sel:[1,0,0] op_sel_hi:[1,0,0]
	v_fma_mix_f32 v207, v135, v135, v207 op_sel:[1,1,0] op_sel_hi:[1,1,0]
	ds_read_b128 v[88:91], v236
	ds_read_b128 v[92:95], v236 offset:1152
	s_waitcnt vmcnt(9)
	v_cvt_f32_f16_e32 v72, v216
	v_cvt_f32_f16_sdwa v73, v216 dst_sel:DWORD dst_unused:UNUSED_PAD src0_sel:WORD_1
	v_cvt_f32_f16_e32 v74, v217
	v_cvt_f32_f16_sdwa v75, v217 dst_sel:DWORD dst_unused:UNUSED_PAD src0_sel:WORD_1
	v_cvt_f32_f16_e32 v80, v218
	v_cvt_f32_f16_sdwa v81, v218 dst_sel:DWORD dst_unused:UNUSED_PAD src0_sel:WORD_1
	v_cvt_f32_f16_e32 v82, v219
	v_cvt_f32_f16_sdwa v83, v219 dst_sel:DWORD dst_unused:UNUSED_PAD src0_sel:WORD_1
	v_sub_f32_e32 v72, v72, v192
	v_sub_f32_e32 v73, v73, v192
	v_sub_f32_e32 v74, v74, v192
	v_sub_f32_e32 v75, v75, v192
	v_sub_f32_e32 v80, v80, v192
	v_sub_f32_e32 v81, v81, v192
	v_sub_f32_e32 v82, v82, v192
	v_sub_f32_e32 v83, v83, v192
	v_pk_mul_f32 v[72:73], v[192:193], v[72:73] op_sel:[1,0]
	v_pk_mul_f32 v[74:75], v[192:193], v[74:75] op_sel:[1,0]
	v_pk_mul_f32 v[80:81], v[192:193], v[80:81] op_sel:[1,0]
	v_pk_mul_f32 v[82:83], v[192:193], v[82:83] op_sel:[1,0]
	v_pk_fma_f32 v[124:125], v[72:73], v[160:161], v[124:125]
	v_pk_fma_f32 v[126:127], v[74:75], v[162:163], v[126:127]
	v_pk_fma_f32 v[120:121], v[80:81], v[164:165], v[120:121]
	v_pk_fma_f32 v[122:123], v[82:83], v[166:167], v[122:123]
	v_cvt_pk_f16_f32 v124, v124, v125
	v_cvt_pk_f16_f32 v125, v126, v127
	v_cvt_pk_f16_f32 v126, v120, v121
	v_cvt_pk_f16_f32 v127, v122, v123
	s_waitcnt lgkmcnt(0)
	buffer_store_dwordx4 v[88:91], v225, s[24:27], 0 offen nt
	v_add_u32_e32 v82, 0x3000, v225
	buffer_store_dwordx4 v[92:95], v82, s[24:27], 0 offen nt
	ds_write_b128 v235, v[124:127]
	v_fma_mix_f32 v140, v124, 1.0, 0 op_sel_hi:[1,0,0]
	v_fma_mix_f32 v141, v124, v124, 0 op_sel_hi:[1,1,0]
	v_fma_mix_f32 v140, v124, 1.0, v140 op_sel:[1,0,0] op_sel_hi:[1,0,0]
	v_fma_mix_f32 v141, v124, v124, v141 op_sel:[1,1,0] op_sel_hi:[1,1,0]
	v_fma_mix_f32 v140, v125, 1.0, v140 op_sel_hi:[1,0,0]
	v_fma_mix_f32 v141, v125, v125, v141 op_sel_hi:[1,1,0]
	v_fma_mix_f32 v140, v125, 1.0, v140 op_sel:[1,0,0] op_sel_hi:[1,0,0]
	v_fma_mix_f32 v141, v125, v125, v141 op_sel:[1,1,0] op_sel_hi:[1,1,0]
	v_fma_mix_f32 v140, v126, 1.0, v140 op_sel_hi:[1,0,0]
	v_fma_mix_f32 v141, v126, v126, v141 op_sel_hi:[1,1,0]
	v_fma_mix_f32 v140, v126, 1.0, v140 op_sel:[1,0,0] op_sel_hi:[1,0,0]
	v_fma_mix_f32 v141, v126, v126, v141 op_sel:[1,1,0] op_sel_hi:[1,1,0]
	v_fma_mix_f32 v140, v127, 1.0, v140 op_sel_hi:[1,0,0]
	v_fma_mix_f32 v141, v127, v127, v141 op_sel_hi:[1,1,0]
	v_fma_mix_f32 v140, v127, 1.0, v140 op_sel:[1,0,0] op_sel_hi:[1,0,0]
	v_fma_mix_f32 v141, v127, v127, v141 op_sel:[1,1,0] op_sel_hi:[1,1,0]
	s_waitcnt vmcnt(10)
	v_cvt_f32_f16_e32 v72, v220
	v_cvt_f32_f16_sdwa v73, v220 dst_sel:DWORD dst_unused:UNUSED_PAD src0_sel:WORD_1
	v_cvt_f32_f16_e32 v74, v221
	v_cvt_f32_f16_sdwa v75, v221 dst_sel:DWORD dst_unused:UNUSED_PAD src0_sel:WORD_1
	v_cvt_f32_f16_e32 v80, v222
	v_cvt_f32_f16_sdwa v81, v222 dst_sel:DWORD dst_unused:UNUSED_PAD src0_sel:WORD_1
	v_cvt_f32_f16_e32 v82, v223
	v_cvt_f32_f16_sdwa v83, v223 dst_sel:DWORD dst_unused:UNUSED_PAD src0_sel:WORD_1
	v_sub_f32_e32 v72, v72, v192
	v_sub_f32_e32 v73, v73, v192
	v_sub_f32_e32 v74, v74, v192
	v_sub_f32_e32 v75, v75, v192
	v_sub_f32_e32 v80, v80, v192
	v_sub_f32_e32 v81, v81, v192
	v_sub_f32_e32 v82, v82, v192
	v_sub_f32_e32 v83, v83, v192
	v_pk_mul_f32 v[72:73], v[192:193], v[72:73] op_sel:[1,0]
	v_pk_mul_f32 v[74:75], v[192:193], v[74:75] op_sel:[1,0]
	v_pk_mul_f32 v[80:81], v[192:193], v[80:81] op_sel:[1,0]
	v_pk_mul_f32 v[82:83], v[192:193], v[82:83] op_sel:[1,0]
	v_pk_fma_f32 v[116:117], v[72:73], v[168:169], v[116:117]
	v_pk_fma_f32 v[118:119], v[74:75], v[170:171], v[118:119]
	v_pk_fma_f32 v[112:113], v[80:81], v[172:173], v[112:113]
	v_pk_fma_f32 v[114:115], v[82:83], v[174:175], v[114:115]
	v_cvt_pk_f16_f32 v116, v116, v117
	v_cvt_pk_f16_f32 v117, v118, v119
	v_cvt_pk_f16_f32 v118, v112, v113
	v_cvt_pk_f16_f32 v119, v114, v115
	ds_write_b128 v235, v[116:119] offset:64
	v_fma_mix_f32 v140, v116, 1.0, v140 op_sel_hi:[1,0,0]
	v_fma_mix_f32 v141, v116, v116, v141 op_sel_hi:[1,1,0]
	v_fma_mix_f32 v140, v116, 1.0, v140 op_sel:[1,0,0] op_sel_hi:[1,0,0]
	v_fma_mix_f32 v141, v116, v116, v141 op_sel:[1,1,0] op_sel_hi:[1,1,0]
	v_fma_mix_f32 v140, v117, 1.0, v140 op_sel_hi:[1,0,0]
	v_fma_mix_f32 v141, v117, v117, v141 op_sel_hi:[1,1,0]
	v_fma_mix_f32 v140, v117, 1.0, v140 op_sel:[1,0,0] op_sel_hi:[1,0,0]
	v_fma_mix_f32 v141, v117, v117, v141 op_sel:[1,1,0] op_sel_hi:[1,1,0]
	v_fma_mix_f32 v140, v118, 1.0, v140 op_sel_hi:[1,0,0]
	v_fma_mix_f32 v141, v118, v118, v141 op_sel_hi:[1,1,0]
	v_fma_mix_f32 v140, v118, 1.0, v140 op_sel:[1,0,0] op_sel_hi:[1,0,0]
	v_fma_mix_f32 v141, v118, v118, v141 op_sel:[1,1,0] op_sel_hi:[1,1,0]
	v_fma_mix_f32 v140, v119, 1.0, v140 op_sel_hi:[1,0,0]
	v_fma_mix_f32 v141, v119, v119, v141 op_sel_hi:[1,1,0]
	v_fma_mix_f32 v140, v119, 1.0, v140 op_sel:[1,0,0] op_sel_hi:[1,0,0]
	v_fma_mix_f32 v141, v119, v119, v141 op_sel:[1,1,0] op_sel_hi:[1,1,0]
	ds_read_b128 v[208:211], v236
	ds_read_b128 v[128:131], v236 offset:1152
	s_add_u32 s94, s98, 0x3c000
	s_addc_u32 s95, s99, 0
	global_load_dwordx4 v[212:215], v191, s[94:95] offset:0 nt
	global_load_dwordx4 v[144:147], v191, s[94:95] offset:64 nt
	s_add_u32 s94, s98, 0x42000
	s_addc_u32 s95, s99, 0
	global_load_dwordx4 v[132:135], v191, s[94:95] offset:0 nt
	global_load_dwordx4 v[88:91], v191, s[94:95] offset:64 nt
	s_waitcnt vmcnt(13)
	v_cvt_f32_f16_e32 v72, v240
	v_cvt_f32_f16_sdwa v73, v240 dst_sel:DWORD dst_unused:UNUSED_PAD src0_sel:WORD_1
	v_cvt_f32_f16_e32 v74, v241
	v_cvt_f32_f16_sdwa v75, v241 dst_sel:DWORD dst_unused:UNUSED_PAD src0_sel:WORD_1
	v_cvt_f32_f16_e32 v80, v242
	v_cvt_f32_f16_sdwa v81, v242 dst_sel:DWORD dst_unused:UNUSED_PAD src0_sel:WORD_1
	v_cvt_f32_f16_e32 v82, v243
	v_cvt_f32_f16_sdwa v83, v243 dst_sel:DWORD dst_unused:UNUSED_PAD src0_sel:WORD_1
	v_sub_f32_e32 v72, v72, v194
	v_sub_f32_e32 v73, v73, v194
	v_sub_f32_e32 v74, v74, v194
	v_sub_f32_e32 v75, v75, v194
	v_sub_f32_e32 v80, v80, v194
	v_sub_f32_e32 v81, v81, v194
	v_sub_f32_e32 v82, v82, v194
	v_sub_f32_e32 v83, v83, v194
	v_pk_mul_f32 v[72:73], v[194:195], v[72:73] op_sel:[1,0]
	v_pk_mul_f32 v[74:75], v[194:195], v[74:75] op_sel:[1,0]
	v_pk_mul_f32 v[80:81], v[194:195], v[80:81] op_sel:[1,0]
	v_pk_mul_f32 v[82:83], v[194:195], v[82:83] op_sel:[1,0]
	v_pk_fma_f32 v[108:109], v[72:73], v[160:161], v[108:109]
	v_pk_fma_f32 v[110:111], v[74:75], v[162:163], v[110:111]
	v_pk_fma_f32 v[104:105], v[80:81], v[164:165], v[104:105]
	v_pk_fma_f32 v[106:107], v[82:83], v[166:167], v[106:107]
	v_cvt_pk_f16_f32 v108, v108, v109
	v_cvt_pk_f16_f32 v109, v110, v111
	v_cvt_pk_f16_f32 v110, v104, v105
	v_cvt_pk_f16_f32 v111, v106, v107
	s_waitcnt lgkmcnt(0)
	v_add_u32_e32 v83, 0x6000, v225
	buffer_store_dwordx4 v[208:211], v83, s[24:27], 0 offen nt
	v_add_u32_e32 v82, 0x9000, v225
	buffer_store_dwordx4 v[128:131], v82, s[24:27], 0 offen nt
	ds_write_b128 v235, v[108:111]
	v_fma_mix_f32 v142, v108, 1.0, 0 op_sel_hi:[1,0,0]
	v_fma_mix_f32 v143, v108, v108, 0 op_sel_hi:[1,1,0]
	v_fma_mix_f32 v142, v108, 1.0, v142 op_sel:[1,0,0] op_sel_hi:[1,0,0]
	v_fma_mix_f32 v143, v108, v108, v143 op_sel:[1,1,0] op_sel_hi:[1,1,0]
	v_fma_mix_f32 v142, v109, 1.0, v142 op_sel_hi:[1,0,0]
	v_fma_mix_f32 v143, v109, v109, v143 op_sel_hi:[1,1,0]
	v_fma_mix_f32 v142, v109, 1.0, v142 op_sel:[1,0,0] op_sel_hi:[1,0,0]
	v_fma_mix_f32 v143, v109, v109, v143 op_sel:[1,1,0] op_sel_hi:[1,1,0]
	v_fma_mix_f32 v142, v110, 1.0, v142 op_sel_hi:[1,0,0]
	v_fma_mix_f32 v143, v110, v110, v143 op_sel_hi:[1,1,0]
	v_fma_mix_f32 v142, v110, 1.0, v142 op_sel:[1,0,0] op_sel_hi:[1,0,0]
	v_fma_mix_f32 v143, v110, v110, v143 op_sel:[1,1,0] op_sel_hi:[1,1,0]
	v_fma_mix_f32 v142, v111, 1.0, v142 op_sel_hi:[1,0,0]
	v_fma_mix_f32 v143, v111, v111, v143 op_sel_hi:[1,1,0]
	v_fma_mix_f32 v142, v111, 1.0, v142 op_sel:[1,0,0] op_sel_hi:[1,0,0]
	v_fma_mix_f32 v143, v111, v111, v143 op_sel:[1,1,0] op_sel_hi:[1,1,0]
	s_waitcnt vmcnt(14)
	v_cvt_f32_f16_e32 v72, v244
	v_cvt_f32_f16_sdwa v73, v244 dst_sel:DWORD dst_unused:UNUSED_PAD src0_sel:WORD_1
	v_cvt_f32_f16_e32 v74, v245
	v_cvt_f32_f16_sdwa v75, v245 dst_sel:DWORD dst_unused:UNUSED_PAD src0_sel:WORD_1
	v_cvt_f32_f16_e32 v80, v246
	v_cvt_f32_f16_sdwa v81, v246 dst_sel:DWORD dst_unused:UNUSED_PAD src0_sel:WORD_1
	v_cvt_f32_f16_e32 v82, v247
	v_cvt_f32_f16_sdwa v83, v247 dst_sel:DWORD dst_unused:UNUSED_PAD src0_sel:WORD_1
	v_sub_f32_e32 v72, v72, v194
	v_sub_f32_e32 v73, v73, v194
	v_sub_f32_e32 v74, v74, v194
	v_sub_f32_e32 v75, v75, v194
	v_sub_f32_e32 v80, v80, v194
	v_sub_f32_e32 v81, v81, v194
	v_sub_f32_e32 v82, v82, v194
	v_sub_f32_e32 v83, v83, v194
	v_pk_mul_f32 v[72:73], v[194:195], v[72:73] op_sel:[1,0]
	v_pk_mul_f32 v[74:75], v[194:195], v[74:75] op_sel:[1,0]
	v_pk_mul_f32 v[80:81], v[194:195], v[80:81] op_sel:[1,0]
	v_pk_mul_f32 v[82:83], v[194:195], v[82:83] op_sel:[1,0]
	v_pk_fma_f32 v[100:101], v[72:73], v[168:169], v[100:101]
	v_pk_fma_f32 v[102:103], v[74:75], v[170:171], v[102:103]
	v_pk_fma_f32 v[96:97], v[80:81], v[172:173], v[96:97]
	v_pk_fma_f32 v[98:99], v[82:83], v[174:175], v[98:99]
	v_cvt_pk_f16_f32 v100, v100, v101
	v_cvt_pk_f16_f32 v101, v102, v103
	v_cvt_pk_f16_f32 v102, v96, v97
	v_cvt_pk_f16_f32 v103, v98, v99
	ds_write_b128 v235, v[100:103] offset:64
	v_fma_mix_f32 v142, v100, 1.0, v142 op_sel_hi:[1,0,0]
	v_fma_mix_f32 v143, v100, v100, v143 op_sel_hi:[1,1,0]
	v_fma_mix_f32 v142, v100, 1.0, v142 op_sel:[1,0,0] op_sel_hi:[1,0,0]
	v_fma_mix_f32 v143, v100, v100, v143 op_sel:[1,1,0] op_sel_hi:[1,1,0]
	v_fma_mix_f32 v142, v101, 1.0, v142 op_sel_hi:[1,0,0]
	v_fma_mix_f32 v143, v101, v101, v143 op_sel_hi:[1,1,0]
	v_fma_mix_f32 v142, v101, 1.0, v142 op_sel:[1,0,0] op_sel_hi:[1,0,0]
	v_fma_mix_f32 v143, v101, v101, v143 op_sel:[1,1,0] op_sel_hi:[1,1,0]
	v_fma_mix_f32 v142, v102, 1.0, v142 op_sel_hi:[1,0,0]
	v_fma_mix_f32 v143, v102, v102, v143 op_sel_hi:[1,1,0]
	v_fma_mix_f32 v142, v102, 1.0, v142 op_sel:[1,0,0] op_sel_hi:[1,0,0]
	v_fma_mix_f32 v143, v102, v102, v143 op_sel:[1,1,0] op_sel_hi:[1,1,0]
	v_fma_mix_f32 v142, v103, 1.0, v142 op_sel_hi:[1,0,0]
	v_fma_mix_f32 v143, v103, v103, v143 op_sel_hi:[1,1,0]
	v_fma_mix_f32 v142, v103, 1.0, v142 op_sel:[1,0,0] op_sel_hi:[1,0,0]
	v_fma_mix_f32 v143, v103, v103, v143 op_sel:[1,1,0] op_sel_hi:[1,1,0]
	ds_read_b128 v[92:95], v236
	ds_read_b128 v[120:123], v236 offset:1152
	s_waitcnt vmcnt(13)
	v_cvt_f32_f16_e32 v72, v248
	v_cvt_f32_f16_sdwa v73, v248 dst_sel:DWORD dst_unused:UNUSED_PAD src0_sel:WORD_1
	v_cvt_f32_f16_e32 v74, v249
	v_cvt_f32_f16_sdwa v75, v249 dst_sel:DWORD dst_unused:UNUSED_PAD src0_sel:WORD_1
	v_cvt_f32_f16_e32 v80, v250
	v_cvt_f32_f16_sdwa v81, v250 dst_sel:DWORD dst_unused:UNUSED_PAD src0_sel:WORD_1
	v_cvt_f32_f16_e32 v82, v251
	v_cvt_f32_f16_sdwa v83, v251 dst_sel:DWORD dst_unused:UNUSED_PAD src0_sel:WORD_1
	v_sub_f32_e32 v72, v72, v196
	v_sub_f32_e32 v73, v73, v196
	v_sub_f32_e32 v74, v74, v196
	v_sub_f32_e32 v75, v75, v196
	v_sub_f32_e32 v80, v80, v196
	v_sub_f32_e32 v81, v81, v196
	v_sub_f32_e32 v82, v82, v196
	v_sub_f32_e32 v83, v83, v196
	v_pk_mul_f32 v[72:73], v[196:197], v[72:73] op_sel:[1,0]
	v_pk_mul_f32 v[74:75], v[196:197], v[74:75] op_sel:[1,0]
	v_pk_mul_f32 v[80:81], v[196:197], v[80:81] op_sel:[1,0]
	v_pk_mul_f32 v[82:83], v[196:197], v[82:83] op_sel:[1,0]
	v_pk_fma_f32 v[84:85], v[72:73], v[160:161], v[84:85]
	v_pk_fma_f32 v[86:87], v[74:75], v[162:163], v[86:87]
	v_pk_fma_f32 v[76:77], v[80:81], v[164:165], v[76:77]
	v_pk_fma_f32 v[78:79], v[82:83], v[166:167], v[78:79]
	v_cvt_pk_f16_f32 v84, v84, v85
	v_cvt_pk_f16_f32 v85, v86, v87
	v_cvt_pk_f16_f32 v86, v76, v77
	v_cvt_pk_f16_f32 v87, v78, v79
	s_waitcnt lgkmcnt(0)
	v_add_u32_e32 v83, 0xc000, v225
	buffer_store_dwordx4 v[92:95], v83, s[24:27], 0 offen nt
	v_add_u32_e32 v82, 0xf000, v225
	buffer_store_dwordx4 v[120:123], v82, s[24:27], 0 offen nt
	ds_write_b128 v235, v[84:87]
	v_fma_mix_f32 v216, v84, 1.0, 0 op_sel_hi:[1,0,0]
	v_fma_mix_f32 v217, v84, v84, 0 op_sel_hi:[1,1,0]
	v_fma_mix_f32 v216, v84, 1.0, v216 op_sel:[1,0,0] op_sel_hi:[1,0,0]
	v_fma_mix_f32 v217, v84, v84, v217 op_sel:[1,1,0] op_sel_hi:[1,1,0]
	v_fma_mix_f32 v216, v85, 1.0, v216 op_sel_hi:[1,0,0]
	v_fma_mix_f32 v217, v85, v85, v217 op_sel_hi:[1,1,0]
	v_fma_mix_f32 v216, v85, 1.0, v216 op_sel:[1,0,0] op_sel_hi:[1,0,0]
	v_fma_mix_f32 v217, v85, v85, v217 op_sel:[1,1,0] op_sel_hi:[1,1,0]
	v_fma_mix_f32 v216, v86, 1.0, v216 op_sel_hi:[1,0,0]
	v_fma_mix_f32 v217, v86, v86, v217 op_sel_hi:[1,1,0]
	v_fma_mix_f32 v216, v86, 1.0, v216 op_sel:[1,0,0] op_sel_hi:[1,0,0]
	v_fma_mix_f32 v217, v86, v86, v217 op_sel:[1,1,0] op_sel_hi:[1,1,0]
	v_fma_mix_f32 v216, v87, 1.0, v216 op_sel_hi:[1,0,0]
	v_fma_mix_f32 v217, v87, v87, v217 op_sel_hi:[1,1,0]
	v_fma_mix_f32 v216, v87, 1.0, v216 op_sel:[1,0,0] op_sel_hi:[1,0,0]
	v_fma_mix_f32 v217, v87, v87, v217 op_sel:[1,1,0] op_sel_hi:[1,1,0]
	s_waitcnt vmcnt(14)
	v_cvt_f32_f16_e32 v72, v252
	v_cvt_f32_f16_sdwa v73, v252 dst_sel:DWORD dst_unused:UNUSED_PAD src0_sel:WORD_1
	v_cvt_f32_f16_e32 v74, v253
	v_cvt_f32_f16_sdwa v75, v253 dst_sel:DWORD dst_unused:UNUSED_PAD src0_sel:WORD_1
	v_cvt_f32_f16_e32 v80, v254
	v_cvt_f32_f16_sdwa v81, v254 dst_sel:DWORD dst_unused:UNUSED_PAD src0_sel:WORD_1
	v_cvt_f32_f16_e32 v82, v255
	v_cvt_f32_f16_sdwa v83, v255 dst_sel:DWORD dst_unused:UNUSED_PAD src0_sel:WORD_1
	v_sub_f32_e32 v72, v72, v196
	v_sub_f32_e32 v73, v73, v196
	v_sub_f32_e32 v74, v74, v196
	v_sub_f32_e32 v75, v75, v196
	v_sub_f32_e32 v80, v80, v196
	v_sub_f32_e32 v81, v81, v196
	v_sub_f32_e32 v82, v82, v196
	v_sub_f32_e32 v83, v83, v196
	v_pk_mul_f32 v[72:73], v[196:197], v[72:73] op_sel:[1,0]
	v_pk_mul_f32 v[74:75], v[196:197], v[74:75] op_sel:[1,0]
	v_pk_mul_f32 v[80:81], v[196:197], v[80:81] op_sel:[1,0]
	v_pk_mul_f32 v[82:83], v[196:197], v[82:83] op_sel:[1,0]
	v_pk_fma_f32 v[68:69], v[72:73], v[168:169], v[68:69]
	v_pk_fma_f32 v[70:71], v[74:75], v[170:171], v[70:71]
	v_pk_fma_f32 v[64:65], v[80:81], v[172:173], v[64:65]
	v_pk_fma_f32 v[66:67], v[82:83], v[174:175], v[66:67]
	v_cvt_pk_f16_f32 v68, v68, v69
	v_cvt_pk_f16_f32 v69, v70, v71
	v_cvt_pk_f16_f32 v70, v64, v65
	v_cvt_pk_f16_f32 v71, v66, v67
	ds_write_b128 v235, v[68:71] offset:64
	v_fma_mix_f32 v216, v68, 1.0, v216 op_sel_hi:[1,0,0]
	v_fma_mix_f32 v217, v68, v68, v217 op_sel_hi:[1,1,0]
	v_fma_mix_f32 v216, v68, 1.0, v216 op_sel:[1,0,0] op_sel_hi:[1,0,0]
	v_fma_mix_f32 v217, v68, v68, v217 op_sel:[1,1,0] op_sel_hi:[1,1,0]
	v_fma_mix_f32 v216, v69, 1.0, v216 op_sel_hi:[1,0,0]
	v_fma_mix_f32 v217, v69, v69, v217 op_sel_hi:[1,1,0]
	v_fma_mix_f32 v216, v69, 1.0, v216 op_sel:[1,0,0] op_sel_hi:[1,0,0]
	v_fma_mix_f32 v217, v69, v69, v217 op_sel:[1,1,0] op_sel_hi:[1,1,0]
	v_fma_mix_f32 v216, v70, 1.0, v216 op_sel_hi:[1,0,0]
	v_fma_mix_f32 v217, v70, v70, v217 op_sel_hi:[1,1,0]
	v_fma_mix_f32 v216, v70, 1.0, v216 op_sel:[1,0,0] op_sel_hi:[1,0,0]
	v_fma_mix_f32 v217, v70, v70, v217 op_sel:[1,1,0] op_sel_hi:[1,1,0]
	v_fma_mix_f32 v216, v71, 1.0, v216 op_sel_hi:[1,0,0]
	v_fma_mix_f32 v217, v71, v71, v217 op_sel_hi:[1,1,0]
	v_fma_mix_f32 v216, v71, 1.0, v216 op_sel:[1,0,0] op_sel_hi:[1,0,0]
	v_fma_mix_f32 v217, v71, v71, v217 op_sel:[1,1,0] op_sel_hi:[1,1,0]
	ds_read_b128 v[112:115], v236
	ds_read_b128 v[220:223], v236 offset:1152
	s_waitcnt vmcnt(13)
	v_cvt_f32_f16_e32 v72, v136
	v_cvt_f32_f16_sdwa v73, v136 dst_sel:DWORD dst_unused:UNUSED_PAD src0_sel:WORD_1
	v_cvt_f32_f16_e32 v74, v137
	v_cvt_f32_f16_sdwa v75, v137 dst_sel:DWORD dst_unused:UNUSED_PAD src0_sel:WORD_1
	v_cvt_f32_f16_e32 v80, v138
	v_cvt_f32_f16_sdwa v81, v138 dst_sel:DWORD dst_unused:UNUSED_PAD src0_sel:WORD_1
	v_cvt_f32_f16_e32 v82, v139
	v_cvt_f32_f16_sdwa v83, v139 dst_sel:DWORD dst_unused:UNUSED_PAD src0_sel:WORD_1
	v_sub_f32_e32 v72, v72, v198
	v_sub_f32_e32 v73, v73, v198
	v_sub_f32_e32 v74, v74, v198
	v_sub_f32_e32 v75, v75, v198
	v_sub_f32_e32 v80, v80, v198
	v_sub_f32_e32 v81, v81, v198
	v_sub_f32_e32 v82, v82, v198
	v_sub_f32_e32 v83, v83, v198
	v_pk_mul_f32 v[72:73], v[198:199], v[72:73] op_sel:[1,0]
	v_pk_mul_f32 v[74:75], v[198:199], v[74:75] op_sel:[1,0]
	v_pk_mul_f32 v[80:81], v[198:199], v[80:81] op_sel:[1,0]
	v_pk_mul_f32 v[82:83], v[198:199], v[82:83] op_sel:[1,0]
	v_pk_fma_f32 v[60:61], v[72:73], v[160:161], v[60:61]
	v_pk_fma_f32 v[62:63], v[74:75], v[162:163], v[62:63]
	v_pk_fma_f32 v[56:57], v[80:81], v[164:165], v[56:57]
	v_pk_fma_f32 v[58:59], v[82:83], v[166:167], v[58:59]
	v_cvt_pk_f16_f32 v60, v60, v61
	v_cvt_pk_f16_f32 v61, v62, v63
	v_cvt_pk_f16_f32 v62, v56, v57
	v_cvt_pk_f16_f32 v63, v58, v59
	s_waitcnt lgkmcnt(0)
	v_add_u32_e32 v83, 0x12000, v225
	buffer_store_dwordx4 v[112:115], v83, s[24:27], 0 offen nt
	v_add_u32_e32 v82, 0x15000, v225
	buffer_store_dwordx4 v[220:223], v82, s[24:27], 0 offen nt
	ds_write_b128 v235, v[60:63]
	v_fma_mix_f32 v218, v60, 1.0, 0 op_sel_hi:[1,0,0]
	v_fma_mix_f32 v219, v60, v60, 0 op_sel_hi:[1,1,0]
	v_fma_mix_f32 v218, v60, 1.0, v218 op_sel:[1,0,0] op_sel_hi:[1,0,0]
	v_fma_mix_f32 v219, v60, v60, v219 op_sel:[1,1,0] op_sel_hi:[1,1,0]
	v_fma_mix_f32 v218, v61, 1.0, v218 op_sel_hi:[1,0,0]
	v_fma_mix_f32 v219, v61, v61, v219 op_sel_hi:[1,1,0]
	v_fma_mix_f32 v218, v61, 1.0, v218 op_sel:[1,0,0] op_sel_hi:[1,0,0]
	v_fma_mix_f32 v219, v61, v61, v219 op_sel:[1,1,0] op_sel_hi:[1,1,0]
	v_fma_mix_f32 v218, v62, 1.0, v218 op_sel_hi:[1,0,0]
	v_fma_mix_f32 v219, v62, v62, v219 op_sel_hi:[1,1,0]
	v_fma_mix_f32 v218, v62, 1.0, v218 op_sel:[1,0,0] op_sel_hi:[1,0,0]
	v_fma_mix_f32 v219, v62, v62, v219 op_sel:[1,1,0] op_sel_hi:[1,1,0]
	v_fma_mix_f32 v218, v63, 1.0, v218 op_sel_hi:[1,0,0]
	v_fma_mix_f32 v219, v63, v63, v219 op_sel_hi:[1,1,0]
	v_fma_mix_f32 v218, v63, 1.0, v218 op_sel:[1,0,0] op_sel_hi:[1,0,0]
	v_fma_mix_f32 v219, v63, v63, v219 op_sel:[1,1,0] op_sel_hi:[1,1,0]
	s_waitcnt vmcnt(14)
	v_cvt_f32_f16_e32 v72, v148
	v_cvt_f32_f16_sdwa v73, v148 dst_sel:DWORD dst_unused:UNUSED_PAD src0_sel:WORD_1
	v_cvt_f32_f16_e32 v74, v149
	v_cvt_f32_f16_sdwa v75, v149 dst_sel:DWORD dst_unused:UNUSED_PAD src0_sel:WORD_1
	v_cvt_f32_f16_e32 v80, v150
	v_cvt_f32_f16_sdwa v81, v150 dst_sel:DWORD dst_unused:UNUSED_PAD src0_sel:WORD_1
	v_cvt_f32_f16_e32 v82, v151
	v_cvt_f32_f16_sdwa v83, v151 dst_sel:DWORD dst_unused:UNUSED_PAD src0_sel:WORD_1
	v_sub_f32_e32 v72, v72, v198
	v_sub_f32_e32 v73, v73, v198
	v_sub_f32_e32 v74, v74, v198
	v_sub_f32_e32 v75, v75, v198
	v_sub_f32_e32 v80, v80, v198
	v_sub_f32_e32 v81, v81, v198
	v_sub_f32_e32 v82, v82, v198
	v_sub_f32_e32 v83, v83, v198
	v_pk_mul_f32 v[72:73], v[198:199], v[72:73] op_sel:[1,0]
	v_pk_mul_f32 v[74:75], v[198:199], v[74:75] op_sel:[1,0]
	v_pk_mul_f32 v[80:81], v[198:199], v[80:81] op_sel:[1,0]
	v_pk_mul_f32 v[82:83], v[198:199], v[82:83] op_sel:[1,0]
	v_pk_fma_f32 v[52:53], v[72:73], v[168:169], v[52:53]
	v_pk_fma_f32 v[54:55], v[74:75], v[170:171], v[54:55]
	v_pk_fma_f32 v[48:49], v[80:81], v[172:173], v[48:49]
	v_pk_fma_f32 v[50:51], v[82:83], v[174:175], v[50:51]
	v_cvt_pk_f16_f32 v52, v52, v53
	v_cvt_pk_f16_f32 v53, v54, v55
	v_cvt_pk_f16_f32 v54, v48, v49
	v_cvt_pk_f16_f32 v55, v50, v51
	ds_write_b128 v235, v[52:55] offset:64
	v_fma_mix_f32 v218, v52, 1.0, v218 op_sel_hi:[1,0,0]
	v_fma_mix_f32 v219, v52, v52, v219 op_sel_hi:[1,1,0]
	v_fma_mix_f32 v218, v52, 1.0, v218 op_sel:[1,0,0] op_sel_hi:[1,0,0]
	v_fma_mix_f32 v219, v52, v52, v219 op_sel:[1,1,0] op_sel_hi:[1,1,0]
	v_fma_mix_f32 v218, v53, 1.0, v218 op_sel_hi:[1,0,0]
	v_fma_mix_f32 v219, v53, v53, v219 op_sel_hi:[1,1,0]
	v_fma_mix_f32 v218, v53, 1.0, v218 op_sel:[1,0,0] op_sel_hi:[1,0,0]
	v_fma_mix_f32 v219, v53, v53, v219 op_sel:[1,1,0] op_sel_hi:[1,1,0]
	v_fma_mix_f32 v218, v54, 1.0, v218 op_sel_hi:[1,0,0]
	v_fma_mix_f32 v219, v54, v54, v219 op_sel_hi:[1,1,0]
	v_fma_mix_f32 v218, v54, 1.0, v218 op_sel:[1,0,0] op_sel_hi:[1,0,0]
	v_fma_mix_f32 v219, v54, v54, v219 op_sel:[1,1,0] op_sel_hi:[1,1,0]
	v_fma_mix_f32 v218, v55, 1.0, v218 op_sel_hi:[1,0,0]
	v_fma_mix_f32 v219, v55, v55, v219 op_sel_hi:[1,1,0]
	v_fma_mix_f32 v218, v55, 1.0, v218 op_sel:[1,0,0] op_sel_hi:[1,0,0]
	v_fma_mix_f32 v219, v55, v55, v219 op_sel:[1,1,0] op_sel_hi:[1,1,0]
	ds_read_b128 v[124:127], v236
	ds_read_b128 v[116:119], v236 offset:1152
	s_waitcnt vmcnt(13)
	v_cvt_f32_f16_e32 v72, v152
	v_cvt_f32_f16_sdwa v73, v152 dst_sel:DWORD dst_unused:UNUSED_PAD src0_sel:WORD_1
	v_cvt_f32_f16_e32 v74, v153
	v_cvt_f32_f16_sdwa v75, v153 dst_sel:DWORD dst_unused:UNUSED_PAD src0_sel:WORD_1
	v_cvt_f32_f16_e32 v80, v154
	v_cvt_f32_f16_sdwa v81, v154 dst_sel:DWORD dst_unused:UNUSED_PAD src0_sel:WORD_1
	v_cvt_f32_f16_e32 v82, v155
	v_cvt_f32_f16_sdwa v83, v155 dst_sel:DWORD dst_unused:UNUSED_PAD src0_sel:WORD_1
	v_sub_f32_e32 v72, v72, v200
	v_sub_f32_e32 v73, v73, v200
	v_sub_f32_e32 v74, v74, v200
	v_sub_f32_e32 v75, v75, v200
	v_sub_f32_e32 v80, v80, v200
	v_sub_f32_e32 v81, v81, v200
	v_sub_f32_e32 v82, v82, v200
	v_sub_f32_e32 v83, v83, v200
	v_pk_mul_f32 v[72:73], v[200:201], v[72:73] op_sel:[1,0]
	v_pk_mul_f32 v[74:75], v[200:201], v[74:75] op_sel:[1,0]
	v_pk_mul_f32 v[80:81], v[200:201], v[80:81] op_sel:[1,0]
	v_pk_mul_f32 v[82:83], v[200:201], v[82:83] op_sel:[1,0]
	v_pk_fma_f32 v[44:45], v[72:73], v[160:161], v[44:45]
	v_pk_fma_f32 v[46:47], v[74:75], v[162:163], v[46:47]
	v_pk_fma_f32 v[40:41], v[80:81], v[164:165], v[40:41]
	v_pk_fma_f32 v[42:43], v[82:83], v[166:167], v[42:43]
	v_cvt_pk_f16_f32 v44, v44, v45
	v_cvt_pk_f16_f32 v45, v46, v47
	v_cvt_pk_f16_f32 v46, v40, v41
	v_cvt_pk_f16_f32 v47, v42, v43
	s_waitcnt lgkmcnt(0)
	v_add_u32_e32 v83, 0x30000, v225
	buffer_store_dwordx4 v[124:127], v83, s[24:27], 0 offen nt
	v_add_u32_e32 v82, 0x33000, v225
	buffer_store_dwordx4 v[116:119], v82, s[24:27], 0 offen nt
	ds_write_b128 v235, v[44:47]
	v_fma_mix_f32 v208, v44, 1.0, 0 op_sel_hi:[1,0,0]
	v_fma_mix_f32 v209, v44, v44, 0 op_sel_hi:[1,1,0]
	v_fma_mix_f32 v208, v44, 1.0, v208 op_sel:[1,0,0] op_sel_hi:[1,0,0]
	v_fma_mix_f32 v209, v44, v44, v209 op_sel:[1,1,0] op_sel_hi:[1,1,0]
	v_fma_mix_f32 v208, v45, 1.0, v208 op_sel_hi:[1,0,0]
	v_fma_mix_f32 v209, v45, v45, v209 op_sel_hi:[1,1,0]
	v_fma_mix_f32 v208, v45, 1.0, v208 op_sel:[1,0,0] op_sel_hi:[1,0,0]
	v_fma_mix_f32 v209, v45, v45, v209 op_sel:[1,1,0] op_sel_hi:[1,1,0]
	v_fma_mix_f32 v208, v46, 1.0, v208 op_sel_hi:[1,0,0]
	v_fma_mix_f32 v209, v46, v46, v209 op_sel_hi:[1,1,0]
	v_fma_mix_f32 v208, v46, 1.0, v208 op_sel:[1,0,0] op_sel_hi:[1,0,0]
	v_fma_mix_f32 v209, v46, v46, v209 op_sel:[1,1,0] op_sel_hi:[1,1,0]
	v_fma_mix_f32 v208, v47, 1.0, v208 op_sel_hi:[1,0,0]
	v_fma_mix_f32 v209, v47, v47, v209 op_sel_hi:[1,1,0]
	v_fma_mix_f32 v208, v47, 1.0, v208 op_sel:[1,0,0] op_sel_hi:[1,0,0]
	v_fma_mix_f32 v209, v47, v47, v209 op_sel:[1,1,0] op_sel_hi:[1,1,0]
	s_waitcnt vmcnt(14)
	v_cvt_f32_f16_e32 v72, v156
	v_cvt_f32_f16_sdwa v73, v156 dst_sel:DWORD dst_unused:UNUSED_PAD src0_sel:WORD_1
	v_cvt_f32_f16_e32 v74, v157
	v_cvt_f32_f16_sdwa v75, v157 dst_sel:DWORD dst_unused:UNUSED_PAD src0_sel:WORD_1
	v_cvt_f32_f16_e32 v80, v158
	v_cvt_f32_f16_sdwa v81, v158 dst_sel:DWORD dst_unused:UNUSED_PAD src0_sel:WORD_1
	v_cvt_f32_f16_e32 v82, v159
	v_cvt_f32_f16_sdwa v83, v159 dst_sel:DWORD dst_unused:UNUSED_PAD src0_sel:WORD_1
	v_sub_f32_e32 v72, v72, v200
	v_sub_f32_e32 v73, v73, v200
	v_sub_f32_e32 v74, v74, v200
	v_sub_f32_e32 v75, v75, v200
	v_sub_f32_e32 v80, v80, v200
	v_sub_f32_e32 v81, v81, v200
	v_sub_f32_e32 v82, v82, v200
	v_sub_f32_e32 v83, v83, v200
	v_pk_mul_f32 v[72:73], v[200:201], v[72:73] op_sel:[1,0]
	v_pk_mul_f32 v[74:75], v[200:201], v[74:75] op_sel:[1,0]
	v_pk_mul_f32 v[80:81], v[200:201], v[80:81] op_sel:[1,0]
	v_pk_mul_f32 v[82:83], v[200:201], v[82:83] op_sel:[1,0]
	v_pk_fma_f32 v[36:37], v[72:73], v[168:169], v[36:37]
	v_pk_fma_f32 v[38:39], v[74:75], v[170:171], v[38:39]
	v_pk_fma_f32 v[32:33], v[80:81], v[172:173], v[32:33]
	v_pk_fma_f32 v[34:35], v[82:83], v[174:175], v[34:35]
	v_cvt_pk_f16_f32 v36, v36, v37
	v_cvt_pk_f16_f32 v37, v38, v39
	v_cvt_pk_f16_f32 v38, v32, v33
	v_cvt_pk_f16_f32 v39, v34, v35
	ds_write_b128 v235, v[36:39] offset:64
	v_fma_mix_f32 v208, v36, 1.0, v208 op_sel_hi:[1,0,0]
	v_fma_mix_f32 v209, v36, v36, v209 op_sel_hi:[1,1,0]
	v_fma_mix_f32 v208, v36, 1.0, v208 op_sel:[1,0,0] op_sel_hi:[1,0,0]
	v_fma_mix_f32 v209, v36, v36, v209 op_sel:[1,1,0] op_sel_hi:[1,1,0]
	v_fma_mix_f32 v208, v37, 1.0, v208 op_sel_hi:[1,0,0]
	v_fma_mix_f32 v209, v37, v37, v209 op_sel_hi:[1,1,0]
	v_fma_mix_f32 v208, v37, 1.0, v208 op_sel:[1,0,0] op_sel_hi:[1,0,0]
	v_fma_mix_f32 v209, v37, v37, v209 op_sel:[1,1,0] op_sel_hi:[1,1,0]
	v_fma_mix_f32 v208, v38, 1.0, v208 op_sel_hi:[1,0,0]
	v_fma_mix_f32 v209, v38, v38, v209 op_sel_hi:[1,1,0]
	v_fma_mix_f32 v208, v38, 1.0, v208 op_sel:[1,0,0] op_sel_hi:[1,0,0]
	v_fma_mix_f32 v209, v38, v38, v209 op_sel:[1,1,0] op_sel_hi:[1,1,0]
	v_fma_mix_f32 v208, v39, 1.0, v208 op_sel_hi:[1,0,0]
	v_fma_mix_f32 v209, v39, v39, v209 op_sel_hi:[1,1,0]
	v_fma_mix_f32 v208, v39, 1.0, v208 op_sel:[1,0,0] op_sel_hi:[1,0,0]
	v_fma_mix_f32 v209, v39, v39, v209 op_sel:[1,1,0] op_sel_hi:[1,1,0]
	ds_read_b128 v[128:131], v236
	ds_read_b128 v[104:107], v236 offset:1152
	s_waitcnt vmcnt(11)
	v_cvt_f32_f16_e32 v72, v212
	v_cvt_f32_f16_sdwa v73, v212 dst_sel:DWORD dst_unused:UNUSED_PAD src0_sel:WORD_1
	v_cvt_f32_f16_e32 v74, v213
	v_cvt_f32_f16_sdwa v75, v213 dst_sel:DWORD dst_unused:UNUSED_PAD src0_sel:WORD_1
	v_cvt_f32_f16_e32 v80, v214
	v_cvt_f32_f16_sdwa v81, v214 dst_sel:DWORD dst_unused:UNUSED_PAD src0_sel:WORD_1
	v_cvt_f32_f16_e32 v82, v215
	v_cvt_f32_f16_sdwa v83, v215 dst_sel:DWORD dst_unused:UNUSED_PAD src0_sel:WORD_1
	v_sub_f32_e32 v72, v72, v202
	v_sub_f32_e32 v73, v73, v202
	v_sub_f32_e32 v74, v74, v202
	v_sub_f32_e32 v75, v75, v202
	v_sub_f32_e32 v80, v80, v202
	v_sub_f32_e32 v81, v81, v202
	v_sub_f32_e32 v82, v82, v202
	v_sub_f32_e32 v83, v83, v202
	v_pk_mul_f32 v[72:73], v[202:203], v[72:73] op_sel:[1,0]
	v_pk_mul_f32 v[74:75], v[202:203], v[74:75] op_sel:[1,0]
	v_pk_mul_f32 v[80:81], v[202:203], v[80:81] op_sel:[1,0]
	v_pk_mul_f32 v[82:83], v[202:203], v[82:83] op_sel:[1,0]
	v_pk_fma_f32 v[28:29], v[72:73], v[160:161], v[28:29]
	v_pk_fma_f32 v[30:31], v[74:75], v[162:163], v[30:31]
	v_pk_fma_f32 v[24:25], v[80:81], v[164:165], v[24:25]
	v_pk_fma_f32 v[26:27], v[82:83], v[166:167], v[26:27]
	v_cvt_pk_f16_f32 v28, v28, v29
	v_cvt_pk_f16_f32 v29, v30, v31
	v_cvt_pk_f16_f32 v30, v24, v25
	v_cvt_pk_f16_f32 v31, v26, v27
	s_waitcnt lgkmcnt(0)
	v_add_u32_e32 v83, 0x36000, v225
	buffer_store_dwordx4 v[128:131], v83, s[24:27], 0 offen nt
	v_add_u32_e32 v82, 0x39000, v225
	buffer_store_dwordx4 v[104:107], v82, s[24:27], 0 offen nt
	ds_write_b128 v235, v[28:31]
	v_fma_mix_f32 v210, v28, 1.0, 0 op_sel_hi:[1,0,0]
	v_fma_mix_f32 v211, v28, v28, 0 op_sel_hi:[1,1,0]
	v_fma_mix_f32 v210, v28, 1.0, v210 op_sel:[1,0,0] op_sel_hi:[1,0,0]
	v_fma_mix_f32 v211, v28, v28, v211 op_sel:[1,1,0] op_sel_hi:[1,1,0]
	v_fma_mix_f32 v210, v29, 1.0, v210 op_sel_hi:[1,0,0]
	v_fma_mix_f32 v211, v29, v29, v211 op_sel_hi:[1,1,0]
	v_fma_mix_f32 v210, v29, 1.0, v210 op_sel:[1,0,0] op_sel_hi:[1,0,0]
	v_fma_mix_f32 v211, v29, v29, v211 op_sel:[1,1,0] op_sel_hi:[1,1,0]
	v_fma_mix_f32 v210, v30, 1.0, v210 op_sel_hi:[1,0,0]
	v_fma_mix_f32 v211, v30, v30, v211 op_sel_hi:[1,1,0]
	v_fma_mix_f32 v210, v30, 1.0, v210 op_sel:[1,0,0] op_sel_hi:[1,0,0]
	v_fma_mix_f32 v211, v30, v30, v211 op_sel:[1,1,0] op_sel_hi:[1,1,0]
	v_fma_mix_f32 v210, v31, 1.0, v210 op_sel_hi:[1,0,0]
	v_fma_mix_f32 v211, v31, v31, v211 op_sel_hi:[1,1,0]
	v_fma_mix_f32 v210, v31, 1.0, v210 op_sel:[1,0,0] op_sel_hi:[1,0,0]
	v_fma_mix_f32 v211, v31, v31, v211 op_sel:[1,1,0] op_sel_hi:[1,1,0]
	s_waitcnt vmcnt(12)
	v_cvt_f32_f16_e32 v72, v144
	v_cvt_f32_f16_sdwa v73, v144 dst_sel:DWORD dst_unused:UNUSED_PAD src0_sel:WORD_1
	v_cvt_f32_f16_e32 v74, v145
	v_cvt_f32_f16_sdwa v75, v145 dst_sel:DWORD dst_unused:UNUSED_PAD src0_sel:WORD_1
	v_cvt_f32_f16_e32 v80, v146
	v_cvt_f32_f16_sdwa v81, v146 dst_sel:DWORD dst_unused:UNUSED_PAD src0_sel:WORD_1
	v_cvt_f32_f16_e32 v82, v147
	v_cvt_f32_f16_sdwa v83, v147 dst_sel:DWORD dst_unused:UNUSED_PAD src0_sel:WORD_1
	v_sub_f32_e32 v72, v72, v202
	v_sub_f32_e32 v73, v73, v202
	v_sub_f32_e32 v74, v74, v202
	v_sub_f32_e32 v75, v75, v202
	v_sub_f32_e32 v80, v80, v202
	v_sub_f32_e32 v81, v81, v202
	v_sub_f32_e32 v82, v82, v202
	v_sub_f32_e32 v83, v83, v202
	v_pk_mul_f32 v[72:73], v[202:203], v[72:73] op_sel:[1,0]
	v_pk_mul_f32 v[74:75], v[202:203], v[74:75] op_sel:[1,0]
	v_pk_mul_f32 v[80:81], v[202:203], v[80:81] op_sel:[1,0]
	v_pk_mul_f32 v[82:83], v[202:203], v[82:83] op_sel:[1,0]
	v_pk_fma_f32 v[20:21], v[72:73], v[168:169], v[20:21]
	v_pk_fma_f32 v[22:23], v[74:75], v[170:171], v[22:23]
	v_pk_fma_f32 v[16:17], v[80:81], v[172:173], v[16:17]
	v_pk_fma_f32 v[18:19], v[82:83], v[174:175], v[18:19]
	v_cvt_pk_f16_f32 v20, v20, v21
	v_cvt_pk_f16_f32 v21, v22, v23
	v_cvt_pk_f16_f32 v22, v16, v17
	v_cvt_pk_f16_f32 v23, v18, v19
	ds_write_b128 v235, v[20:23] offset:64
	v_fma_mix_f32 v210, v20, 1.0, v210 op_sel_hi:[1,0,0]
	v_fma_mix_f32 v211, v20, v20, v211 op_sel_hi:[1,1,0]
	v_fma_mix_f32 v210, v20, 1.0, v210 op_sel:[1,0,0] op_sel_hi:[1,0,0]
	v_fma_mix_f32 v211, v20, v20, v211 op_sel:[1,1,0] op_sel_hi:[1,1,0]
	v_fma_mix_f32 v210, v21, 1.0, v210 op_sel_hi:[1,0,0]
	v_fma_mix_f32 v211, v21, v21, v211 op_sel_hi:[1,1,0]
	v_fma_mix_f32 v210, v21, 1.0, v210 op_sel:[1,0,0] op_sel_hi:[1,0,0]
	v_fma_mix_f32 v211, v21, v21, v211 op_sel:[1,1,0] op_sel_hi:[1,1,0]
	v_fma_mix_f32 v210, v22, 1.0, v210 op_sel_hi:[1,0,0]
	v_fma_mix_f32 v211, v22, v22, v211 op_sel_hi:[1,1,0]
	v_fma_mix_f32 v210, v22, 1.0, v210 op_sel:[1,0,0] op_sel_hi:[1,0,0]
	v_fma_mix_f32 v211, v22, v22, v211 op_sel:[1,1,0] op_sel_hi:[1,1,0]
	v_fma_mix_f32 v210, v23, 1.0, v210 op_sel_hi:[1,0,0]
	v_fma_mix_f32 v211, v23, v23, v211 op_sel_hi:[1,1,0]
	v_fma_mix_f32 v210, v23, 1.0, v210 op_sel:[1,0,0] op_sel_hi:[1,0,0]
	v_fma_mix_f32 v211, v23, v23, v211 op_sel:[1,1,0] op_sel_hi:[1,1,0]
	ds_read_b128 v[240:243], v236
	ds_read_b128 v[96:99], v236 offset:1152
	s_waitcnt vmcnt(11)
	v_cvt_f32_f16_e32 v72, v132
	v_cvt_f32_f16_sdwa v73, v132 dst_sel:DWORD dst_unused:UNUSED_PAD src0_sel:WORD_1
	v_cvt_f32_f16_e32 v74, v133
	v_cvt_f32_f16_sdwa v75, v133 dst_sel:DWORD dst_unused:UNUSED_PAD src0_sel:WORD_1
	v_cvt_f32_f16_e32 v80, v134
	v_cvt_f32_f16_sdwa v81, v134 dst_sel:DWORD dst_unused:UNUSED_PAD src0_sel:WORD_1
	v_cvt_f32_f16_e32 v82, v135
	v_cvt_f32_f16_sdwa v83, v135 dst_sel:DWORD dst_unused:UNUSED_PAD src0_sel:WORD_1
	v_sub_f32_e32 v72, v72, v204
	v_sub_f32_e32 v73, v73, v204
	v_sub_f32_e32 v74, v74, v204
	v_sub_f32_e32 v75, v75, v204
	v_sub_f32_e32 v80, v80, v204
	v_sub_f32_e32 v81, v81, v204
	v_sub_f32_e32 v82, v82, v204
	v_sub_f32_e32 v83, v83, v204
	v_pk_mul_f32 v[72:73], v[204:205], v[72:73] op_sel:[1,0]
	v_pk_mul_f32 v[74:75], v[204:205], v[74:75] op_sel:[1,0]
	v_pk_mul_f32 v[80:81], v[204:205], v[80:81] op_sel:[1,0]
	v_pk_mul_f32 v[82:83], v[204:205], v[82:83] op_sel:[1,0]
	v_pk_fma_f32 v[12:13], v[72:73], v[160:161], v[12:13]
	v_pk_fma_f32 v[14:15], v[74:75], v[162:163], v[14:15]
	v_pk_fma_f32 v[8:9], v[80:81], v[164:165], v[8:9]
	v_pk_fma_f32 v[10:11], v[82:83], v[166:167], v[10:11]
	v_cvt_pk_f16_f32 v12, v12, v13
	v_cvt_pk_f16_f32 v13, v14, v15
	v_cvt_pk_f16_f32 v14, v8, v9
	v_cvt_pk_f16_f32 v15, v10, v11
	s_waitcnt lgkmcnt(0)
	v_add_u32_e32 v83, 0x3c000, v225
	buffer_store_dwordx4 v[240:243], v83, s[24:27], 0 offen nt
	v_add_u32_e32 v82, 0x3f000, v225
	buffer_store_dwordx4 v[96:99], v82, s[24:27], 0 offen nt
	ds_write_b128 v235, v[12:15]
	v_fma_mix_f32 v244, v12, 1.0, 0 op_sel_hi:[1,0,0]
	v_fma_mix_f32 v245, v12, v12, 0 op_sel_hi:[1,1,0]
	v_fma_mix_f32 v244, v12, 1.0, v244 op_sel:[1,0,0] op_sel_hi:[1,0,0]
	v_fma_mix_f32 v245, v12, v12, v245 op_sel:[1,1,0] op_sel_hi:[1,1,0]
	v_fma_mix_f32 v244, v13, 1.0, v244 op_sel_hi:[1,0,0]
	v_fma_mix_f32 v245, v13, v13, v245 op_sel_hi:[1,1,0]
	v_fma_mix_f32 v244, v13, 1.0, v244 op_sel:[1,0,0] op_sel_hi:[1,0,0]
	v_fma_mix_f32 v245, v13, v13, v245 op_sel:[1,1,0] op_sel_hi:[1,1,0]
	v_fma_mix_f32 v244, v14, 1.0, v244 op_sel_hi:[1,0,0]
	v_fma_mix_f32 v245, v14, v14, v245 op_sel_hi:[1,1,0]
	v_fma_mix_f32 v244, v14, 1.0, v244 op_sel:[1,0,0] op_sel_hi:[1,0,0]
	v_fma_mix_f32 v245, v14, v14, v245 op_sel:[1,1,0] op_sel_hi:[1,1,0]
	v_fma_mix_f32 v244, v15, 1.0, v244 op_sel_hi:[1,0,0]
	v_fma_mix_f32 v245, v15, v15, v245 op_sel_hi:[1,1,0]
	v_fma_mix_f32 v244, v15, 1.0, v244 op_sel:[1,0,0] op_sel_hi:[1,0,0]
	v_fma_mix_f32 v245, v15, v15, v245 op_sel:[1,1,0] op_sel_hi:[1,1,0]
	s_waitcnt vmcnt(12)
	v_cvt_f32_f16_e32 v72, v88
	v_cvt_f32_f16_sdwa v73, v88 dst_sel:DWORD dst_unused:UNUSED_PAD src0_sel:WORD_1
	v_cvt_f32_f16_e32 v74, v89
	v_cvt_f32_f16_sdwa v75, v89 dst_sel:DWORD dst_unused:UNUSED_PAD src0_sel:WORD_1
	v_cvt_f32_f16_e32 v80, v90
	v_cvt_f32_f16_sdwa v81, v90 dst_sel:DWORD dst_unused:UNUSED_PAD src0_sel:WORD_1
	v_cvt_f32_f16_e32 v82, v91
	v_cvt_f32_f16_sdwa v83, v91 dst_sel:DWORD dst_unused:UNUSED_PAD src0_sel:WORD_1
	v_sub_f32_e32 v72, v72, v204
	v_sub_f32_e32 v73, v73, v204
	v_sub_f32_e32 v74, v74, v204
	v_sub_f32_e32 v75, v75, v204
	v_sub_f32_e32 v80, v80, v204
	v_sub_f32_e32 v81, v81, v204
	v_sub_f32_e32 v82, v82, v204
	v_sub_f32_e32 v83, v83, v204
	v_pk_mul_f32 v[72:73], v[204:205], v[72:73] op_sel:[1,0]
	v_pk_mul_f32 v[74:75], v[204:205], v[74:75] op_sel:[1,0]
	v_pk_mul_f32 v[80:81], v[204:205], v[80:81] op_sel:[1,0]
	v_pk_mul_f32 v[82:83], v[204:205], v[82:83] op_sel:[1,0]
	v_pk_fma_f32 v[4:5], v[72:73], v[168:169], v[4:5]
	v_pk_fma_f32 v[6:7], v[74:75], v[170:171], v[6:7]
	v_pk_fma_f32 v[0:1], v[80:81], v[172:173], v[0:1]
	v_pk_fma_f32 v[2:3], v[82:83], v[174:175], v[2:3]
	v_cvt_pk_f16_f32 v4, v4, v5
	v_cvt_pk_f16_f32 v5, v6, v7
	v_cvt_pk_f16_f32 v6, v0, v1
	v_cvt_pk_f16_f32 v7, v2, v3
	ds_write_b128 v235, v[4:7] offset:64
	v_fma_mix_f32 v244, v4, 1.0, v244 op_sel_hi:[1,0,0]
	v_fma_mix_f32 v245, v4, v4, v245 op_sel_hi:[1,1,0]
	v_fma_mix_f32 v244, v4, 1.0, v244 op_sel:[1,0,0] op_sel_hi:[1,0,0]
	v_fma_mix_f32 v245, v4, v4, v245 op_sel:[1,1,0] op_sel_hi:[1,1,0]
	v_fma_mix_f32 v244, v5, 1.0, v244 op_sel_hi:[1,0,0]
	v_fma_mix_f32 v245, v5, v5, v245 op_sel_hi:[1,1,0]
	v_fma_mix_f32 v244, v5, 1.0, v244 op_sel:[1,0,0] op_sel_hi:[1,0,0]
	v_fma_mix_f32 v245, v5, v5, v245 op_sel:[1,1,0] op_sel_hi:[1,1,0]
	v_fma_mix_f32 v244, v6, 1.0, v244 op_sel_hi:[1,0,0]
	v_fma_mix_f32 v245, v6, v6, v245 op_sel_hi:[1,1,0]
	v_fma_mix_f32 v244, v6, 1.0, v244 op_sel:[1,0,0] op_sel_hi:[1,0,0]
	v_fma_mix_f32 v245, v6, v6, v245 op_sel:[1,1,0] op_sel_hi:[1,1,0]
	v_fma_mix_f32 v244, v7, 1.0, v244 op_sel_hi:[1,0,0]
	v_fma_mix_f32 v245, v7, v7, v245 op_sel_hi:[1,1,0]
	v_fma_mix_f32 v244, v7, 1.0, v244 op_sel:[1,0,0] op_sel_hi:[1,0,0]
	v_fma_mix_f32 v245, v7, v7, v245 op_sel:[1,1,0] op_sel_hi:[1,1,0]
	ds_read_b128 v[108:111], v236
	ds_read_b128 v[100:103], v236 offset:1152
	s_waitcnt lgkmcnt(0)
	v_add_u32_e32 v83, 0x42000, v225
	buffer_store_dwordx4 v[108:111], v83, s[24:27], 0 offen nt
	v_add_u32_e32 v82, 0x45000, v225
	buffer_store_dwordx4 v[100:103], v82, s[24:27], 0 offen nt
	v_xor_b32_e32 v246, 16, v234
	v_lshlrev_b32_e32 v246, 2, v246
	v_xor_b32_e32 v247, 32, v234
	v_lshlrev_b32_e32 v247, 2, v247
	ds_bpermute_b32 v92, v246, v206
	ds_bpermute_b32 v93, v246, v207
	ds_bpermute_b32 v94, v246, v140
	ds_bpermute_b32 v95, v246, v141
	ds_bpermute_b32 v120, v246, v142
	ds_bpermute_b32 v121, v246, v143
	ds_bpermute_b32 v122, v246, v216
	ds_bpermute_b32 v123, v246, v217
	s_waitcnt lgkmcnt(0)
	v_pk_add_f32 v[206:207], v[206:207], v[92:93]
	v_pk_add_f32 v[140:141], v[140:141], v[94:95]
	v_pk_add_f32 v[142:143], v[142:143], v[120:121]
	v_pk_add_f32 v[216:217], v[216:217], v[122:123]
	ds_bpermute_b32 v92, v246, v218
	ds_bpermute_b32 v93, v246, v219
	ds_bpermute_b32 v94, v246, v208
	ds_bpermute_b32 v95, v246, v209
	ds_bpermute_b32 v120, v246, v210
	ds_bpermute_b32 v121, v246, v211
	ds_bpermute_b32 v122, v246, v244
	ds_bpermute_b32 v123, v246, v245
	s_waitcnt lgkmcnt(0)
	v_pk_add_f32 v[218:219], v[218:219], v[92:93]
	v_pk_add_f32 v[208:209], v[208:209], v[94:95]
	v_pk_add_f32 v[210:211], v[210:211], v[120:121]
	v_pk_add_f32 v[244:245], v[244:245], v[122:123]
	ds_bpermute_b32 v92, v247, v206
	ds_bpermute_b32 v93, v247, v207
	ds_bpermute_b32 v94, v247, v140
	ds_bpermute_b32 v95, v247, v141
	ds_bpermute_b32 v120, v247, v142
	ds_bpermute_b32 v121, v247, v143
	ds_bpermute_b32 v122, v247, v216
	ds_bpermute_b32 v123, v247, v217
	s_waitcnt lgkmcnt(0)
	v_pk_add_f32 v[206:207], v[206:207], v[92:93]
	v_pk_add_f32 v[140:141], v[140:141], v[94:95]
	v_pk_add_f32 v[142:143], v[142:143], v[120:121]
	v_pk_add_f32 v[216:217], v[216:217], v[122:123]
	ds_bpermute_b32 v92, v247, v218
	ds_bpermute_b32 v93, v247, v219
	ds_bpermute_b32 v94, v247, v208
	ds_bpermute_b32 v95, v247, v209
	ds_bpermute_b32 v120, v247, v210
	ds_bpermute_b32 v121, v247, v211
	ds_bpermute_b32 v122, v247, v244
	ds_bpermute_b32 v123, v247, v245
	s_waitcnt lgkmcnt(0)
	v_pk_add_f32 v[218:219], v[218:219], v[92:93]
	v_pk_add_f32 v[208:209], v[208:209], v[94:95]
	v_pk_add_f32 v[210:211], v[210:211], v[120:121]
	v_pk_add_f32 v[244:245], v[244:245], v[122:123]
	s_mov_b64 exec, 0xffff
	global_store_dwordx2 v224, v[206:207], s[100:101] offset:-2048
	global_store_dwordx2 v224, v[140:141], s[100:101] offset:-512
	global_store_dwordx2 v224, v[142:143], s[100:101] offset:1024
	global_store_dwordx2 v224, v[216:217], s[100:101] offset:2560
	s_add_u32 s100, s100, 0x3000
	s_addc_u32 s101, s101, 0
	global_store_dwordx2 v224, v[218:219], s[100:101] offset:-2048
	global_store_dwordx2 v224, v[208:209], s[100:101] offset:-512
	global_store_dwordx2 v224, v[210:211], s[100:101] offset:1024
	global_store_dwordx2 v224, v[244:245], s[100:101] offset:2560
	s_mov_b64 exec, -1
	s_mov_b32 s83, s81
	s_mov_b32 s84, s82
	s_mov_b64 s[40:41], s[0:1]
	s_mov_b64 s[38:39], s[8:9]
	s_mov_b64 vcc, s[6:7]
	s_cbranch_vccz .LBB10_12
	s_waitcnt vmcnt(0)
	s_cmpk_gt_u32 s44, 0xff
	s_cbranch_scc1 .LBB10_31
	s_barrier

.LBB10_32:
	s_endpgm
	s_endpgm
	s_endpgm
	s_endpgm
	s_endpgm
	s_endpgm
	s_endpgm
	s_endpgm
	s_endpgm
	s_endpgm
	s_endpgm
	s_endpgm
	s_endpgm
	s_endpgm
	s_endpgm
	s_endpgm
	s_endpgm
	s_endpgm
	s_endpgm
	s_endpgm
	s_endpgm
	s_endpgm
	s_endpgm
	s_endpgm
	s_endpgm
	s_endpgm
	s_endpgm
	s_endpgm
	s_endpgm
	s_endpgm
	s_endpgm
	s_endpgm
	s_endpgm
	s_endpgm
	s_endpgm
	s_endpgm
	s_endpgm
	s_endpgm
	s_endpgm
	s_endpgm
	s_endpgm
	s_endpgm
	s_endpgm
	.section	.rodata,"a",@progbits
	.p2align	6, 0x0
